# nt (streaming) hint on the once-read f32 weight/x/p loads of the prologue and of the filler conversions
# speedup vs baseline: 1.0295x; 1.0071x over previous
; #define GAS __attribute__((address_space(1)))
; __device__ __forceinline__ unsigned pk2(float lo, float hi) { return f2bf(lo) | (f2bf(hi) << 16); }
; template <int MODE, int KL>
; __device__ __forceinline__ void p0_cvt_item(const float* W, int K, int N, unsigned char* WT, int il, int which, int item, int lane, const float* gk, float scale, int ldk, int koff) {
;     const int nblk = N >> 6, kb = item / nblk, nb = item - kb * nblk, nq = lane & 15, kr = lane >> 4, k0 = 4 * KL * kb + KL * kr, n0 = 64 * nb + 4 * nq;
;     const GAS f32x4* src = (const GAS f32x4*)(W + (size_t)k0 * N + n0);
;     f32x4 v[KL];
; #pragma unroll
;     for (int i = 0; i < KL; ++i) v[i] = src[(size_t)i * (N >> 2)];
;     if (MODE == 1) {
; #pragma unroll
;         for (int q = 0; q < KL / 4; ++q) { const f32x4 g = *(const GAS f32x4*)(gk + k0 + 4 * q); v[4 * q] *= g.x; v[4 * q + 1] *= g.y; v[4 * q + 2] *= g.z; v[4 * q + 3] *= g.w; } }
;     if (MODE == 2) {
; #pragma unroll
;         for (int i = 0; i < KL; ++i) v[i] *= scale; }
; #pragma unroll
;     for (int c = 0; c < 4; ++c) { const int n = n0 + c, row = il ? ((n >> 4) * 32 + which * 16 + (n & 15)) : n;
;         if (MODE == 2) { GAS v4u* dst = (GAS v4u*)(WT + (size_t)row * ldk + koff + k0);
; #pragma unroll
;             for (int q = 0; q < KL / 16; ++q) { v4u o;
;                 o.x = pg8::pk4_fp8(v[16 * q][c], v[16 * q + 1][c], v[16 * q + 2][c], v[16 * q + 3][c]);     o.y = pg8::pk4_fp8(v[16 * q + 4][c], v[16 * q + 5][c], v[16 * q + 6][c], v[16 * q + 7][c]);
;                 o.z = pg8::pk4_fp8(v[16 * q + 8][c], v[16 * q + 9][c], v[16 * q + 10][c], v[16 * q + 11][c]); o.w = pg8::pk4_fp8(v[16 * q + 12][c], v[16 * q + 13][c], v[16 * q + 14][c], v[16 * q + 15][c]);
;                 dst[q] = o; } }
;         else { GAS v4u* dst = (GAS v4u*)(WT + ((size_t)row * ldk + koff + k0) * 2);
; #pragma unroll
;             for (int q = 0; q < KL / 8; ++q) { v4u o;
;                 if (MODE == 1) { o.x = pg8::pk_f16(v[8 * q][c], v[8 * q + 1][c]); o.y = pg8::pk_f16(v[8 * q + 2][c], v[8 * q + 3][c]); o.z = pg8::pk_f16(v[8 * q + 4][c], v[8 * q + 5][c]); o.w = pg8::pk_f16(v[8 * q + 6][c], v[8 * q + 7][c]); }
;                 else { o.x = pk2(v[8 * q][c], v[8 * q + 1][c]); o.y = pk2(v[8 * q + 2][c], v[8 * q + 3][c]); o.z = pk2(v[8 * q + 4][c], v[8 * q + 5][c]); o.w = pk2(v[8 * q + 6][c], v[8 * q + 7][c]); }
;                 dst[q] = o; } } }
.LBB0_42:
	s_lshr_b32 s83, s2, 6
	v_cvt_f32_i32_e32 v2, s83
	v_cvt_f32_i32_e32 v3, s82
	s_ashr_i32 s18, s82, 30
	s_or_b32 s84, s18, 1
	v_rcp_iflag_f32_e32 v4, v2
	s_mov_b32 s87, s3
	v_mul_f32_e32 v4, v3, v4
	v_trunc_f32_e32 v4, v4
	v_fma_f32 v3, -v4, v2, v3
	v_cvt_i32_f32_e32 v4, v4
	v_cmp_ge_f32_e64 s[18:19], |v3|, v2
	s_and_b64 s[18:19], s[18:19], exec
	s_cselect_b32 s19, s84, 0
	v_readfirstlane_b32 s85, v4
	s_add_i32 s85, s85, s19
	s_sext_i32_i16 s19, s85
	s_mul_i32 s83, s83, s19
	s_sub_i32 s83, s82, s83
	v_lshl_or_b32 v2, s19, 6, v111
	v_lshl_or_b32 v68, s83, 6, v119
	v_mul_hi_i32_i24_e32 v5, s2, v2
	v_mul_i32_i24_e32 v4, s2, v2
	v_lshl_add_u64 v[4:5], v[4:5], 2, s[0:1]
	v_ashrrev_i32_e32 v69, 31, v68
	s_lshr_b32 s18, s2, 2
	v_lshl_add_u64 v[6:7], v[68:69], 2, v[4:5]
	s_lshr_b32 s84, s2, 1
	s_add_i32 s82, s18, s2
	s_lshl_b32 s86, s2, 1
	v_lshl_add_u64 v[14:15], s[2:3], 4, v[6:7]
	s_mul_i32 s2, s18, 6
	v_lshl_add_u64 v[18:19], s[2:3], 4, v[6:7]
	s_mul_i32 s2, s18, 7
	v_lshl_add_u64 v[20:21], s[2:3], 4, v[6:7]
	s_mul_i32 s2, s18, 9
	v_lshl_add_u64 v[24:25], s[2:3], 4, v[6:7]
	s_mul_i32 s2, s18, 10
	v_lshl_add_u64 v[70:71], s[2:3], 4, v[6:7]
	s_mul_i32 s2, s18, 11
	v_lshl_add_u64 v[74:75], s[2:3], 4, v[6:7]
	s_mul_i32 s2, s18, 12
	v_lshl_add_u64 v[76:77], s[2:3], 4, v[6:7]
	s_mul_i32 s2, s18, 13
	v_lshl_add_u64 v[78:79], s[2:3], 4, v[6:7]
	s_mul_i32 s2, s18, 14
	v_ashrrev_i32_e32 v3, 31, v2
	s_mov_b32 s19, s3
	s_mov_b32 s85, s3
	s_mul_i32 s0, s18, 3
	s_mov_b32 s1, s3
	s_mov_b32 s83, s3
	v_lshl_add_u64 v[80:81], s[2:3], 4, v[6:7]
	s_mul_i32 s2, s18, 15
	v_lshlrev_b32_e32 v4, 1, v68
	s_cmp_eq_u64 s[14:15], 0
	v_lshl_add_u64 v[8:9], s[18:19], 4, v[6:7]
	v_lshl_add_u64 v[10:11], s[84:85], 4, v[6:7]
	v_lshl_add_u64 v[12:13], s[0:1], 4, v[6:7]
	v_lshl_add_u64 v[16:17], s[82:83], 4, v[6:7]
	v_lshl_add_u64 v[22:23], s[86:87], 4, v[6:7]
	v_lshl_add_u64 v[82:83], s[2:3], 4, v[6:7]
	v_lshl_add_u64 v[66:67], s[16:17], 0, v[2:3]
	v_or_b32_e32 v85, 1, v68
	v_or_b32_e32 v84, 2, v68
	v_or_b32_e32 v69, 3, v68
	v_and_b32_e32 v86, 0xffffffe0, v4
	s_cbranch_scc1 .LBB0_54
	v_lshl_add_u64 v[72:73], v[2:3], 2, s[14:15]
	global_load_dwordx4 v[2:5], v[72:73], off nt
	global_load_dwordx4 v[26:29], v[6:7], off nt
	global_load_dwordx4 v[30:33], v[8:9], off nt
	global_load_dwordx4 v[34:37], v[10:11], off nt
	global_load_dwordx4 v[38:41], v[72:73], off offset:16 nt
	global_load_dwordx4 v[42:45], v[14:15], off nt
	global_load_dwordx4 v[46:49], v[16:17], off nt
	global_load_dwordx4 v[50:53], v[18:19], off nt
	global_load_dwordx4 v[54:57], v[72:73], off offset:32 nt
	global_load_dwordx4 v[58:61], v[22:23], off nt
	global_load_dwordx4 v[62:65], v[24:25], off nt
	global_load_dwordx4 v[88:91], v[70:71], off nt
	global_load_dwordx4 v[92:95], v[72:73], off offset:48 nt
	global_load_dwordx4 v[96:99], v[76:77], off nt
	global_load_dwordx4 v[100:103], v[78:79], off nt
	global_load_dwordx4 v[104:107], v[80:81], off nt
	global_load_dwordx4 v[112:115], v[12:13], off nt
	global_load_dwordx4 v[124:127], v[20:21], off nt
	global_load_dwordx4 v[128:131], v[74:75], off nt
	global_load_dwordx4 v[132:135], v[82:83], off nt
	v_or_b32_e32 v87, s81, v86
	v_or_b32_e32 v72, v87, v120
	v_and_or_b32 v73, v85, 13, v87
	v_cndmask_b32_e64 v108, v72, v68, s[8:9]
	v_cndmask_b32_e64 v109, v73, v85, s[8:9]
	v_ashrrev_i32_e32 v116, 31, v108
	v_ashrrev_i32_e32 v123, 31, v109
	v_mad_u64_u32 v[72:73], s[0:1], s12, v108, v[66:67]
	v_mul_lo_u32 v117, s13, v108
	v_mul_lo_u32 v136, s13, v109
	v_mad_u64_u32 v[108:109], s[0:1], s12, v109, v[66:67]
	v_mul_lo_u32 v116, s12, v116
	v_mul_lo_u32 v123, s12, v123
	v_add3_u32 v73, v117, v73, v116
	v_add3_u32 v109, v136, v109, v123
	v_lshl_add_u64 v[72:73], v[72:73], 1, s[10:11]
	s_waitcnt vmcnt(18)
	v_pk_mul_f32 v[116:117], v[28:29], v[2:3] op_sel_hi:[1,0]
	v_pk_mul_f32 v[136:137], v[26:27], v[2:3] op_sel_hi:[1,0]
	s_waitcnt vmcnt(17)
	v_pk_mul_f32 v[32:33], v[32:33], v[2:3] op_sel:[0,1]
	v_pk_mul_f32 v[30:31], v[30:31], v[2:3] op_sel:[0,1]
	s_waitcnt vmcnt(16)
	v_pk_mul_f32 v[36:37], v[36:37], v[4:5] op_sel_hi:[1,0]
	v_pk_mul_f32 v[34:35], v[34:35], v[4:5] op_sel_hi:[1,0]
	v_mov_b32_e32 v2, v5
	s_waitcnt vmcnt(15)
	v_mov_b32_e32 v4, v41
	s_waitcnt vmcnt(11)
	v_mov_b32_e32 v26, v57
	v_pk_mul_f32 v[44:45], v[44:45], v[38:39] op_sel_hi:[1,0]
	v_pk_mul_f32 v[42:43], v[42:43], v[38:39] op_sel_hi:[1,0]
	v_pk_mul_f32 v[48:49], v[48:49], v[38:39] op_sel:[0,1]
	v_pk_mul_f32 v[38:39], v[46:47], v[38:39] op_sel:[0,1]
	v_pk_mul_f32 v[46:47], v[52:53], v[40:41] op_sel_hi:[1,0]
	v_pk_mul_f32 v[50:51], v[50:51], v[40:41] op_sel_hi:[1,0]
	s_waitcnt vmcnt(10)
	v_pk_mul_f32 v[40:41], v[60:61], v[54:55] op_sel_hi:[1,0]
	v_pk_mul_f32 v[52:53], v[58:59], v[54:55] op_sel_hi:[1,0]
	s_waitcnt vmcnt(9)
	v_pk_mul_f32 v[58:59], v[64:65], v[54:55] op_sel:[0,1]
	v_pk_mul_f32 v[54:55], v[62:63], v[54:55] op_sel:[0,1]
	s_waitcnt vmcnt(8)
	v_pk_mul_f32 v[60:61], v[90:91], v[56:57] op_sel_hi:[1,0]
	v_pk_mul_f32 v[62:63], v[88:89], v[56:57] op_sel_hi:[1,0]
	s_waitcnt vmcnt(6)
	v_pk_mul_f32 v[56:57], v[98:99], v[92:93] op_sel_hi:[1,0]
	v_pk_mul_f32 v[64:65], v[96:97], v[92:93] op_sel_hi:[1,0]
	s_waitcnt vmcnt(5)
	v_pk_mul_f32 v[88:89], v[102:103], v[92:93] op_sel:[0,1]
	v_pk_mul_f32 v[90:91], v[100:101], v[92:93] op_sel:[0,1]
	s_waitcnt vmcnt(4)
	v_pk_mul_f32 v[92:93], v[106:107], v[94:95] op_sel_hi:[1,0]
	v_mov_b32_e32 v28, v95
	s_waitcnt vmcnt(3)
	v_pk_mul_f32 v[98:99], v[112:113], v[2:3] op_sel_hi:[1,0]
	s_waitcnt vmcnt(2)
	v_pk_mul_f32 v[102:103], v[124:125], v[4:5] op_sel_hi:[1,0]
	s_waitcnt vmcnt(1)
; __device__ __forceinline__ unsigned pk4_fp8(float a, float b, float c, float d) { int w = 0; w = __builtin_amdgcn_cvt_pk_fp8_f32(a, b, w, false); w = __builtin_amdgcn_cvt_pk_fp8_f32(c, d, w, true); return (unsigned)w; }
; #define GAS __attribute__((address_space(1)))
; __device__ __forceinline__ unsigned pk2(float lo, float hi) { return f2bf(lo) | (f2bf(hi) << 16); }
; template <int MODE, int KL>
; __device__ __forceinline__ void p0_cvt_item(const float* W, int K, int N, unsigned char* WT, int il, int which, int item, int lane, const float* gk, float scale, int ldk, int koff) {
;     const int nblk = N >> 6, kb = item / nblk, nb = item - kb * nblk, nq = lane & 15, kr = lane >> 4, k0 = 4 * KL * kb + KL * kr, n0 = 64 * nb + 4 * nq;
;     const GAS f32x4* src = (const GAS f32x4*)(W + (size_t)k0 * N + n0);
;     f32x4 v[KL];
; #pragma unroll
;     for (int i = 0; i < KL; ++i) v[i] = src[(size_t)i * (N >> 2)];
;     ...
;     for (int c = 0; c < 4; ++c) { const int n = n0 + c, row = il ? ((n >> 4) * 32 + which * 16 + (n & 15)) : n;
;         if (MODE == 2) { GAS v4u* dst = (GAS v4u*)(WT + (size_t)row * ldk + koff + k0);
; #pragma unroll
;             for (int q = 0; q < KL / 16; ++q) { v4u o;
;                 o.x = pg8::pk4_fp8(v[16 * q][c], v[16 * q + 1][c], v[16 * q + 2][c], v[16 * q + 3][c]);     o.y = pg8::pk4_fp8(v[16 * q + 4][c], v[16 * q + 5][c], v[16 * q + 6][c], v[16 * q + 7][c]);
;                 o.z = pg8::pk4_fp8(v[16 * q + 8][c], v[16 * q + 9][c], v[16 * q + 10][c], v[16 * q + 11][c]); o.w = pg8::pk4_fp8(v[16 * q + 12][c], v[16 * q + 13][c], v[16 * q + 14][c], v[16 * q + 15][c]);
;                 dst[q] = o; } }
;         else { GAS v4u* dst = (GAS v4u*)(WT + ((size_t)row * ldk + koff + k0) * 2);
; #pragma unroll
;             for (int q = 0; q < KL / 8; ++q) { v4u o;
;                 if (MODE == 1) { o.x = pg8::pk_f16(v[8 * q][c], v[8 * q + 1][c]); o.y = pg8::pk_f16(v[8 * q + 2][c], v[8 * q + 3][c]); o.z = pg8::pk_f16(v[8 * q + 4][c], v[8 * q + 5][c]); o.w = pg8::pk_f16(v[8 * q + 6][c], v[8 * q + 7][c]); }
;                 else { o.x = pk2(v[8 * q][c], v[8 * q + 1][c]); o.y = pk2(v[8 * q + 2][c], v[8 * q + 3][c]); o.z = pk2(v[8 * q + 4][c], v[8 * q + 5][c]); o.w = pk2(v[8 * q + 6][c], v[8 * q + 7][c]); }
;                 dst[q] = o; } } }
	v_pk_mul_f32 v[106:107], v[128:129], v[26:27] op_sel_hi:[1,0]
	v_pk_mul_f32 v[96:97], v[104:105], v[94:95] op_sel_hi:[1,0]
	v_pk_mul_f32 v[94:95], v[114:115], v[2:3] op_sel_hi:[1,0]
	v_pk_mul_f32 v[100:101], v[126:127], v[4:5] op_sel_hi:[1,0]
	v_pk_mul_f32 v[104:105], v[130:131], v[26:27] op_sel_hi:[1,0]
	s_waitcnt vmcnt(0)
	v_pk_mul_f32 v[114:115], v[132:133], v[28:29] op_sel_hi:[1,0]
	v_cvt_pk_f16_f32 v2, v136, v30
	v_cvt_pk_f16_f32 v4, v42, v38
	v_cvt_pk_f16_f32 v26, v52, v54
	v_cvt_pk_f16_f32 v3, v34, v98
	v_cvt_pk_f16_f32 v5, v50, v102
	v_cvt_pk_f16_f32 v27, v62, v106
	v_pk_mul_f32 v[112:113], v[134:135], v[28:29] op_sel_hi:[1,0]
	v_cvt_pk_f16_f32 v28, v64, v90
	v_cvt_pk_f16_f32 v29, v96, v114
	global_store_dwordx4 v[72:73], v[2:5], off
	global_store_dwordx4 v[72:73], v[26:29], off offset:16
	s_nop 0
	v_cvt_pk_f16_f32 v2, v137, v31
	v_lshl_add_u64 v[26:27], v[108:109], 1, s[10:11]
	v_cvt_pk_f16_f32 v3, v35, v99
	v_cvt_pk_f16_f32 v4, v43, v39
	v_cvt_pk_f16_f32 v5, v51, v103
	global_store_dwordx4 v[26:27], v[2:5], off
	s_nop 1
	v_cvt_pk_f16_f32 v2, v53, v55
	v_cvt_pk_f16_f32 v3, v63, v107
	v_cvt_pk_f16_f32 v4, v65, v91
	v_cvt_pk_f16_f32 v5, v97, v115
	global_store_dwordx4 v[26:27], v[2:5], off offset:16
	s_nop 1
	v_and_or_b32 v2, v84, 14, v87
	v_cndmask_b32_e64 v2, v2, v84, s[8:9]
	v_ashrrev_i32_e32 v3, 31, v2
	v_mul_lo_u32 v4, s12, v3
	v_mul_lo_u32 v5, s13, v2
	v_mad_u64_u32 v[2:3], s[0:1], s12, v2, v[66:67]
	v_add3_u32 v3, v5, v3, v4
	v_lshl_add_u64 v[26:27], v[2:3], 1, s[10:11]
	v_cvt_pk_f16_f32 v2, v116, v32
	v_cvt_pk_f16_f32 v3, v36, v94
	v_cvt_pk_f16_f32 v4, v44, v48
	v_cvt_pk_f16_f32 v5, v46, v100
	global_store_dwordx4 v[26:27], v[2:5], off
	s_nop 1
	v_cvt_pk_f16_f32 v2, v40, v58
	v_cvt_pk_f16_f32 v3, v60, v104
	v_cvt_pk_f16_f32 v4, v56, v88
	v_cvt_pk_f16_f32 v5, v92, v112
	global_store_dwordx4 v[26:27], v[2:5], off offset:16
	s_nop 1
	v_and_or_b32 v2, v69, 15, v87
	v_cndmask_b32_e64 v2, v2, v69, s[8:9]
	v_ashrrev_i32_e32 v3, 31, v2
	v_mul_lo_u32 v4, s12, v3
	v_mul_lo_u32 v5, s13, v2
	v_mad_u64_u32 v[2:3], s[0:1], s12, v2, v[66:67]
	v_add3_u32 v3, v5, v3, v4
	v_lshl_add_u64 v[72:73], v[2:3], 1, s[10:11]
	v_cvt_pk_f16_f32 v2, v117, v33
	v_cvt_pk_f16_f32 v3, v37, v95
	v_cvt_pk_f16_f32 v4, v45, v49
	v_cvt_pk_f16_f32 v5, v47, v101
	global_store_dwordx4 v[72:73], v[2:5], off
	s_nop 1
	v_cvt_pk_f16_f32 v2, v41, v59
	v_cvt_pk_f16_f32 v3, v61, v105
	v_cvt_pk_f16_f32 v4, v57, v89
	v_cvt_pk_f16_f32 v5, v93, v113
	s_cbranch_execnz .LBB0_45
.LBB0_44:
	global_load_dwordx4 v[62:65], v[6:7], off nt
	global_load_dwordx4 v[58:61], v[8:9], off nt
	global_load_dwordx4 v[54:57], v[10:11], off nt
	global_load_dwordx4 v[50:53], v[12:13], off nt
	global_load_dwordx4 v[46:49], v[14:15], off nt
	global_load_dwordx4 v[42:45], v[16:17], off nt
	global_load_dwordx4 v[38:41], v[18:19], off nt
	global_load_dwordx4 v[34:37], v[20:21], off nt
	global_load_dwordx4 v[30:33], v[22:23], off nt
	global_load_dwordx4 v[26:29], v[24:25], off nt
	s_nop 0
	global_load_dwordx4 v[22:25], v[70:71], off nt
	global_load_dwordx4 v[18:21], v[74:75], off nt
	global_load_dwordx4 v[14:17], v[76:77], off nt
	global_load_dwordx4 v[10:13], v[78:79], off nt
	global_load_dwordx4 v[6:9], v[80:81], off nt
	global_load_dwordx4 v[2:5], v[82:83], off nt
	v_or_b32_e32 v82, s81, v86
	v_or_b32_e32 v70, v82, v120
	v_and_or_b32 v71, v85, 13, v82
	v_cndmask_b32_e64 v68, v70, v68, s[8:9]
	v_cndmask_b32_e64 v72, v71, v85, s[8:9]
	v_ashrrev_i32_e32 v74, 31, v68
	v_ashrrev_i32_e32 v75, 31, v72
	v_mad_u64_u32 v[70:71], s[0:1], s12, v68, v[66:67]
	v_mul_lo_u32 v68, s13, v68
	v_mul_lo_u32 v76, s13, v72
	v_mad_u64_u32 v[72:73], s[0:1], s12, v72, v[66:67]
	v_mul_lo_u32 v74, s12, v74
	v_mul_lo_u32 v75, s12, v75
	v_add3_u32 v71, v68, v71, v74
	v_add3_u32 v73, v76, v73, v75
	v_lshl_add_u64 v[78:79], v[70:71], 1, s[10:11]
	v_lshl_add_u64 v[80:81], v[72:73], 1, s[10:11]
	s_waitcnt vmcnt(15)
	v_bfe_u32 v68, v62, 16, 1
	s_waitcnt vmcnt(14)
	v_bfe_u32 v70, v58, 16, 1
	s_waitcnt vmcnt(13)
	v_bfe_u32 v71, v54, 16, 1
	s_waitcnt vmcnt(12)
	v_bfe_u32 v72, v50, 16, 1
	s_waitcnt vmcnt(11)
	v_bfe_u32 v73, v46, 16, 1
	s_waitcnt vmcnt(10)
	v_bfe_u32 v74, v42, 16, 1
	s_waitcnt vmcnt(9)
	v_bfe_u32 v75, v38, 16, 1
	s_waitcnt vmcnt(8)
	v_bfe_u32 v76, v34, 16, 1
	s_waitcnt vmcnt(7)
	v_bfe_u32 v77, v30, 16, 1
	v_add3_u32 v62, v62, v68, s42
	s_waitcnt vmcnt(5)
	v_bfe_u32 v85, v22, 16, 1
	v_add3_u32 v54, v54, v71, s42
	s_waitcnt vmcnt(3)
	v_bfe_u32 v87, v14, 16, 1
	v_add3_u32 v46, v46, v73, s42
	s_waitcnt vmcnt(1)
	v_bfe_u32 v89, v6, 16, 1
	s_waitcnt vmcnt(0)
; __device__ __forceinline__ unsigned pk4_fp8(float a, float b, float c, float d) { int w = 0; w = __builtin_amdgcn_cvt_pk_fp8_f32(a, b, w, false); w = __builtin_amdgcn_cvt_pk_fp8_f32(c, d, w, true); return (unsigned)w; }
; #define GAS __attribute__((address_space(1)))
; __device__ __forceinline__ unsigned pk2(float lo, float hi) { return f2bf(lo) | (f2bf(hi) << 16); }
; template <int MODE, int KL>
; __device__ __forceinline__ void p0_cvt_item(const float* W, int K, int N, unsigned char* WT, int il, int which, int item, int lane, const float* gk, float scale, int ldk, int koff) {
;     ...
;     for (int c = 0; c < 4; ++c) { const int n = n0 + c, row = il ? ((n >> 4) * 32 + which * 16 + (n & 15)) : n;
;         if (MODE == 2) { GAS v4u* dst = (GAS v4u*)(WT + (size_t)row * ldk + koff + k0);
; #pragma unroll
;             for (int q = 0; q < KL / 16; ++q) { v4u o;
;                 o.x = pg8::pk4_fp8(v[16 * q][c], v[16 * q + 1][c], v[16 * q + 2][c], v[16 * q + 3][c]);     o.y = pg8::pk4_fp8(v[16 * q + 4][c], v[16 * q + 5][c], v[16 * q + 6][c], v[16 * q + 7][c]);
;                 o.z = pg8::pk4_fp8(v[16 * q + 8][c], v[16 * q + 9][c], v[16 * q + 10][c], v[16 * q + 11][c]); o.w = pg8::pk4_fp8(v[16 * q + 12][c], v[16 * q + 13][c], v[16 * q + 14][c], v[16 * q + 15][c]);
;                 dst[q] = o; } }
;         else { GAS v4u* dst = (GAS v4u*)(WT + ((size_t)row * ldk + koff + k0) * 2);
; #pragma unroll
;             for (int q = 0; q < KL / 8; ++q) { v4u o;
;                 if (MODE == 1) { o.x = pg8::pk_f16(v[8 * q][c], v[8 * q + 1][c]); o.y = pg8::pk_f16(v[8 * q + 2][c], v[8 * q + 3][c]); o.z = pg8::pk_f16(v[8 * q + 4][c], v[8 * q + 5][c]); o.w = pg8::pk_f16(v[8 * q + 6][c], v[8 * q + 7][c]); }
;                 else { o.x = pk2(v[8 * q][c], v[8 * q + 1][c]); o.y = pk2(v[8 * q + 2][c], v[8 * q + 3][c]); o.z = pk2(v[8 * q + 4][c], v[8 * q + 5][c]); o.w = pk2(v[8 * q + 6][c], v[8 * q + 7][c]); }
;                 dst[q] = o; } } }
	v_bfe_u32 v90, v2, 16, 1
	v_add3_u32 v6, v6, v89, s42
	v_add3_u32 v2, v2, v90, s42
	v_lshrrev_b32_e32 v6, 16, v6
	v_add3_u32 v38, v38, v75, s42
	v_add3_u32 v30, v30, v77, s42
	v_and_or_b32 v77, v2, s43, v6
	v_bfe_u32 v2, v63, 16, 1
	v_bfe_u32 v83, v26, 16, 1
	v_bfe_u32 v86, v18, 16, 1
	v_bfe_u32 v88, v10, 16, 1
	v_add3_u32 v58, v58, v70, s42
	v_add3_u32 v50, v50, v72, s42
	v_add3_u32 v42, v42, v74, s42
	v_add3_u32 v34, v34, v76, s42
	v_add3_u32 v22, v22, v85, s42
	v_add3_u32 v14, v14, v87, s42
	v_lshrrev_b32_e32 v62, 16, v62
	v_lshrrev_b32_e32 v54, 16, v54
	v_lshrrev_b32_e32 v46, 16, v46
	v_lshrrev_b32_e32 v38, 16, v38
	v_add3_u32 v2, v63, v2, s42
	v_bfe_u32 v6, v59, 16, 1
	v_add3_u32 v26, v26, v83, s42
	v_add3_u32 v18, v18, v86, s42
	v_add3_u32 v10, v10, v88, s42
	v_lshrrev_b32_e32 v30, 16, v30
	v_lshrrev_b32_e32 v22, 16, v22
	v_lshrrev_b32_e32 v14, 16, v14
	v_and_or_b32 v70, v58, s43, v62
	v_and_or_b32 v71, v50, s43, v54
	v_and_or_b32 v72, v42, s43, v46
	v_and_or_b32 v73, v34, s43, v38
	v_lshrrev_b32_e32 v2, 16, v2
	v_add3_u32 v6, v59, v6, s42
	v_and_or_b32 v74, v26, s43, v30
	v_and_or_b32 v75, v18, s43, v22
	v_and_or_b32 v76, v10, s43, v14
	global_store_dwordx4 v[78:79], v[70:73], off
	global_store_dwordx4 v[78:79], v[74:77], off offset:16
	s_nop 0
	v_and_or_b32 v70, v6, s43, v2
	v_bfe_u32 v2, v55, 16, 1
	v_add3_u32 v2, v55, v2, s42
	v_bfe_u32 v6, v51, 16, 1
	v_lshrrev_b32_e32 v2, 16, v2
	v_add3_u32 v6, v51, v6, s42
	v_and_or_b32 v71, v6, s43, v2
	v_bfe_u32 v2, v47, 16, 1
	v_add3_u32 v2, v47, v2, s42
	v_bfe_u32 v6, v43, 16, 1
	v_lshrrev_b32_e32 v2, 16, v2
	v_add3_u32 v6, v43, v6, s42
	v_and_or_b32 v72, v6, s43, v2
	v_bfe_u32 v2, v39, 16, 1
	v_add3_u32 v2, v39, v2, s42
	v_bfe_u32 v6, v35, 16, 1
	v_lshrrev_b32_e32 v2, 16, v2
	v_add3_u32 v6, v35, v6, s42
	v_and_or_b32 v73, v6, s43, v2
	v_bfe_u32 v2, v31, 16, 1
	v_add3_u32 v2, v31, v2, s42
	v_bfe_u32 v6, v27, 16, 1
	v_lshrrev_b32_e32 v2, 16, v2
	v_add3_u32 v6, v27, v6, s42
	global_store_dwordx4 v[80:81], v[70:73], off
	s_nop 1
	v_and_or_b32 v70, v6, s43, v2
	v_bfe_u32 v2, v23, 16, 1
	v_add3_u32 v2, v23, v2, s42
	v_bfe_u32 v6, v19, 16, 1
	v_lshrrev_b32_e32 v2, 16, v2
	v_add3_u32 v6, v19, v6, s42
	v_and_or_b32 v71, v6, s43, v2
	v_bfe_u32 v2, v15, 16, 1
	v_add3_u32 v2, v15, v2, s42
	v_bfe_u32 v6, v11, 16, 1
	v_lshrrev_b32_e32 v2, 16, v2
	v_add3_u32 v6, v11, v6, s42
	v_and_or_b32 v72, v6, s43, v2
	v_bfe_u32 v2, v7, 16, 1
	v_add3_u32 v2, v7, v2, s42
	v_bfe_u32 v6, v3, 16, 1
	v_lshrrev_b32_e32 v2, 16, v2
	v_add3_u32 v3, v3, v6, s42
	v_and_or_b32 v73, v3, s43, v2
	v_and_or_b32 v2, v84, 14, v82
	v_cndmask_b32_e64 v2, v2, v84, s[8:9]
	v_ashrrev_i32_e32 v3, 31, v2
	v_mul_lo_u32 v6, s12, v3
	v_mul_lo_u32 v7, s13, v2
	v_mad_u64_u32 v[2:3], s[0:1], s12, v2, v[66:67]
	v_add3_u32 v3, v7, v3, v6
	v_bfe_u32 v6, v64, 16, 1
	v_add3_u32 v6, v64, v6, s42
	v_bfe_u32 v7, v60, 16, 1
	v_lshrrev_b32_e32 v6, 16, v6
	v_add3_u32 v7, v60, v7, s42
	global_store_dwordx4 v[80:81], v[70:73], off offset:16
	v_lshl_add_u64 v[2:3], v[2:3], 1, s[10:11]
	s_nop 0
	v_and_or_b32 v70, v7, s43, v6
	v_bfe_u32 v6, v56, 16, 1
	v_add3_u32 v6, v56, v6, s42
	v_bfe_u32 v7, v52, 16, 1
	v_lshrrev_b32_e32 v6, 16, v6
	v_add3_u32 v7, v52, v7, s42
	v_and_or_b32 v71, v7, s43, v6
	v_bfe_u32 v6, v48, 16, 1
	v_add3_u32 v6, v48, v6, s42
	v_bfe_u32 v7, v44, 16, 1
	v_lshrrev_b32_e32 v6, 16, v6
	v_add3_u32 v7, v44, v7, s42
	v_and_or_b32 v72, v7, s43, v6
	v_bfe_u32 v6, v40, 16, 1
	v_add3_u32 v6, v40, v6, s42
	v_bfe_u32 v7, v36, 16, 1
	v_lshrrev_b32_e32 v6, 16, v6
	v_add3_u32 v7, v36, v7, s42
	v_and_or_b32 v73, v7, s43, v6
	v_bfe_u32 v6, v32, 16, 1
	v_add3_u32 v6, v32, v6, s42
	v_bfe_u32 v7, v28, 16, 1
	v_lshrrev_b32_e32 v6, 16, v6
	v_add3_u32 v7, v28, v7, s42
	global_store_dwordx4 v[2:3], v[70:73], off
	s_nop 1
	v_and_or_b32 v70, v7, s43, v6
	v_bfe_u32 v6, v24, 16, 1
	v_add3_u32 v6, v24, v6, s42
	v_bfe_u32 v7, v20, 16, 1
	v_lshrrev_b32_e32 v6, 16, v6
	v_add3_u32 v7, v20, v7, s42
	v_and_or_b32 v71, v7, s43, v6
	v_bfe_u32 v6, v16, 16, 1
	v_add3_u32 v6, v16, v6, s42
	v_bfe_u32 v7, v12, 16, 1
	v_lshrrev_b32_e32 v6, 16, v6
	v_add3_u32 v7, v12, v7, s42
	v_and_or_b32 v72, v7, s43, v6
	v_bfe_u32 v6, v8, 16, 1
	v_add3_u32 v6, v8, v6, s42
	v_bfe_u32 v7, v4, 16, 1
	v_lshrrev_b32_e32 v6, 16, v6
	v_add3_u32 v4, v4, v7, s42
	v_and_or_b32 v73, v4, s43, v6
	global_store_dwordx4 v[2:3], v[70:73], off offset:16
	v_and_or_b32 v2, v69, 15, v82
	v_cndmask_b32_e64 v2, v2, v69, s[8:9]
	v_ashrrev_i32_e32 v3, 31, v2
	v_mul_lo_u32 v4, s12, v3
	v_mul_lo_u32 v6, s13, v2
	v_mad_u64_u32 v[2:3], s[0:1], s12, v2, v[66:67]
	v_add3_u32 v3, v6, v3, v4
	v_lshl_add_u64 v[72:73], v[2:3], 1, s[10:11]
	v_bfe_u32 v2, v65, 16, 1
	v_add3_u32 v2, v65, v2, s42
	v_bfe_u32 v3, v61, 16, 1
	v_lshrrev_b32_e32 v2, 16, v2
	v_add3_u32 v3, v61, v3, s42
	v_and_or_b32 v34, v3, s43, v2
	v_bfe_u32 v2, v57, 16, 1
	v_add3_u32 v2, v57, v2, s42
	v_bfe_u32 v3, v53, 16, 1
	v_lshrrev_b32_e32 v2, 16, v2
	v_add3_u32 v3, v53, v3, s42
	v_and_or_b32 v35, v3, s43, v2
	v_bfe_u32 v2, v49, 16, 1
	v_add3_u32 v2, v49, v2, s42
	v_bfe_u32 v3, v45, 16, 1
	v_lshrrev_b32_e32 v2, 16, v2
	v_add3_u32 v3, v45, v3, s42
	v_and_or_b32 v36, v3, s43, v2
	v_bfe_u32 v2, v41, 16, 1
	v_add3_u32 v2, v41, v2, s42
	v_bfe_u32 v3, v37, 16, 1
	v_lshrrev_b32_e32 v2, 16, v2
	v_add3_u32 v3, v37, v3, s42
	v_and_or_b32 v37, v3, s43, v2
	v_bfe_u32 v2, v33, 16, 1
	v_add3_u32 v2, v33, v2, s42
	v_bfe_u32 v3, v29, 16, 1
	v_lshrrev_b32_e32 v2, 16, v2
	v_add3_u32 v3, v29, v3, s42
	v_and_or_b32 v2, v3, s43, v2
	v_bfe_u32 v3, v25, 16, 1
	v_add3_u32 v3, v25, v3, s42
	v_bfe_u32 v4, v21, 16, 1
	v_lshrrev_b32_e32 v3, 16, v3
	v_add3_u32 v4, v21, v4, s42
	v_and_or_b32 v3, v4, s43, v3
	v_bfe_u32 v4, v17, 16, 1
	v_add3_u32 v4, v17, v4, s42
	v_bfe_u32 v6, v13, 16, 1
	v_lshrrev_b32_e32 v4, 16, v4
	v_add3_u32 v6, v13, v6, s42
	v_and_or_b32 v4, v6, s43, v4
	v_bfe_u32 v6, v9, 16, 1
	v_add3_u32 v6, v9, v6, s42
	v_bfe_u32 v7, v5, 16, 1
	v_lshrrev_b32_e32 v6, 16, v6
	v_add3_u32 v5, v5, v7, s42
	v_and_or_b32 v5, v5, s43, v6
	global_store_dwordx4 v[72:73], v[34:37], off

; __device__ __forceinline__ unsigned pk4_fp8(float a, float b, float c, float d) { int w = 0; w = __builtin_amdgcn_cvt_pk_fp8_f32(a, b, w, false); w = __builtin_amdgcn_cvt_pk_fp8_f32(c, d, w, true); return (unsigned)w; }
; template <int MODE, int KL>
; __device__ __forceinline__ void p0_cvt_item(const float* W, int K, int N, unsigned char* WT, int il, int which, int item, int lane, const float* gk, float scale, int ldk, int koff) {
;     const int nblk = N >> 6, kb = item / nblk, nb = item - kb * nblk, nq = lane & 15, kr = lane >> 4, k0 = 4 * KL * kb + KL * kr, n0 = 64 * nb + 4 * nq;
;     const GAS f32x4* src = (const GAS f32x4*)(W + (size_t)k0 * N + n0);
;     f32x4 v[KL];
; #pragma unroll
;     for (int i = 0; i < KL; ++i) v[i] = src[(size_t)i * (N >> 2)];
;     if (MODE == 1) {
; #pragma unroll
;         for (int q = 0; q < KL / 4; ++q) { const f32x4 g = *(const GAS f32x4*)(gk + k0 + 4 * q); v[4 * q] *= g.x; v[4 * q + 1] *= g.y; v[4 * q + 2] *= g.z; v[4 * q + 3] *= g.w; } }
;     if (MODE == 2) {
; #pragma unroll
;         for (int i = 0; i < KL; ++i) v[i] *= scale; }
; #pragma unroll
;     for (int c = 0; c < 4; ++c) { const int n = n0 + c, row = il ? ((n >> 4) * 32 + which * 16 + (n & 15)) : n;
;         if (MODE == 2) { GAS v4u* dst = (GAS v4u*)(WT + (size_t)row * ldk + koff + k0);
; #pragma unroll
;             for (int q = 0; q < KL / 16; ++q) { v4u o;
;                 o.x = pg8::pk4_fp8(v[16 * q][c], v[16 * q + 1][c], v[16 * q + 2][c], v[16 * q + 3][c]);     o.y = pg8::pk4_fp8(v[16 * q + 4][c], v[16 * q + 5][c], v[16 * q + 6][c], v[16 * q + 7][c]);
;                 o.z = pg8::pk4_fp8(v[16 * q + 8][c], v[16 * q + 9][c], v[16 * q + 10][c], v[16 * q + 11][c]); o.w = pg8::pk4_fp8(v[16 * q + 12][c], v[16 * q + 13][c], v[16 * q + 14][c], v[16 * q + 15][c]);
;                 dst[q] = o; } }
; __device__ __forceinline__ void moe_cvt_tile(const Args& a, int set, int id, int lane) {
;     const int j = id / MT_PER, item = id - j * MT_PER;
;     if (j < 16) { const int e = set * 8 + (j & 7), wh = j >> 3;
;         p0_cvt_item<2, 32>(a.in[17 + wh] + (size_t)e * D * FE, D, FE, a.ws + W_13M + (size_t)e * 2 * FE * D, 1, wh, item, lane, nullptr, 32.f, D, 0); }
;     else { const int e = set * 8 + (j - 16); p0_cvt_item<2, 32>(a.in[19] + (size_t)e * FE * D, FE, D, a.ws + W_2M + (size_t)e * D * FE, 0, 0, item, lane, nullptr, 64.f, FE, 0); }
; }
.LBB0_46:
	s_and_b64 vcc, exec, s[0:1]
	s_cbranch_vccz .LBB0_48
	s_and_b32 s0, 0xffff, s40
	s_mul_hi_u32 s0, s0, 0x924925
	s_add_i32 s11, s80, 0x1400
	s_mul_i32 s2, s0, 0xffff9000
	s_mul_i32 s10, s0, 0xfffffe40
	s_bfe_u32 s0, s11, 0xa0006
	s_mul_i32 s8, s0, 0x2493
	s_load_dwordx2 s[0:1], s[92:93], 0x98
	s_lshr_b32 s8, s8, 16
	s_add_i32 s12, s8, -8
	s_mul_i32 s8, s12, 0xe00000
	s_mul_hi_u32 s9, s12, 0xe00000
	s_waitcnt lgkmcnt(0)
	s_add_u32 s8, s0, s8
	s_addc_u32 s9, s1, s9
	s_mul_hi_u32 s1, s12, 0x380000
	s_mul_i32 s12, s12, 0x380000
	s_add_u32 s0, s34, s12
	s_addc_u32 s1, s35, s1
	s_add_i32 s10, s11, s10
	s_sext_i32_i16 s11, s10
	s_bfe_u32 s11, s11, 0x4001b
	s_add_i32 s10, s10, s11
	s_sext_i32_i16 s10, s10
	s_ashr_i32 s10, s10, 4
	v_lshl_or_b32 v108, s10, 7, v121
	s_lshl_b32 s10, s10, 10
	v_subrev_u32_e32 v2, s10, v122
	v_add_u32_e32 v123, s2, v2
	v_ashrrev_i32_e32 v109, 31, v108
	v_add_u32_e32 v10, 0xfffefffd, v123
	v_lshlrev_b64 v[2:3], 12, v[108:109]
	v_lshl_add_u64 v[2:3], s[8:9], 0, v[2:3]
	v_ashrrev_i32_e32 v11, 31, v10
	v_lshl_add_u64 v[6:7], v[10:11], 2, v[2:3]
	v_add_co_u32_e32 v8, vcc, s44, v6
	global_load_dwordx4 v[2:5], v[6:7], off nt
	s_nop 0
	v_addc_co_u32_e32 v9, vcc, 0, v7, vcc
	global_load_dwordx4 v[12:15], v[8:9], off offset:-4096 nt
	global_load_dwordx4 v[16:19], v[8:9], off nt
	v_add_co_u32_e32 v8, vcc, s45, v6
	v_lshl_add_u64 v[108:109], s[0:1], 0, v[108:109]
	s_nop 0
	v_addc_co_u32_e32 v9, vcc, 0, v7, vcc
	global_load_dwordx4 v[20:23], v[8:9], off offset:-4096 nt
	global_load_dwordx4 v[24:27], v[8:9], off nt
	v_add_co_u32_e32 v8, vcc, s46, v6
	v_mad_i64_i32 v[10:11], s[0:1], v10, s61, v[108:109]
	s_nop 0
	v_addc_co_u32_e32 v9, vcc, 0, v7, vcc
	global_load_dwordx4 v[28:31], v[8:9], off offset:-4096 nt
	global_load_dwordx4 v[32:35], v[8:9], off nt
	v_add_co_u32_e32 v8, vcc, s47, v6
	s_waitcnt vmcnt(6)
	v_pk_mul_f32 v[116:117], v[2:3], s[4:5] op_sel_hi:[1,0]
	v_addc_co_u32_e32 v9, vcc, 0, v7, vcc
	global_load_dwordx4 v[36:39], v[8:9], off offset:-4096 nt
	global_load_dwordx4 v[40:43], v[8:9], off nt
	v_add_co_u32_e32 v8, vcc, s48, v6
	s_waitcnt vmcnt(7)
	v_pk_mul_f32 v[148:149], v[12:13], s[4:5] op_sel_hi:[1,0]
	v_addc_co_u32_e32 v9, vcc, 0, v7, vcc
	global_load_dwordx4 v[44:47], v[8:9], off offset:-4096 nt
	global_load_dwordx4 v[48:51], v[8:9], off nt
	v_add_co_u32_e32 v8, vcc, s49, v6
	s_waitcnt vmcnt(8)
	v_pk_mul_f32 v[2:3], v[18:19], s[4:5] op_sel_hi:[1,0]
	v_addc_co_u32_e32 v9, vcc, 0, v7, vcc
	global_load_dwordx4 v[52:55], v[8:9], off offset:-4096 nt
	global_load_dwordx4 v[56:59], v[8:9], off nt
	v_add_co_u32_e32 v8, vcc, s50, v6
	v_pk_mul_f32 v[150:151], v[16:17], s[4:5] op_sel_hi:[1,0]
	s_nop 0
	v_addc_co_u32_e32 v9, vcc, 0, v7, vcc
	global_load_dwordx4 v[60:63], v[8:9], off offset:-4096 nt
	global_load_dwordx4 v[64:67], v[8:9], off nt
	v_add_co_u32_e32 v8, vcc, s51, v6
	s_waitcnt vmcnt(11)
	v_pk_mul_f32 v[152:153], v[20:21], s[4:5] op_sel_hi:[1,0]
	v_addc_co_u32_e32 v9, vcc, 0, v7, vcc
	global_load_dwordx4 v[68:71], v[8:9], off offset:-4096 nt
	global_load_dwordx4 v[72:75], v[8:9], off nt
	v_add_co_u32_e32 v8, vcc, s52, v6
	s_waitcnt vmcnt(12)
	v_pk_mul_f32 v[154:155], v[24:25], s[4:5] op_sel_hi:[1,0]
	v_addc_co_u32_e32 v9, vcc, 0, v7, vcc
	global_load_dwordx4 v[76:79], v[8:9], off offset:-4096 nt
	global_load_dwordx4 v[80:83], v[8:9], off nt
	v_add_co_u32_e32 v8, vcc, s53, v6
	s_waitcnt vmcnt(13)
	v_pk_mul_f32 v[18:19], v[30:31], s[4:5] op_sel_hi:[1,0]
	v_addc_co_u32_e32 v9, vcc, 0, v7, vcc
	global_load_dwordx4 v[84:87], v[8:9], off offset:-4096 nt
	global_load_dwordx4 v[88:91], v[8:9], off nt
	v_add_co_u32_e32 v8, vcc, s54, v6
	v_pk_mul_f32 v[156:157], v[28:29], s[4:5] op_sel_hi:[1,0]
	s_nop 0
	v_addc_co_u32_e32 v9, vcc, 0, v7, vcc
	global_load_dwordx4 v[92:95], v[8:9], off offset:-4096 nt
	global_load_dwordx4 v[96:99], v[8:9], off nt
	v_add_co_u32_e32 v8, vcc, s55, v6
	v_mov_b32_e32 v28, 0
	s_nop 0
	v_addc_co_u32_e32 v9, vcc, 0, v7, vcc
	global_load_dwordx4 v[100:103], v[8:9], off offset:-4096 nt
	global_load_dwordx4 v[104:107], v[8:9], off nt
	v_add_co_u32_e32 v8, vcc, s56, v6
	v_mov_b32_e32 v29, 0
	s_nop 0
	v_addc_co_u32_e32 v9, vcc, 0, v7, vcc
	global_load_dwordx4 v[112:115], v[8:9], off offset:-4096 nt
	global_load_dwordx4 v[124:127], v[8:9], off nt
	v_add_co_u32_e32 v8, vcc, s57, v6
	v_mov_b32_e32 v30, 0
	s_nop 0
	v_addc_co_u32_e32 v9, vcc, 0, v7, vcc
	global_load_dwordx4 v[128:131], v[8:9], off offset:-4096 nt
	global_load_dwordx4 v[132:135], v[8:9], off nt
	v_add_co_u32_e32 v8, vcc, s58, v6
	v_mov_b32_e32 v31, 0
	s_nop 0
	v_addc_co_u32_e32 v9, vcc, 0, v7, vcc
	global_load_dwordx4 v[136:139], v[8:9], off offset:-4096 nt
	global_load_dwordx4 v[140:143], v[8:9], off nt
	v_add_co_u32_e32 v6, vcc, s60, v6
	s_waitcnt vmcnt(24)
	v_pk_mul_f32 v[12:13], v[34:35], s[4:5] op_sel_hi:[1,0]
	v_addc_co_u32_e32 v7, vcc, 0, v7, vcc
	global_load_dwordx4 v[144:147], v[6:7], off nt
	v_pk_mul_f32 v[158:159], v[32:33], s[4:5] op_sel_hi:[1,0]
	v_cvt_pk_fp8_f32 v28, v116, v148
	v_cvt_pk_fp8_f32 v29, v154, v156
	v_mov_b32_e32 v32, 0
	v_mov_b32_e32 v33, 0
	v_mov_b32_e32 v34, 0
	s_waitcnt vmcnt(24)
	v_pk_mul_f32 v[16:17], v[38:39], s[4:5] op_sel_hi:[1,0]
	s_waitcnt vmcnt(23)
	v_pk_mul_f32 v[20:21], v[42:43], s[4:5] op_sel_hi:[1,0]
	v_pk_mul_f32 v[38:39], v[40:41], s[4:5] op_sel_hi:[1,0]
	v_mov_b32_e32 v35, 0
	v_pk_mul_f32 v[36:37], v[36:37], s[4:5] op_sel_hi:[1,0]
	v_cvt_pk_fp8_f32 v28, v150, v152 op_sel:[0,0,1]
	s_waitcnt vmcnt(22)
	v_pk_mul_f32 v[40:41], v[44:45], s[4:5] op_sel_hi:[1,0]
	s_waitcnt vmcnt(21)
; __device__ __forceinline__ unsigned pk4_fp8(float a, float b, float c, float d) { int w = 0; w = __builtin_amdgcn_cvt_pk_fp8_f32(a, b, w, false); w = __builtin_amdgcn_cvt_pk_fp8_f32(c, d, w, true); return (unsigned)w; }
; #define GAS __attribute__((address_space(1)))
; template <int MODE, int KL>
; __device__ __forceinline__ void p0_cvt_item(const float* W, int K, int N, unsigned char* WT, int il, int which, int item, int lane, const float* gk, float scale, int ldk, int koff) {
;     ...
; #pragma unroll
;     for (int c = 0; c < 4; ++c) { const int n = n0 + c, row = il ? ((n >> 4) * 32 + which * 16 + (n & 15)) : n;
;         if (MODE == 2) { GAS v4u* dst = (GAS v4u*)(WT + (size_t)row * ldk + koff + k0);
; #pragma unroll
;             for (int q = 0; q < KL / 16; ++q) { v4u o;
;                 o.x = pg8::pk4_fp8(v[16 * q][c], v[16 * q + 1][c], v[16 * q + 2][c], v[16 * q + 3][c]);     o.y = pg8::pk4_fp8(v[16 * q + 4][c], v[16 * q + 5][c], v[16 * q + 6][c], v[16 * q + 7][c]);
;                 o.z = pg8::pk4_fp8(v[16 * q + 8][c], v[16 * q + 9][c], v[16 * q + 10][c], v[16 * q + 11][c]); o.w = pg8::pk4_fp8(v[16 * q + 12][c], v[16 * q + 13][c], v[16 * q + 14][c], v[16 * q + 15][c]);
;                 dst[q] = o; } }
	v_pk_mul_f32 v[42:43], v[48:49], s[4:5] op_sel_hi:[1,0]
	v_cvt_pk_fp8_f32 v30, v38, v40
	v_cvt_pk_fp8_f32 v29, v158, v36 op_sel:[0,0,1]
	v_pk_mul_f32 v[6:7], v[4:5], s[4:5] op_sel_hi:[1,0]
	v_pk_mul_f32 v[8:9], v[14:15], s[4:5] op_sel_hi:[1,0]
	s_waitcnt vmcnt(20)
	v_pk_mul_f32 v[44:45], v[52:53], s[4:5] op_sel_hi:[1,0]
	s_waitcnt vmcnt(19)
	v_pk_mul_f32 v[48:49], v[56:57], s[4:5] op_sel_hi:[1,0]
	v_cvt_pk_fp8_f32 v30, v42, v44 op_sel:[0,0,1]
	v_pk_mul_f32 v[4:5], v[22:23], s[4:5] op_sel_hi:[1,0]
	v_pk_mul_f32 v[14:15], v[26:27], s[4:5] op_sel_hi:[1,0]
	v_pk_mul_f32 v[24:25], v[46:47], s[4:5] op_sel_hi:[1,0]
	s_waitcnt vmcnt(18)
	v_pk_mul_f32 v[52:53], v[60:61], s[4:5] op_sel_hi:[1,0]
	s_waitcnt vmcnt(17)
	v_pk_mul_f32 v[56:57], v[64:65], s[4:5] op_sel_hi:[1,0]
	v_cvt_pk_fp8_f32 v31, v48, v52
	v_pk_mul_f32 v[22:23], v[50:51], s[4:5] op_sel_hi:[1,0]
	v_pk_mul_f32 v[46:47], v[58:59], s[4:5] op_sel_hi:[1,0]
	v_pk_mul_f32 v[50:51], v[62:63], s[4:5] op_sel_hi:[1,0]
	s_waitcnt vmcnt(16)
	v_pk_mul_f32 v[60:61], v[68:69], s[4:5] op_sel_hi:[1,0]
	s_waitcnt vmcnt(15)
	v_pk_mul_f32 v[64:65], v[72:73], s[4:5] op_sel_hi:[1,0]
	v_cvt_pk_fp8_f32 v31, v56, v60 op_sel:[0,0,1]
	v_pk_mul_f32 v[26:27], v[54:55], s[4:5] op_sel_hi:[1,0]
	v_pk_mul_f32 v[54:55], v[66:67], s[4:5] op_sel_hi:[1,0]
	v_pk_mul_f32 v[58:59], v[70:71], s[4:5] op_sel_hi:[1,0]
	s_waitcnt vmcnt(14)
	v_pk_mul_f32 v[68:69], v[76:77], s[4:5] op_sel_hi:[1,0]
	s_waitcnt vmcnt(13)
	v_pk_mul_f32 v[72:73], v[80:81], s[4:5] op_sel_hi:[1,0]
	v_cvt_pk_fp8_f32 v32, v64, v68
	v_pk_mul_f32 v[62:63], v[74:75], s[4:5] op_sel_hi:[1,0]
	v_pk_mul_f32 v[66:67], v[78:79], s[4:5] op_sel_hi:[1,0]
	v_pk_mul_f32 v[70:71], v[82:83], s[4:5] op_sel_hi:[1,0]
	s_waitcnt vmcnt(12)
	v_pk_mul_f32 v[76:77], v[84:85], s[4:5] op_sel_hi:[1,0]
	s_waitcnt vmcnt(11)
	v_pk_mul_f32 v[80:81], v[88:89], s[4:5] op_sel_hi:[1,0]
	v_cvt_pk_fp8_f32 v32, v72, v76 op_sel:[0,0,1]
	v_pk_mul_f32 v[74:75], v[86:87], s[4:5] op_sel_hi:[1,0]
	v_pk_mul_f32 v[78:79], v[90:91], s[4:5] op_sel_hi:[1,0]
	s_waitcnt vmcnt(10)
	v_pk_mul_f32 v[84:85], v[92:93], s[4:5] op_sel_hi:[1,0]
	s_waitcnt vmcnt(9)
	v_pk_mul_f32 v[88:89], v[96:97], s[4:5] op_sel_hi:[1,0]
	v_cvt_pk_fp8_f32 v33, v80, v84
	v_pk_mul_f32 v[82:83], v[94:95], s[4:5] op_sel_hi:[1,0]
	v_pk_mul_f32 v[86:87], v[98:99], s[4:5] op_sel_hi:[1,0]
	s_waitcnt vmcnt(8)
	v_pk_mul_f32 v[92:93], v[100:101], s[4:5] op_sel_hi:[1,0]
	s_waitcnt vmcnt(7)
	v_pk_mul_f32 v[96:97], v[104:105], s[4:5] op_sel_hi:[1,0]
	v_cvt_pk_fp8_f32 v33, v88, v92 op_sel:[0,0,1]
	v_pk_mul_f32 v[90:91], v[102:103], s[4:5] op_sel_hi:[1,0]
	v_pk_mul_f32 v[94:95], v[106:107], s[4:5] op_sel_hi:[1,0]
	s_waitcnt vmcnt(6)
	v_pk_mul_f32 v[100:101], v[112:113], s[4:5] op_sel_hi:[1,0]
	s_waitcnt vmcnt(5)
	v_pk_mul_f32 v[104:105], v[124:125], s[4:5] op_sel_hi:[1,0]
	v_cvt_pk_fp8_f32 v34, v96, v100
	v_pk_mul_f32 v[98:99], v[114:115], s[4:5] op_sel_hi:[1,0]
	v_pk_mul_f32 v[102:103], v[126:127], s[4:5] op_sel_hi:[1,0]
	s_waitcnt vmcnt(4)
	v_pk_mul_f32 v[112:113], v[128:129], s[4:5] op_sel_hi:[1,0]
	s_waitcnt vmcnt(3)
	v_pk_mul_f32 v[124:125], v[132:133], s[4:5] op_sel_hi:[1,0]
	v_cvt_pk_fp8_f32 v34, v104, v112 op_sel:[0,0,1]
	v_pk_mul_f32 v[114:115], v[134:135], s[4:5] op_sel_hi:[1,0]
	v_pk_mul_f32 v[106:107], v[130:131], s[4:5] op_sel_hi:[1,0]
	s_waitcnt vmcnt(2)
	v_pk_mul_f32 v[128:129], v[136:137], s[4:5] op_sel_hi:[1,0]
	s_nop 0
	v_cvt_pk_fp8_f32 v35, v124, v128
	s_waitcnt vmcnt(1)
	v_pk_mul_f32 v[132:133], v[140:141], s[4:5] op_sel_hi:[1,0]
	v_pk_mul_f32 v[126:127], v[138:139], s[4:5] op_sel_hi:[1,0]
	v_pk_mul_f32 v[130:131], v[142:143], s[4:5] op_sel_hi:[1,0]
	s_waitcnt vmcnt(0)
	v_pk_mul_f32 v[136:137], v[144:145], s[4:5] op_sel_hi:[1,0]
	s_nop 0
	v_cvt_pk_fp8_f32 v35, v132, v136 op_sel:[0,0,1]
	global_store_dwordx4 v[10:11], v[28:31], off
	global_store_dwordx4 v[10:11], v[32:35], off offset:16
	s_nop 0
	v_mov_b32_e32 v28, 0
	v_mov_b32_e32 v29, 0
	v_mov_b32_e32 v30, 0
	v_mov_b32_e32 v31, 0
	v_cvt_pk_fp8_f32 v28, v117, v149
	v_cvt_pk_fp8_f32 v29, v155, v157
	v_cvt_pk_fp8_f32 v30, v39, v41
	v_cvt_pk_fp8_f32 v31, v49, v53
	v_mov_b32_e32 v32, 0
	v_mov_b32_e32 v33, 0
	v_mov_b32_e32 v34, 0
	v_mov_b32_e32 v35, 0
	v_cvt_pk_fp8_f32 v32, v65, v69
	v_cvt_pk_fp8_f32 v33, v81, v85
	v_cvt_pk_fp8_f32 v34, v97, v101
	v_cvt_pk_fp8_f32 v35, v125, v129
	v_cvt_pk_fp8_f32 v28, v151, v153 op_sel:[0,0,1]
	v_cvt_pk_fp8_f32 v29, v159, v37 op_sel:[0,0,1]
	v_cvt_pk_fp8_f32 v30, v43, v45 op_sel:[0,0,1]
	v_cvt_pk_fp8_f32 v31, v57, v61 op_sel:[0,0,1]
	v_cvt_pk_fp8_f32 v32, v73, v77 op_sel:[0,0,1]
	v_cvt_pk_fp8_f32 v33, v89, v93 op_sel:[0,0,1]
	v_cvt_pk_fp8_f32 v34, v105, v113 op_sel:[0,0,1]
	v_cvt_pk_fp8_f32 v35, v133, v137 op_sel:[0,0,1]
	v_add_u32_e32 v10, 0xfffefffe, v123
	v_mad_i64_i32 v[10:11], s[0:1], v10, s61, v[108:109]
	global_store_dwordx4 v[10:11], v[28:31], off
	global_store_dwordx4 v[10:11], v[32:35], off offset:16
	v_pk_mul_f32 v[134:135], v[146:147], s[4:5] op_sel_hi:[1,0]
	v_mov_b32_e32 v28, 0
	v_cvt_pk_fp8_f32 v28, v6, v8
	v_mov_b32_e32 v6, 0
	v_cvt_pk_fp8_f32 v6, v7, v9
	v_mov_b32_e32 v29, 0
	v_mov_b32_e32 v30, 0
	v_mov_b32_e32 v31, 0
	v_cvt_pk_fp8_f32 v29, v14, v18
	v_cvt_pk_fp8_f32 v30, v20, v24
	v_cvt_pk_fp8_f32 v31, v46, v50
	v_mov_b32_e32 v32, 0
	v_mov_b32_e32 v33, 0
	v_mov_b32_e32 v34, 0
	v_mov_b32_e32 v35, 0
	v_cvt_pk_fp8_f32 v28, v2, v4 op_sel:[0,0,1]
	v_cvt_pk_fp8_f32 v32, v62, v66
	v_cvt_pk_fp8_f32 v33, v78, v82
	v_cvt_pk_fp8_f32 v34, v94, v98
	v_cvt_pk_fp8_f32 v35, v114, v126
	v_mov_b32_e32 v7, 0
	v_mov_b32_e32 v8, 0
	v_mov_b32_e32 v9, 0
	v_cvt_pk_fp8_f32 v6, v3, v5 op_sel:[0,0,1]
	v_mov_b32_e32 v2, 0
	v_mov_b32_e32 v3, 0
	v_mov_b32_e32 v4, 0
	v_mov_b32_e32 v5, 0
	v_cvt_pk_fp8_f32 v7, v15, v19
	v_cvt_pk_fp8_f32 v8, v21, v25
	v_cvt_pk_fp8_f32 v9, v47, v51
	v_cvt_pk_fp8_f32 v2, v63, v67
	v_cvt_pk_fp8_f32 v3, v79, v83
	v_cvt_pk_fp8_f32 v4, v95, v99
	v_cvt_pk_fp8_f32 v5, v115, v127
	v_cvt_pk_fp8_f32 v29, v12, v16 op_sel:[0,0,1]
	v_cvt_pk_fp8_f32 v30, v22, v26 op_sel:[0,0,1]
	v_cvt_pk_fp8_f32 v31, v54, v58 op_sel:[0,0,1]
	v_cvt_pk_fp8_f32 v32, v70, v74 op_sel:[0,0,1]
	v_cvt_pk_fp8_f32 v33, v86, v90 op_sel:[0,0,1]
	v_cvt_pk_fp8_f32 v34, v102, v106 op_sel:[0,0,1]
	v_cvt_pk_fp8_f32 v35, v130, v134 op_sel:[0,0,1]
	v_add_u32_e32 v10, 0xfffeffff, v123
	v_cvt_pk_fp8_f32 v7, v13, v17 op_sel:[0,0,1]
	v_cvt_pk_fp8_f32 v8, v23, v27 op_sel:[0,0,1]
	v_cvt_pk_fp8_f32 v9, v55, v59 op_sel:[0,0,1]
	v_cvt_pk_fp8_f32 v2, v71, v75 op_sel:[0,0,1]
	v_cvt_pk_fp8_f32 v3, v87, v91 op_sel:[0,0,1]
	v_cvt_pk_fp8_f32 v4, v103, v107 op_sel:[0,0,1]
	v_cvt_pk_fp8_f32 v5, v131, v135 op_sel:[0,0,1]
	v_mad_i64_i32 v[10:11], s[0:1], v10, s61, v[108:109]
	global_store_dwordx4 v[10:11], v[28:31], off
	global_store_dwordx4 v[10:11], v[32:35], off offset:16
	v_add_u32_e32 v10, 0xffff0000, v123
	v_mad_i64_i32 v[72:73], s[0:1], v10, s61, v[108:109]
	global_store_dwordx4 v[72:73], v[6:9], off

; __device__ __forceinline__ unsigned pk4_fp8(float a, float b, float c, float d) { int w = 0; w = __builtin_amdgcn_cvt_pk_fp8_f32(a, b, w, false); w = __builtin_amdgcn_cvt_pk_fp8_f32(c, d, w, true); return (unsigned)w; }
; template <int MODE, int KL>
; __device__ __forceinline__ void p0_cvt_item(const float* W, int K, int N, unsigned char* WT, int il, int which, int item, int lane, const float* gk, float scale, int ldk, int koff) {
;     const int nblk = N >> 6, kb = item / nblk, nb = item - kb * nblk, nq = lane & 15, kr = lane >> 4, k0 = 4 * KL * kb + KL * kr, n0 = 64 * nb + 4 * nq;
;     const GAS f32x4* src = (const GAS f32x4*)(W + (size_t)k0 * N + n0);
;     f32x4 v[KL];
; #pragma unroll
;     for (int i = 0; i < KL; ++i) v[i] = src[(size_t)i * (N >> 2)];
;     if (MODE == 1) {
; #pragma unroll
;         for (int q = 0; q < KL / 4; ++q) { const f32x4 g = *(const GAS f32x4*)(gk + k0 + 4 * q); v[4 * q] *= g.x; v[4 * q + 1] *= g.y; v[4 * q + 2] *= g.z; v[4 * q + 3] *= g.w; } }
;     if (MODE == 2) {
; #pragma unroll
;         for (int i = 0; i < KL; ++i) v[i] *= scale; }
; #pragma unroll
;     for (int c = 0; c < 4; ++c) { const int n = n0 + c, row = il ? ((n >> 4) * 32 + which * 16 + (n & 15)) : n;
;         if (MODE == 2) { GAS v4u* dst = (GAS v4u*)(WT + (size_t)row * ldk + koff + k0);
; #pragma unroll
;             for (int q = 0; q < KL / 16; ++q) { v4u o;
;                 o.x = pg8::pk4_fp8(v[16 * q][c], v[16 * q + 1][c], v[16 * q + 2][c], v[16 * q + 3][c]);     o.y = pg8::pk4_fp8(v[16 * q + 4][c], v[16 * q + 5][c], v[16 * q + 6][c], v[16 * q + 7][c]);
;                 o.z = pg8::pk4_fp8(v[16 * q + 8][c], v[16 * q + 9][c], v[16 * q + 10][c], v[16 * q + 11][c]); o.w = pg8::pk4_fp8(v[16 * q + 12][c], v[16 * q + 13][c], v[16 * q + 14][c], v[16 * q + 15][c]);
;                 dst[q] = o; } }
; __device__ __forceinline__ void moe_cvt_tile(const Args& a, int set, int id, int lane) {
;     const int j = id / MT_PER, item = id - j * MT_PER;
;     if (j < 16) { const int e = set * 8 + (j & 7), wh = j >> 3;
;         p0_cvt_item<2, 32>(a.in[17 + wh] + (size_t)e * D * FE, D, FE, a.ws + W_13M + (size_t)e * 2 * FE * D, 1, wh, item, lane, nullptr, 32.f, D, 0); }
;     else { const int e = set * 8 + (j - 16); p0_cvt_item<2, 32>(a.in[19] + (size_t)e * FE * D, FE, D, a.ws + W_2M + (size_t)e * D * FE, 0, 0, item, lane, nullptr, 64.f, FE, 0); }
; }
.LBB0_49:
	s_andn2_b64 vcc, exec, s[0:1]
	s_cbranch_vccnz .LBB0_17
	s_add_i32 s10, s80, 0x1800
	s_mul_hi_i32 s0, s10, 0x92492493
	s_add_i32 s0, s0, s10
	s_lshr_b32 s1, s0, 31
	s_ashr_i32 s2, s0, 8
	s_add_i32 s2, s2, s1
	s_mul_i32 s0, s2, 0xfffffe40
	s_add_i32 s10, s10, s0
	s_cmpk_gt_i32 s80, 0x3ff
	s_mov_b64 s[0:1], -1
	s_cbranch_scc0 .LBB0_52
	s_load_dwordx2 s[0:1], s[92:93], 0x98
	s_add_i32 s11, s2, -16
	s_mul_i32 s8, s11, 0xe00000
	s_mul_hi_i32 s9, s11, 0xe00000
	s_mul_hi_i32 s12, s11, 0x380000
	s_waitcnt lgkmcnt(0)
	s_add_u32 s8, s0, s8
	s_addc_u32 s9, s1, s9
	s_mul_i32 s11, s11, 0x380000
	s_add_u32 s0, s34, s11
	s_addc_u32 s1, s35, s12
	s_ashr_i32 s11, s10, 31
	s_lshr_b32 s11, s11, 28
	s_add_i32 s11, s10, s11
	s_ashr_i32 s11, s11, 4
	v_lshl_or_b32 v114, s11, 7, v121
	s_lshl_b32 s11, s11, 10
	s_mul_i32 s12, s2, 0x7000
	s_add_i32 s11, s11, s12
	v_subrev_u32_e32 v123, s11, v122
	v_ashrrev_i32_e32 v115, 31, v114
	v_add_u32_e32 v112, -3, v123
	v_lshlrev_b64 v[2:3], 12, v[114:115]
	v_lshl_add_u64 v[2:3], s[8:9], 0, v[2:3]
	v_ashrrev_i32_e32 v113, 31, v112
	v_lshl_add_u64 v[116:117], v[112:113], 2, v[2:3]
	v_add_co_u32_e32 v10, vcc, s44, v116
	global_load_dwordx4 v[2:5], v[116:117], off nt
	s_nop 0
	v_addc_co_u32_e32 v11, vcc, 0, v117, vcc
	v_add_co_u32_e32 v18, vcc, s45, v116
	global_load_dwordx4 v[6:9], v[10:11], off offset:-4096 nt
	s_nop 0
	global_load_dwordx4 v[10:13], v[10:11], off nt
	v_addc_co_u32_e32 v19, vcc, 0, v117, vcc
	v_add_co_u32_e32 v26, vcc, s46, v116
	global_load_dwordx4 v[14:17], v[18:19], off offset:-4096 nt
	s_nop 0
	global_load_dwordx4 v[18:21], v[18:19], off nt
	v_addc_co_u32_e32 v27, vcc, 0, v117, vcc
	v_add_co_u32_e32 v34, vcc, s47, v116
	global_load_dwordx4 v[22:25], v[26:27], off offset:-4096 nt
	s_nop 0
	global_load_dwordx4 v[26:29], v[26:27], off nt
	v_addc_co_u32_e32 v35, vcc, 0, v117, vcc
	v_add_co_u32_e32 v42, vcc, s48, v116
	global_load_dwordx4 v[30:33], v[34:35], off offset:-4096 nt
	s_nop 0
	global_load_dwordx4 v[34:37], v[34:35], off nt
	v_addc_co_u32_e32 v43, vcc, 0, v117, vcc
	v_add_co_u32_e32 v50, vcc, s49, v116
	global_load_dwordx4 v[38:41], v[42:43], off offset:-4096 nt
	s_nop 0
	global_load_dwordx4 v[42:45], v[42:43], off nt
	v_addc_co_u32_e32 v51, vcc, 0, v117, vcc
	v_add_co_u32_e32 v58, vcc, s50, v116
	global_load_dwordx4 v[46:49], v[50:51], off offset:-4096 nt
	s_nop 0
	global_load_dwordx4 v[50:53], v[50:51], off nt
	v_addc_co_u32_e32 v59, vcc, 0, v117, vcc
	v_add_co_u32_e32 v66, vcc, s51, v116
	global_load_dwordx4 v[54:57], v[58:59], off offset:-4096 nt
	s_nop 0
	global_load_dwordx4 v[58:61], v[58:59], off nt
	v_addc_co_u32_e32 v67, vcc, 0, v117, vcc
	v_add_co_u32_e32 v74, vcc, s52, v116
	global_load_dwordx4 v[62:65], v[66:67], off offset:-4096 nt
	s_nop 0
	global_load_dwordx4 v[66:69], v[66:67], off nt
	v_addc_co_u32_e32 v75, vcc, 0, v117, vcc
	v_add_co_u32_e32 v82, vcc, s53, v116
	global_load_dwordx4 v[70:73], v[74:75], off offset:-4096 nt
	s_nop 0
	global_load_dwordx4 v[74:77], v[74:75], off nt
	v_addc_co_u32_e32 v83, vcc, 0, v117, vcc
	v_add_co_u32_e32 v90, vcc, s54, v116
	global_load_dwordx4 v[78:81], v[82:83], off offset:-4096 nt
	s_nop 0
	global_load_dwordx4 v[82:85], v[82:83], off nt
	v_addc_co_u32_e32 v91, vcc, 0, v117, vcc
	v_add_co_u32_e32 v98, vcc, s55, v116
	global_load_dwordx4 v[86:89], v[90:91], off offset:-4096 nt
	s_nop 0
	global_load_dwordx4 v[90:93], v[90:91], off nt
	v_addc_co_u32_e32 v99, vcc, 0, v117, vcc
	v_add_co_u32_e32 v106, vcc, s56, v116
	global_load_dwordx4 v[94:97], v[98:99], off offset:-4096 nt
	s_nop 0
	global_load_dwordx4 v[98:101], v[98:99], off nt
	v_addc_co_u32_e32 v107, vcc, 0, v117, vcc
	v_add_co_u32_e32 v128, vcc, s57, v116
	global_load_dwordx4 v[102:105], v[106:107], off offset:-4096 nt
	s_nop 0
	global_load_dwordx4 v[106:109], v[106:107], off nt
	v_addc_co_u32_e32 v129, vcc, 0, v117, vcc
	v_add_co_u32_e32 v136, vcc, s58, v116
	v_lshl_add_u64 v[148:149], s[0:1], 0, v[114:115]
	s_nop 0
	v_addc_co_u32_e32 v137, vcc, 0, v117, vcc
	global_load_dwordx4 v[124:127], v[128:129], off offset:-4096 nt
	s_nop 0
	global_load_dwordx4 v[128:131], v[128:129], off nt
	s_nop 0
	global_load_dwordx4 v[132:135], v[136:137], off offset:-4096 nt
	v_add_co_u32_e32 v116, vcc, s60, v116
	v_mov_b32_e32 v114, 0
	s_nop 0
	v_addc_co_u32_e32 v117, vcc, 0, v117, vcc
	global_load_dwordx4 v[136:139], v[136:137], off nt
	s_nop 0
	global_load_dwordx4 v[140:143], v[116:117], off nt
	s_waitcnt vmcnt(31)
	v_pk_mul_f32 v[2:3], v[2:3], s[4:5] op_sel_hi:[1,0]
	v_mov_b32_e32 v115, 0
	v_mov_b32_e32 v116, 0
	v_mov_b32_e32 v117, 0
	s_waitcnt vmcnt(30)
	v_pk_mul_f32 v[6:7], v[6:7], s[4:5] op_sel_hi:[1,0]
	v_mov_b32_e32 v144, 0
	v_cvt_pk_fp8_f32 v114, v2, v6
	v_mov_b32_e32 v145, 0
	v_mov_b32_e32 v146, 0
	v_mov_b32_e32 v147, 0
	s_waitcnt vmcnt(27)
	v_pk_mul_f32 v[18:19], v[18:19], s[4:5] op_sel_hi:[1,0]
	v_pk_mul_f32 v[10:11], v[10:11], s[4:5] op_sel_hi:[1,0]
	v_pk_mul_f32 v[14:15], v[14:15], s[4:5] op_sel_hi:[1,0]
	v_mad_i64_i32 v[112:113], s[0:1], v112, s61, v[148:149]
	s_waitcnt vmcnt(26)
	v_pk_mul_f32 v[22:23], v[22:23], s[4:5] op_sel_hi:[1,0]
	s_waitcnt vmcnt(25)
	v_pk_mul_f32 v[26:27], v[26:27], s[4:5] op_sel_hi:[1,0]
	v_cvt_pk_fp8_f32 v115, v18, v22
	v_cvt_pk_fp8_f32 v114, v10, v14 op_sel:[0,0,1]
	s_waitcnt vmcnt(24)
	v_pk_mul_f32 v[30:31], v[30:31], s[4:5] op_sel_hi:[1,0]
	s_waitcnt vmcnt(23)
	v_pk_mul_f32 v[34:35], v[34:35], s[4:5] op_sel_hi:[1,0]
	v_cvt_pk_fp8_f32 v115, v26, v30 op_sel:[0,0,1]
	v_pk_mul_f32 v[36:37], v[36:37], s[4:5] op_sel_hi:[1,0]
	v_add_u32_e32 v2, -2, v123
	s_waitcnt vmcnt(22)
	v_pk_mul_f32 v[38:39], v[38:39], s[4:5] op_sel_hi:[1,0]
	s_waitcnt vmcnt(21)
; __device__ __forceinline__ unsigned pk4_fp8(float a, float b, float c, float d) { int w = 0; w = __builtin_amdgcn_cvt_pk_fp8_f32(a, b, w, false); w = __builtin_amdgcn_cvt_pk_fp8_f32(c, d, w, true); return (unsigned)w; }
; #define GAS __attribute__((address_space(1)))
; template <int MODE, int KL>
; __device__ __forceinline__ void p0_cvt_item(const float* W, int K, int N, unsigned char* WT, int il, int which, int item, int lane, const float* gk, float scale, int ldk, int koff) {
;     ...
; #pragma unroll
;     for (int c = 0; c < 4; ++c) { const int n = n0 + c, row = il ? ((n >> 4) * 32 + which * 16 + (n & 15)) : n;
;         if (MODE == 2) { GAS v4u* dst = (GAS v4u*)(WT + (size_t)row * ldk + koff + k0);
; #pragma unroll
;             for (int q = 0; q < KL / 16; ++q) { v4u o;
;                 o.x = pg8::pk4_fp8(v[16 * q][c], v[16 * q + 1][c], v[16 * q + 2][c], v[16 * q + 3][c]);     o.y = pg8::pk4_fp8(v[16 * q + 4][c], v[16 * q + 5][c], v[16 * q + 6][c], v[16 * q + 7][c]);
;                 o.z = pg8::pk4_fp8(v[16 * q + 8][c], v[16 * q + 9][c], v[16 * q + 10][c], v[16 * q + 11][c]); o.w = pg8::pk4_fp8(v[16 * q + 12][c], v[16 * q + 13][c], v[16 * q + 14][c], v[16 * q + 15][c]);
;                 dst[q] = o; } }
	v_pk_mul_f32 v[42:43], v[42:43], s[4:5] op_sel_hi:[1,0]
	v_cvt_pk_fp8_f32 v116, v34, v38
	s_waitcnt vmcnt(20)
	v_pk_mul_f32 v[46:47], v[46:47], s[4:5] op_sel_hi:[1,0]
	s_waitcnt vmcnt(19)
	v_pk_mul_f32 v[50:51], v[50:51], s[4:5] op_sel_hi:[1,0]
	v_cvt_pk_fp8_f32 v116, v42, v46 op_sel:[0,0,1]
	s_waitcnt vmcnt(18)
	v_pk_mul_f32 v[54:55], v[54:55], s[4:5] op_sel_hi:[1,0]
	s_nop 0
	v_cvt_pk_fp8_f32 v117, v50, v54
	s_waitcnt vmcnt(17)
	v_pk_mul_f32 v[58:59], v[58:59], s[4:5] op_sel_hi:[1,0]
	s_waitcnt vmcnt(16)
	v_pk_mul_f32 v[62:63], v[62:63], s[4:5] op_sel_hi:[1,0]
	s_waitcnt vmcnt(15)
	v_pk_mul_f32 v[66:67], v[66:67], s[4:5] op_sel_hi:[1,0]
	v_cvt_pk_fp8_f32 v117, v58, v62 op_sel:[0,0,1]
	s_waitcnt vmcnt(14)
	v_pk_mul_f32 v[70:71], v[70:71], s[4:5] op_sel_hi:[1,0]
	s_waitcnt vmcnt(13)
	v_pk_mul_f32 v[150:151], v[74:75], s[4:5] op_sel_hi:[1,0]
	v_cvt_pk_fp8_f32 v144, v66, v70
	s_waitcnt vmcnt(12)
	v_pk_mul_f32 v[152:153], v[78:79], s[4:5] op_sel_hi:[1,0]
	s_waitcnt vmcnt(11)
	v_pk_mul_f32 v[82:83], v[82:83], s[4:5] op_sel_hi:[1,0]
	v_cvt_pk_fp8_f32 v144, v150, v152 op_sel:[0,0,1]
	s_waitcnt vmcnt(10)
	v_pk_mul_f32 v[86:87], v[86:87], s[4:5] op_sel_hi:[1,0]
	s_nop 0
	v_cvt_pk_fp8_f32 v145, v82, v86
	s_waitcnt vmcnt(9)
	v_pk_mul_f32 v[90:91], v[90:91], s[4:5] op_sel_hi:[1,0]
	v_mov_b32_e32 v82, 0
	s_waitcnt vmcnt(8)
	v_pk_mul_f32 v[94:95], v[94:95], s[4:5] op_sel_hi:[1,0]
	s_waitcnt vmcnt(7)
	v_pk_mul_f32 v[74:75], v[98:99], s[4:5] op_sel_hi:[1,0]
	v_cvt_pk_fp8_f32 v145, v90, v94 op_sel:[0,0,1]
	v_mov_b32_e32 v90, 0
	s_waitcnt vmcnt(6)
	v_pk_mul_f32 v[78:79], v[102:103], s[4:5] op_sel_hi:[1,0]
	s_nop 0
	v_cvt_pk_fp8_f32 v146, v74, v78
	s_waitcnt vmcnt(5)
	v_pk_mul_f32 v[106:107], v[106:107], s[4:5] op_sel_hi:[1,0]
	s_waitcnt vmcnt(4)
	v_pk_mul_f32 v[124:125], v[124:125], s[4:5] op_sel_hi:[1,0]
	s_waitcnt vmcnt(3)
	v_pk_mul_f32 v[98:99], v[128:129], s[4:5] op_sel_hi:[1,0]
	s_waitcnt vmcnt(2)
	v_pk_mul_f32 v[102:103], v[132:133], s[4:5] op_sel_hi:[1,0]
	v_cvt_pk_fp8_f32 v146, v106, v124 op_sel:[0,0,1]
	v_cvt_pk_fp8_f32 v147, v98, v102
	s_waitcnt vmcnt(1)
	v_pk_mul_f32 v[128:129], v[136:137], s[4:5] op_sel_hi:[1,0]
	s_waitcnt vmcnt(0)
	v_pk_mul_f32 v[132:133], v[140:141], s[4:5] op_sel_hi:[1,0]
	s_nop 0
	v_cvt_pk_fp8_f32 v147, v128, v132 op_sel:[0,0,1]
	global_store_dwordx4 v[112:113], v[114:117], off
	global_store_dwordx4 v[112:113], v[144:147], off offset:16
	v_mov_b32_e32 v113, 0
	v_mov_b32_e32 v114, 0
	v_cvt_pk_fp8_f32 v113, v19, v23
	v_cvt_pk_fp8_f32 v114, v35, v39
	v_mov_b32_e32 v145, 0
	v_cvt_pk_fp8_f32 v145, v83, v87
	v_mov_b32_e32 v112, 0
	v_mov_b32_e32 v115, 0
	v_cvt_pk_fp8_f32 v112, v3, v7
	v_cvt_pk_fp8_f32 v115, v51, v55
	v_mov_b32_e32 v144, 0
	v_mov_b32_e32 v146, 0
	v_mov_b32_e32 v147, 0
	v_cvt_pk_fp8_f32 v113, v27, v31 op_sel:[0,0,1]
	v_cvt_pk_fp8_f32 v114, v43, v47 op_sel:[0,0,1]
	v_cvt_pk_fp8_f32 v144, v67, v71
	v_cvt_pk_fp8_f32 v146, v75, v79
	v_pk_mul_f32 v[30:31], v[4:5], s[4:5] op_sel_hi:[1,0]
	v_pk_mul_f32 v[42:43], v[8:9], s[4:5] op_sel_hi:[1,0]
	v_pk_mul_f32 v[34:35], v[20:21], s[4:5] op_sel_hi:[1,0]
	v_pk_mul_f32 v[46:47], v[24:25], s[4:5] op_sel_hi:[1,0]
	v_pk_mul_f32 v[50:51], v[40:41], s[4:5] op_sel_hi:[1,0]
	v_pk_mul_f32 v[38:39], v[52:53], s[4:5] op_sel_hi:[1,0]
	v_pk_mul_f32 v[52:53], v[56:57], s[4:5] op_sel_hi:[1,0]
	v_pk_mul_f32 v[66:67], v[84:85], s[4:5] op_sel_hi:[1,0]
	v_cvt_pk_fp8_f32 v147, v99, v103
	v_mov_b32_e32 v83, 0
	v_mov_b32_e32 v84, 0
	v_mov_b32_e32 v85, 0
	v_pk_mul_f32 v[86:87], v[68:69], s[4:5] op_sel_hi:[1,0]
	v_pk_mul_f32 v[74:75], v[72:73], s[4:5] op_sel_hi:[1,0]
	v_pk_mul_f32 v[18:19], v[76:77], s[4:5] op_sel_hi:[1,0]
	v_pk_mul_f32 v[24:25], v[80:81], s[4:5] op_sel_hi:[1,0]
	v_pk_mul_f32 v[76:77], v[88:89], s[4:5] op_sel_hi:[1,0]
	v_pk_mul_f32 v[68:69], v[100:101], s[4:5] op_sel_hi:[1,0]
	v_pk_mul_f32 v[78:79], v[104:105], s[4:5] op_sel_hi:[1,0]
	v_pk_mul_f32 v[70:71], v[130:131], s[4:5] op_sel_hi:[1,0]
	v_pk_mul_f32 v[80:81], v[134:135], s[4:5] op_sel_hi:[1,0]
	v_cvt_pk_fp8_f32 v145, v91, v95 op_sel:[0,0,1]
	v_cvt_pk_fp8_f32 v82, v30, v42
	v_cvt_pk_fp8_f32 v83, v34, v46
	v_cvt_pk_fp8_f32 v84, v36, v50
	v_cvt_pk_fp8_f32 v85, v38, v52
	v_mov_b32_e32 v88, 0
	v_mov_b32_e32 v89, 0
	v_mov_b32_e32 v91, 0
	v_cvt_pk_fp8_f32 v88, v86, v74
	v_cvt_pk_fp8_f32 v89, v66, v76
	v_cvt_pk_fp8_f32 v90, v68, v78
	v_cvt_pk_fp8_f32 v91, v70, v80
	v_cvt_pk_fp8_f32 v112, v11, v15 op_sel:[0,0,1]
	v_cvt_pk_fp8_f32 v115, v59, v63 op_sel:[0,0,1]
	v_pk_mul_f32 v[4:5], v[12:13], s[4:5] op_sel_hi:[1,0]
	v_pk_mul_f32 v[6:7], v[16:17], s[4:5] op_sel_hi:[1,0]
	v_pk_mul_f32 v[8:9], v[28:29], s[4:5] op_sel_hi:[1,0]
	v_pk_mul_f32 v[10:11], v[32:33], s[4:5] op_sel_hi:[1,0]
	v_pk_mul_f32 v[12:13], v[44:45], s[4:5] op_sel_hi:[1,0]
	v_pk_mul_f32 v[14:15], v[48:49], s[4:5] op_sel_hi:[1,0]
	v_pk_mul_f32 v[16:17], v[60:61], s[4:5] op_sel_hi:[1,0]
	v_pk_mul_f32 v[22:23], v[64:65], s[4:5] op_sel_hi:[1,0]
	v_cvt_pk_fp8_f32 v144, v151, v153 op_sel:[0,0,1]
	v_cvt_pk_fp8_f32 v146, v107, v125 op_sel:[0,0,1]
	v_cvt_pk_fp8_f32 v147, v129, v133 op_sel:[0,0,1]
	v_pk_mul_f32 v[26:27], v[92:93], s[4:5] op_sel_hi:[1,0]
	v_pk_mul_f32 v[54:55], v[96:97], s[4:5] op_sel_hi:[1,0]
	v_pk_mul_f32 v[56:57], v[108:109], s[4:5] op_sel_hi:[1,0]
	v_pk_mul_f32 v[58:59], v[126:127], s[4:5] op_sel_hi:[1,0]
	v_pk_mul_f32 v[60:61], v[138:139], s[4:5] op_sel_hi:[1,0]
	v_pk_mul_f32 v[62:63], v[142:143], s[4:5] op_sel_hi:[1,0]
	v_cvt_pk_fp8_f32 v82, v4, v6 op_sel:[0,0,1]
	v_cvt_pk_fp8_f32 v83, v8, v10 op_sel:[0,0,1]
	v_cvt_pk_fp8_f32 v84, v12, v14 op_sel:[0,0,1]
	v_cvt_pk_fp8_f32 v85, v16, v22 op_sel:[0,0,1]
	v_mad_i64_i32 v[2:3], s[0:1], v2, s61, v[148:149]
	v_cvt_pk_fp8_f32 v88, v18, v24 op_sel:[0,0,1]
	v_cvt_pk_fp8_f32 v89, v26, v54 op_sel:[0,0,1]
	v_cvt_pk_fp8_f32 v90, v56, v58 op_sel:[0,0,1]
	v_cvt_pk_fp8_f32 v91, v60, v62 op_sel:[0,0,1]
	global_store_dwordx4 v[2:3], v[112:115], off
	global_store_dwordx4 v[2:3], v[144:147], off offset:16
	v_add_u32_e32 v2, -1, v123
	v_mad_i64_i32 v[2:3], s[0:1], v2, s61, v[148:149]
	v_mad_i64_i32 v[72:73], s[0:1], v123, s61, v[148:149]
	global_store_dwordx4 v[2:3], v[82:85], off
	global_store_dwordx4 v[2:3], v[88:91], off offset:16
	s_mov_b64 s[0:1], 0
; __device__ __forceinline__ unsigned pk4_fp8(float a, float b, float c, float d) { int w = 0; w = __builtin_amdgcn_cvt_pk_fp8_f32(a, b, w, false); w = __builtin_amdgcn_cvt_pk_fp8_f32(c, d, w, true); return (unsigned)w; }
; template <int MODE, int KL>
; __device__ __forceinline__ void p0_cvt_item(const float* W, int K, int N, unsigned char* WT, int il, int which, int item, int lane, const float* gk, float scale, int ldk, int koff) {
;     const int nblk = N >> 6, kb = item / nblk, nb = item - kb * nblk, nq = lane & 15, kr = lane >> 4, k0 = 4 * KL * kb + KL * kr, n0 = 64 * nb + 4 * nq;
;     const GAS f32x4* src = (const GAS f32x4*)(W + (size_t)k0 * N + n0);
;     f32x4 v[KL];
; #pragma unroll
;     for (int i = 0; i < KL; ++i) v[i] = src[(size_t)i * (N >> 2)];
;     if (MODE == 1) {
; #pragma unroll
;         for (int q = 0; q < KL / 4; ++q) { const f32x4 g = *(const GAS f32x4*)(gk + k0 + 4 * q); v[4 * q] *= g.x; v[4 * q + 1] *= g.y; v[4 * q + 2] *= g.z; v[4 * q + 3] *= g.w; } }
;     if (MODE == 2) {
; #pragma unroll
;         for (int i = 0; i < KL; ++i) v[i] *= scale; }
; #pragma unroll
;     for (int c = 0; c < 4; ++c) { const int n = n0 + c, row = il ? ((n >> 4) * 32 + which * 16 + (n & 15)) : n;
;         if (MODE == 2) { GAS v4u* dst = (GAS v4u*)(WT + (size_t)row * ldk + koff + k0);
; #pragma unroll
;             for (int q = 0; q < KL / 16; ++q) { v4u o;
;                 o.x = pg8::pk4_fp8(v[16 * q][c], v[16 * q + 1][c], v[16 * q + 2][c], v[16 * q + 3][c]);     o.y = pg8::pk4_fp8(v[16 * q + 4][c], v[16 * q + 5][c], v[16 * q + 6][c], v[16 * q + 7][c]);
;                 o.z = pg8::pk4_fp8(v[16 * q + 8][c], v[16 * q + 9][c], v[16 * q + 10][c], v[16 * q + 11][c]); o.w = pg8::pk4_fp8(v[16 * q + 12][c], v[16 * q + 13][c], v[16 * q + 14][c], v[16 * q + 15][c]);
;                 dst[q] = o; } }
; __device__ __forceinline__ void moe_cvt_tile(const Args& a, int set, int id, int lane) {
;     const int j = id / MT_PER, item = id - j * MT_PER;
;     if (j < 16) { const int e = set * 8 + (j & 7), wh = j >> 3;
;         p0_cvt_item<2, 32>(a.in[17 + wh] + (size_t)e * D * FE, D, FE, a.ws + W_13M + (size_t)e * 2 * FE * D, 1, wh, item, lane, nullptr, 32.f, D, 0); }
;     else { const int e = set * 8 + (j - 16); p0_cvt_item<2, 32>(a.in[19] + (size_t)e * FE * D, FE, D, a.ws + W_2M + (size_t)e * D * FE, 0, 0, item, lane, nullptr, 64.f, FE, 0); }
; }
.LBB0_52:
	s_andn2_b64 vcc, exec, s[0:1]
	s_cbranch_vccnz .LBB0_16
	s_ashr_i32 s0, s2, 3
	s_ashr_i32 s1, s0, 31
	s_and_b32 s11, s2, 7
	s_lshl_b64 s[8:9], s[0:1], 3
	s_mov_b64 s[12:13], s[92:93]
	s_add_u32 s8, s12, s8
	s_addc_u32 s9, s13, s9
	s_load_dwordx2 s[8:9], s[8:9], 0x88
	s_mul_i32 s12, s11, 0xe00000
	s_mul_i32 s11, s11, 0x700000
	s_mul_hi_i32 s1, s10, 0x92492493
	s_mulk_i32 s2, 0x1c0
	s_waitcnt lgkmcnt(0)
	s_add_u32 s12, s8, s12
	s_addc_u32 s13, s9, 0
	s_add_u32 s8, s36, s11
	s_addc_u32 s9, s37, 0
	s_add_i32 s1, s1, s10
	s_lshr_b32 s10, s1, 31
	s_ashr_i32 s1, s1, 5
	s_add_i32 s1, s1, s10
	s_mul_i32 s10, s1, 0xffffffc8
	s_sub_i32 s2, s10, s2
	s_add_i32 s2, s80, s2
	s_lshl_b32 s2, s2, 6
	s_add_i32 s2, s2, 0x60000
	v_lshl_or_b32 v2, s1, 7, v121
	v_or_b32_e32 v4, s2, v119
	v_mov_b64_e32 v[6:7], s[12:13]
	s_movk_i32 s1, 0x3800
	v_mad_i64_i32 v[6:7], s[10:11], v2, s1, v[6:7]
	v_ashrrev_i32_e32 v5, 31, v4
	v_lshl_add_u64 v[6:7], v[4:5], 2, v[6:7]
	s_movk_i32 s1, 0x3000
	v_add_co_u32_e32 v8, vcc, s1, v6
	s_movk_i32 s1, 0x7000
	s_nop 0
	v_addc_co_u32_e32 v9, vcc, 0, v7, vcc
	v_add_co_u32_e32 v10, vcc, s1, v6
	s_mov_b32 s1, 0x11000
	s_nop 0
	v_addc_co_u32_e32 v11, vcc, 0, v7, vcc
	v_add_co_u32_e32 v14, vcc, s48, v6
	v_lshlrev_b32_e32 v4, 1, v4
	s_nop 0
	v_addc_co_u32_e32 v15, vcc, 0, v7, vcc
	v_add_co_u32_e32 v12, vcc, s50, v6
	global_load_dwordx4 v[58:61], v[6:7], off nt
	global_load_dwordx4 v[62:65], v[8:9], off offset:2048 nt
	s_nop 0
	global_load_dwordx4 v[8:11], v[10:11], off nt
	s_nop 0
	global_load_dwordx4 v[66:69], v[14:15], off offset:2048 nt
	v_addc_co_u32_e32 v13, vcc, 0, v7, vcc
	v_add_co_u32_e32 v16, vcc, s1, v6
	s_mov_b32 s1, 0x15000
	s_nop 0
	v_addc_co_u32_e32 v17, vcc, 0, v7, vcc
	v_add_co_u32_e32 v18, vcc, s1, v6
	s_mov_b32 s1, 0x23000
	s_nop 0
	v_addc_co_u32_e32 v19, vcc, 0, v7, vcc
	v_add_co_u32_e32 v22, vcc, s55, v6
	v_and_b32_e32 v4, 0xffffffe0, v4
	s_nop 0
	v_addc_co_u32_e32 v23, vcc, 0, v7, vcc
	v_add_co_u32_e32 v20, vcc, s57, v6
	global_load_dwordx4 v[12:15], v[12:13], off nt
	s_nop 0
	global_load_dwordx4 v[70:73], v[16:17], off offset:2048 nt
	s_nop 0
	global_load_dwordx4 v[16:19], v[18:19], off nt
	s_nop 0
	global_load_dwordx4 v[74:77], v[22:23], off offset:2048 nt
	v_addc_co_u32_e32 v21, vcc, 0, v7, vcc
	v_add_co_u32_e32 v24, vcc, s60, v6
	v_ashrrev_i32_e32 v3, 31, v2
	s_nop 0
	v_addc_co_u32_e32 v25, vcc, 0, v7, vcc
	v_add_co_u32_e32 v26, vcc, s1, v6
	s_mov_b32 s1, 0x26000
	s_nop 0
	v_addc_co_u32_e32 v27, vcc, 0, v7, vcc
	v_add_co_u32_e32 v28, vcc, s1, v6
	s_mov_b32 s1, 0x2a000
	s_nop 0
	v_addc_co_u32_e32 v29, vcc, 0, v7, vcc
	v_add_co_u32_e32 v30, vcc, s1, v6
	s_mov_b32 s1, 0x2d000
	s_nop 0
	v_addc_co_u32_e32 v31, vcc, 0, v7, vcc
	v_add_co_u32_e32 v32, vcc, s1, v6
	s_mov_b32 s1, 0x31000
	s_nop 0
	v_addc_co_u32_e32 v33, vcc, 0, v7, vcc
	v_add_co_u32_e32 v34, vcc, s1, v6
	s_mov_b32 s1, 0x34000
	s_nop 0
	v_addc_co_u32_e32 v35, vcc, 0, v7, vcc
	v_add_co_u32_e32 v36, vcc, s1, v6
	global_load_dwordx4 v[20:23], v[20:21], off nt
	s_nop 0
	global_load_dwordx4 v[78:81], v[24:25], off offset:2048 nt
	s_nop 0
	global_load_dwordx4 v[24:27], v[26:27], off nt
	s_nop 0
	global_load_dwordx4 v[82:85], v[28:29], off offset:2048 nt
	global_load_dwordx4 v[86:89], v[30:31], off nt
	s_nop 0
	global_load_dwordx4 v[30:33], v[32:33], off offset:2048 nt
	v_addc_co_u32_e32 v37, vcc, 0, v7, vcc
	v_add_co_u32_e32 v38, vcc, s62, v6
	v_lshl_add_u32 v4, s0, 4, v4
	s_nop 0
	v_addc_co_u32_e32 v39, vcc, 0, v7, vcc
	v_add_co_u32_e32 v40, vcc, s63, v6
	v_mov_b32_e32 v5, 0
	s_nop 0
	v_addc_co_u32_e32 v41, vcc, 0, v7, vcc
	v_add_co_u32_e32 v42, vcc, s66, v6
	global_load_dwordx4 v[90:93], v[34:35], off nt
	global_load_dwordx4 v[94:97], v[36:37], off offset:2048 nt
	global_load_dwordx4 v[98:101], v[38:39], off nt
	s_nop 0
	global_load_dwordx4 v[38:41], v[40:41], off offset:2048 nt
	v_addc_co_u32_e32 v43, vcc, 0, v7, vcc
	v_add_co_u32_e32 v44, vcc, s67, v6
	s_waitcnt vmcnt(13)
	v_pk_mul_f32 v[12:13], v[12:13], s[6:7] op_sel_hi:[1,0]
	v_addc_co_u32_e32 v45, vcc, 0, v7, vcc
	v_add_co_u32_e32 v46, vcc, s68, v6
	s_waitcnt vmcnt(11)
	v_pk_mul_f32 v[16:17], v[16:17], s[6:7] op_sel_hi:[1,0]
	v_addc_co_u32_e32 v47, vcc, 0, v7, vcc
	v_add_co_u32_e32 v48, vcc, s69, v6
	s_waitcnt vmcnt(9)
	v_pk_mul_f32 v[20:21], v[20:21], s[6:7] op_sel_hi:[1,0]
	v_addc_co_u32_e32 v49, vcc, 0, v7, vcc
	v_add_co_u32_e32 v50, vcc, s70, v6
	s_waitcnt vmcnt(4)
	v_pk_mul_f32 v[30:31], v[30:31], s[6:7] op_sel_hi:[1,0]
	v_addc_co_u32_e32 v51, vcc, 0, v7, vcc
	v_add_co_u32_e32 v52, vcc, s71, v6
	v_pk_mul_f32 v[24:25], v[24:25], s[6:7] op_sel_hi:[1,0]
	s_nop 0
	v_addc_co_u32_e32 v53, vcc, 0, v7, vcc
	v_add_co_u32_e32 v54, vcc, s72, v6
	global_load_dwordx4 v[102:105], v[46:47], off nt
	s_nop 0
	global_load_dwordx4 v[46:49], v[48:49], off offset:2048 nt
	s_nop 0
	global_load_dwordx4 v[106:109], v[42:43], off nt
	s_nop 0
	global_load_dwordx4 v[42:45], v[44:45], off offset:2048 nt
	s_nop 0
	global_load_dwordx4 v[112:115], v[50:51], off nt
	global_load_dwordx4 v[124:127], v[52:53], off offset:2048 nt
	v_addc_co_u32_e32 v55, vcc, 0, v7, vcc
	v_add_co_u32_e32 v56, vcc, s73, v6
	v_pk_mul_f32 v[52:53], v[66:67], s[6:7] op_sel_hi:[1,0]
	s_nop 0
	v_addc_co_u32_e32 v57, vcc, 0, v7, vcc
	v_add_co_u32_e32 v116, vcc, s74, v6
	v_pk_mul_f32 v[66:67], v[78:79], s[6:7] op_sel_hi:[1,0]
	s_nop 0
	v_addc_co_u32_e32 v117, vcc, 0, v7, vcc
	v_add_co_u32_e32 v144, vcc, s75, v6
	v_pk_mul_f32 v[50:51], v[8:9], s[6:7] op_sel_hi:[1,0]
	s_nop 0
	v_addc_co_u32_e32 v145, vcc, 0, v7, vcc
	v_add_co_u32_e32 v28, vcc, s76, v6
	s_waitcnt vmcnt(9)
	v_pk_mul_f32 v[78:79], v[90:91], s[6:7] op_sel_hi:[1,0]
	v_addc_co_u32_e32 v29, vcc, 0, v7, vcc
	v_add_co_u32_e32 v34, vcc, s77, v6
	s_waitcnt vmcnt(6)
; __device__ __forceinline__ unsigned pk4_fp8(float a, float b, float c, float d) { int w = 0; w = __builtin_amdgcn_cvt_pk_fp8_f32(a, b, w, false); w = __builtin_amdgcn_cvt_pk_fp8_f32(c, d, w, true); return (unsigned)w; }
; #define GAS __attribute__((address_space(1)))
; template <int MODE, int KL>
; __device__ __forceinline__ void p0_cvt_item(const float* W, int K, int N, unsigned char* WT, int il, int which, int item, int lane, const float* gk, float scale, int ldk, int koff) {
;     const int nblk = N >> 6, kb = item / nblk, nb = item - kb * nblk, nq = lane & 15, kr = lane >> 4, k0 = 4 * KL * kb + KL * kr, n0 = 64 * nb + 4 * nq;
;     const GAS f32x4* src = (const GAS f32x4*)(W + (size_t)k0 * N + n0);
;     f32x4 v[KL];
; #pragma unroll
;     for (int i = 0; i < KL; ++i) v[i] = src[(size_t)i * (N >> 2)];
;     if (MODE == 1) {
; #pragma unroll
;         for (int q = 0; q < KL / 4; ++q) { const f32x4 g = *(const GAS f32x4*)(gk + k0 + 4 * q); v[4 * q] *= g.x; v[4 * q + 1] *= g.y; v[4 * q + 2] *= g.z; v[4 * q + 3] *= g.w; } }
;     if (MODE == 2) {
; #pragma unroll
;         for (int i = 0; i < KL; ++i) v[i] *= scale; }
; #pragma unroll
;     for (int c = 0; c < 4; ++c) { const int n = n0 + c, row = il ? ((n >> 4) * 32 + which * 16 + (n & 15)) : n;
;         if (MODE == 2) { GAS v4u* dst = (GAS v4u*)(WT + (size_t)row * ldk + koff + k0);
; #pragma unroll
;             for (int q = 0; q < KL / 16; ++q) { v4u o;
;                 o.x = pg8::pk4_fp8(v[16 * q][c], v[16 * q + 1][c], v[16 * q + 2][c], v[16 * q + 3][c]);     o.y = pg8::pk4_fp8(v[16 * q + 4][c], v[16 * q + 5][c], v[16 * q + 6][c], v[16 * q + 7][c]);
;                 o.z = pg8::pk4_fp8(v[16 * q + 8][c], v[16 * q + 9][c], v[16 * q + 10][c], v[16 * q + 11][c]); o.w = pg8::pk4_fp8(v[16 * q + 12][c], v[16 * q + 13][c], v[16 * q + 14][c], v[16 * q + 15][c]);
;                 dst[q] = o; } }
	v_pk_mul_f32 v[38:39], v[38:39], s[6:7] op_sel_hi:[1,0]
	v_addc_co_u32_e32 v35, vcc, 0, v7, vcc
	v_add_co_u32_e32 v36, vcc, s78, v6
	global_load_dwordx4 v[128:131], v[54:55], off nt
	s_nop 0
	global_load_dwordx4 v[54:57], v[56:57], off offset:2048 nt
	s_nop 0
	global_load_dwordx4 v[132:135], v[28:29], off nt
	global_load_dwordx4 v[136:139], v[34:35], off offset:2048 nt
	global_load_dwordx4 v[140:143], v[116:117], off nt
	s_nop 0
	global_load_dwordx4 v[144:147], v[144:145], off offset:2048 nt
	v_addc_co_u32_e32 v37, vcc, 0, v7, vcc
	v_add_co_u32_e32 v6, vcc, s79, v6
	v_lshl_add_u64 v[28:29], s[8:9], 0, v[2:3]
	s_nop 0
	v_addc_co_u32_e32 v7, vcc, 0, v7, vcc
	global_load_dwordx4 v[148:151], v[36:37], off nt
	global_load_dwordx4 v[152:155], v[6:7], off offset:2048 nt
	v_or_b32_e32 v116, v4, v120
	v_pk_mul_f32 v[34:35], v[58:59], s[6:7] op_sel_hi:[1,0]
	v_pk_mul_f32 v[36:37], v[62:63], s[6:7] op_sel_hi:[1,0]
	v_mov_b32_e32 v2, 0
	v_mov_b32_e32 v3, 0
	v_pk_mul_f32 v[58:59], v[70:71], s[6:7] op_sel_hi:[1,0]
	v_pk_mul_f32 v[62:63], v[74:75], s[6:7] op_sel_hi:[1,0]
	v_mov_b32_e32 v4, 0
	v_pk_mul_f32 v[74:75], v[86:87], s[6:7] op_sel_hi:[1,0]
	v_cvt_pk_fp8_f32 v2, v34, v36
	v_cvt_pk_fp8_f32 v3, v12, v58
	v_cvt_pk_fp8_f32 v4, v20, v66
	v_pk_mul_f32 v[70:71], v[82:83], s[6:7] op_sel_hi:[1,0]
	v_cvt_pk_fp8_f32 v5, v74, v30
	v_pk_mul_f32 v[82:83], v[94:95], s[6:7] op_sel_hi:[1,0]
	v_pk_mul_f32 v[86:87], v[98:99], s[6:7] op_sel_hi:[1,0]
	v_mov_b32_e32 v6, 0
	v_mov_b32_e32 v7, 0
	v_mov_b32_e32 v8, 0
	v_mov_b32_e32 v9, 0
	v_cvt_pk_fp8_f32 v6, v86, v38
	v_cvt_pk_fp8_f32 v2, v50, v52 op_sel:[0,0,1]
	v_cvt_pk_fp8_f32 v3, v16, v62 op_sel:[0,0,1]
	v_cvt_pk_fp8_f32 v4, v24, v70 op_sel:[0,0,1]
	v_cvt_pk_fp8_f32 v5, v78, v82 op_sel:[0,0,1]
	v_ashrrev_i32_e32 v117, 31, v116
	v_or_b32_e32 v12, 1, v116
	v_mov_b32_e32 v82, 0
	s_waitcnt vmcnt(13)
	v_pk_mul_f32 v[90:91], v[102:103], s[6:7] op_sel_hi:[1,0]
	s_waitcnt vmcnt(12)
	v_pk_mul_f32 v[46:47], v[46:47], s[6:7] op_sel_hi:[1,0]
	s_waitcnt vmcnt(11)
	v_pk_mul_f32 v[94:95], v[106:107], s[6:7] op_sel_hi:[1,0]
	v_cvt_pk_fp8_f32 v7, v90, v46
	s_waitcnt vmcnt(9)
	v_pk_mul_f32 v[98:99], v[112:113], s[6:7] op_sel_hi:[1,0]
	s_waitcnt vmcnt(8)
	v_pk_mul_f32 v[102:103], v[124:125], s[6:7] op_sel_hi:[1,0]
	v_pk_mul_f32 v[42:43], v[42:43], s[6:7] op_sel_hi:[1,0]
	v_cvt_pk_fp8_f32 v7, v98, v102 op_sel:[0,0,1]
	v_cvt_pk_fp8_f32 v6, v94, v42 op_sel:[0,0,1]
	v_mov_b32_e32 v90, 0
	s_waitcnt vmcnt(7)
	v_pk_mul_f32 v[106:107], v[128:129], s[6:7] op_sel_hi:[1,0]
	s_waitcnt vmcnt(6)
	v_pk_mul_f32 v[54:55], v[54:55], s[6:7] op_sel_hi:[1,0]
	s_waitcnt vmcnt(5)
	v_pk_mul_f32 v[112:113], v[132:133], s[6:7] op_sel_hi:[1,0]
	s_waitcnt vmcnt(4)
	v_pk_mul_f32 v[124:125], v[136:137], s[6:7] op_sel_hi:[1,0]
	v_cvt_pk_fp8_f32 v8, v106, v54
	v_cvt_pk_fp8_f32 v9, v112, v124
	s_waitcnt vmcnt(3)
	v_pk_mul_f32 v[128:129], v[140:141], s[6:7] op_sel_hi:[1,0]
	s_waitcnt vmcnt(2)
	v_pk_mul_f32 v[132:133], v[144:145], s[6:7] op_sel_hi:[1,0]
	v_lshlrev_b64 v[144:145], 10, v[116:117]
	v_cvt_pk_fp8_f32 v8, v128, v132 op_sel:[0,0,1]
	v_lshl_add_u64 v[144:145], v[28:29], 0, v[144:145]
	s_waitcnt vmcnt(1)
	v_pk_mul_f32 v[136:137], v[148:149], s[6:7] op_sel_hi:[1,0]
	s_waitcnt vmcnt(0)
; __device__ __forceinline__ unsigned pk4_fp8(float a, float b, float c, float d) { int w = 0; w = __builtin_amdgcn_cvt_pk_fp8_f32(a, b, w, false); w = __builtin_amdgcn_cvt_pk_fp8_f32(c, d, w, true); return (unsigned)w; }
; #define GAS __attribute__((address_space(1)))
; template <int MODE, int KL>
; __device__ __forceinline__ void p0_cvt_item(const float* W, int K, int N, unsigned char* WT, int il, int which, int item, int lane, const float* gk, float scale, int ldk, int koff) {
;     ...
; #pragma unroll
;     for (int c = 0; c < 4; ++c) { const int n = n0 + c, row = il ? ((n >> 4) * 32 + which * 16 + (n & 15)) : n;
;         if (MODE == 2) { GAS v4u* dst = (GAS v4u*)(WT + (size_t)row * ldk + koff + k0);
; #pragma unroll
;             for (int q = 0; q < KL / 16; ++q) { v4u o;
;                 o.x = pg8::pk4_fp8(v[16 * q][c], v[16 * q + 1][c], v[16 * q + 2][c], v[16 * q + 3][c]);     o.y = pg8::pk4_fp8(v[16 * q + 4][c], v[16 * q + 5][c], v[16 * q + 6][c], v[16 * q + 7][c]);
;                 o.z = pg8::pk4_fp8(v[16 * q + 8][c], v[16 * q + 9][c], v[16 * q + 10][c], v[16 * q + 11][c]); o.w = pg8::pk4_fp8(v[16 * q + 12][c], v[16 * q + 13][c], v[16 * q + 14][c], v[16 * q + 15][c]);
;                 dst[q] = o; } }
	v_pk_mul_f32 v[140:141], v[152:153], s[6:7] op_sel_hi:[1,0]
	s_nop 0
	v_cvt_pk_fp8_f32 v9, v136, v140 op_sel:[0,0,1]
	global_store_dwordx4 v[144:145], v[2:5], off
	global_store_dwordx4 v[144:145], v[6:9], off offset:16
	s_nop 0
	v_mov_b32_e32 v2, 0
	v_mov_b32_e32 v3, 0
	v_mov_b32_e32 v4, 0
	v_mov_b32_e32 v5, 0
	v_cvt_pk_fp8_f32 v2, v35, v37
	v_cvt_pk_fp8_f32 v3, v13, v59
	v_cvt_pk_fp8_f32 v4, v21, v67
	v_cvt_pk_fp8_f32 v5, v75, v31
	v_mov_b32_e32 v6, 0
	v_mov_b32_e32 v7, 0
	v_mov_b32_e32 v8, 0
	v_mov_b32_e32 v9, 0
	v_cvt_pk_fp8_f32 v6, v87, v39
	v_cvt_pk_fp8_f32 v7, v91, v47
	v_cvt_pk_fp8_f32 v8, v107, v55
	v_cvt_pk_fp8_f32 v9, v113, v125
	v_cvt_pk_fp8_f32 v2, v51, v53 op_sel:[0,0,1]
	v_cvt_pk_fp8_f32 v3, v17, v63 op_sel:[0,0,1]
	v_cvt_pk_fp8_f32 v4, v25, v71 op_sel:[0,0,1]
	v_cvt_pk_fp8_f32 v5, v79, v83 op_sel:[0,0,1]
	v_cvt_pk_fp8_f32 v6, v95, v43 op_sel:[0,0,1]
	v_cvt_pk_fp8_f32 v7, v99, v103 op_sel:[0,0,1]
	v_cvt_pk_fp8_f32 v8, v129, v133 op_sel:[0,0,1]
	v_cvt_pk_fp8_f32 v9, v137, v141 op_sel:[0,0,1]
	v_ashrrev_i32_e32 v13, 31, v12
	v_lshlrev_b64 v[12:13], 10, v[12:13]
	v_lshl_add_u64 v[12:13], v[28:29], 0, v[12:13]
	v_pk_mul_f32 v[30:31], v[60:61], s[6:7] op_sel_hi:[1,0]
	v_pk_mul_f32 v[42:43], v[64:65], s[6:7] op_sel_hi:[1,0]
	v_pk_mul_f32 v[34:35], v[14:15], s[6:7] op_sel_hi:[1,0]
	v_pk_mul_f32 v[46:47], v[72:73], s[6:7] op_sel_hi:[1,0]
	v_pk_mul_f32 v[36:37], v[22:23], s[6:7] op_sel_hi:[1,0]
	v_pk_mul_f32 v[50:51], v[80:81], s[6:7] op_sel_hi:[1,0]
	v_pk_mul_f32 v[14:15], v[84:85], s[6:7] op_sel_hi:[1,0]
	v_pk_mul_f32 v[38:39], v[88:89], s[6:7] op_sel_hi:[1,0]
	v_pk_mul_f32 v[52:53], v[32:33], s[6:7] op_sel_hi:[1,0]
	v_mov_b32_e32 v83, 0
	v_mov_b32_e32 v84, 0
	v_mov_b32_e32 v85, 0
	global_store_dwordx4 v[12:13], v[2:5], off
	global_store_dwordx4 v[12:13], v[6:9], off offset:16
	v_cvt_pk_fp8_f32 v82, v30, v42
	v_pk_mul_f32 v[4:5], v[10:11], s[6:7] op_sel_hi:[1,0]
	v_pk_mul_f32 v[6:7], v[68:69], s[6:7] op_sel_hi:[1,0]
	v_pk_mul_f32 v[10:11], v[76:77], s[6:7] op_sel_hi:[1,0]
	v_cvt_pk_fp8_f32 v83, v34, v46
	v_cvt_pk_fp8_f32 v84, v36, v50
	v_cvt_pk_fp8_f32 v85, v38, v52
	v_pk_mul_f32 v[86:87], v[100:101], s[6:7] op_sel_hi:[1,0]
	v_pk_mul_f32 v[74:75], v[40:41], s[6:7] op_sel_hi:[1,0]
	v_pk_mul_f32 v[66:67], v[104:105], s[6:7] op_sel_hi:[1,0]
	v_pk_mul_f32 v[76:77], v[48:49], s[6:7] op_sel_hi:[1,0]
	v_pk_mul_f32 v[68:69], v[130:131], s[6:7] op_sel_hi:[1,0]
	v_pk_mul_f32 v[78:79], v[56:57], s[6:7] op_sel_hi:[1,0]
	v_pk_mul_f32 v[70:71], v[134:135], s[6:7] op_sel_hi:[1,0]
	v_pk_mul_f32 v[80:81], v[138:139], s[6:7] op_sel_hi:[1,0]
	v_mov_b32_e32 v88, 0
	v_mov_b32_e32 v89, 0
	v_mov_b32_e32 v91, 0
	v_cvt_pk_fp8_f32 v88, v86, v74
	v_cvt_pk_fp8_f32 v89, v66, v76
	v_cvt_pk_fp8_f32 v90, v68, v78
	v_cvt_pk_fp8_f32 v91, v70, v80
	v_pk_mul_f32 v[8:9], v[18:19], s[6:7] op_sel_hi:[1,0]
	v_pk_mul_f32 v[12:13], v[26:27], s[6:7] op_sel_hi:[1,0]
	v_pk_mul_f32 v[16:17], v[92:93], s[6:7] op_sel_hi:[1,0]
	v_pk_mul_f32 v[22:23], v[96:97], s[6:7] op_sel_hi:[1,0]
	v_cvt_pk_fp8_f32 v82, v4, v6 op_sel:[0,0,1]
	v_cvt_pk_fp8_f32 v83, v8, v10 op_sel:[0,0,1]
	v_cvt_pk_fp8_f32 v84, v12, v14 op_sel:[0,0,1]
	v_cvt_pk_fp8_f32 v85, v16, v22 op_sel:[0,0,1]
	v_or_b32_e32 v2, 2, v116
	v_pk_mul_f32 v[18:19], v[108:109], s[6:7] op_sel_hi:[1,0]
	v_pk_mul_f32 v[24:25], v[44:45], s[6:7] op_sel_hi:[1,0]
	v_pk_mul_f32 v[26:27], v[114:115], s[6:7] op_sel_hi:[1,0]
	v_pk_mul_f32 v[54:55], v[126:127], s[6:7] op_sel_hi:[1,0]
	v_pk_mul_f32 v[56:57], v[142:143], s[6:7] op_sel_hi:[1,0]
	v_pk_mul_f32 v[58:59], v[146:147], s[6:7] op_sel_hi:[1,0]
	v_pk_mul_f32 v[60:61], v[150:151], s[6:7] op_sel_hi:[1,0]
	v_pk_mul_f32 v[62:63], v[154:155], s[6:7] op_sel_hi:[1,0]
	v_ashrrev_i32_e32 v3, 31, v2
	v_cvt_pk_fp8_f32 v88, v18, v24 op_sel:[0,0,1]
	v_cvt_pk_fp8_f32 v89, v26, v54 op_sel:[0,0,1]
	v_cvt_pk_fp8_f32 v90, v56, v58 op_sel:[0,0,1]
	v_cvt_pk_fp8_f32 v91, v60, v62 op_sel:[0,0,1]
	v_lshlrev_b64 v[2:3], 10, v[2:3]
	v_lshl_add_u64 v[2:3], v[28:29], 0, v[2:3]
	global_store_dwordx4 v[2:3], v[82:85], off
	global_store_dwordx4 v[2:3], v[88:91], off offset:16
	v_or_b32_e32 v2, 3, v116
	v_ashrrev_i32_e32 v3, 31, v2
	v_lshlrev_b64 v[2:3], 10, v[2:3]
	v_lshl_add_u64 v[72:73], v[28:29], 0, v[2:3]
	s_branch .LBB0_16

; #define GAS __attribute__((address_space(1)))
; __device__ __forceinline__ void p0_prologue(Frame& F, const Args& a) {
;     ...
;     { float* ssp = (float*)(ws + WS_TBL + T_SSP2); bf16* hb = (bf16*)(ws + WS_U2);
;       for (int m = gw; m < M; m += 4 * NGW) { f32x4 v[4][4];
; #pragma unroll
;           for (int r = 0; r < 4; ++r) { const GAS f32x4* xr = (const GAS f32x4*)(a.in[0] + (size_t)(m + r * NGW) * D) + F.lane;
; #pragma unroll
;               for (int j = 0; j < 4; ++j) v[r][j] = xr[64 * j]; }
; #pragma unroll
;           for (int r = 0; r < 4; ++r) { GAS v2u* o8 = (GAS v2u*)(hb + (size_t)(m + r * NGW) * D) + F.lane; float s = 0.f;
; #pragma unroll
;               for (int j = 0; j < 4; ++j) { const f32x4 x = v[r][j]; s += (x.x * x.x + x.y * x.y) + (x.z * x.z + x.w * x.w); v2u w; w.x = pg8::pk_f16(x.x, x.y); w.y = pg8::pk_f16(x.z, x.w); o8[64 * j] = w; }
;               s = wave_sum(s, F.lane); if (F.lane < 16) ssp[(size_t)(m + r * NGW) * 16 + F.lane] = (F.lane == 0) ? s : 0.f; } } }
.LBB0_61:
	s_ashr_i32 s9, s8, 31
	s_lshl_b64 s[0:1], s[8:9], 12
	v_lshl_add_u64 v[0:1], v[54:55], 0, s[0:1]
	global_load_dwordx4 v[64:67], v[0:1], off nt
	global_load_dwordx4 v[68:71], v[0:1], off offset:1024 nt
	global_load_dwordx4 v[72:75], v[0:1], off offset:2048 nt
	global_load_dwordx4 v[76:79], v[0:1], off offset:3072 nt
	s_add_i32 s0, s8, s54
	s_add_i32 s6, s12, s8
	s_add_i32 s4, s13, s8
	s_ashr_i32 s1, s0, 31
	s_ashr_i32 s7, s6, 31
	s_ashr_i32 s5, s4, 31
	s_lshl_b64 s[10:11], s[0:1], 12
	s_lshl_b64 s[14:15], s[6:7], 12
	s_lshl_b64 s[16:17], s[4:5], 12
	v_lshl_add_u64 v[80:81], v[54:55], 0, s[10:11]
	v_lshl_add_u64 v[82:83], v[54:55], 0, s[14:15]
	v_lshl_add_u64 v[84:85], v[54:55], 0, s[16:17]
	global_load_dwordx4 v[44:47], v[80:81], off nt
	global_load_dwordx4 v[40:43], v[80:81], off offset:1024 nt
	global_load_dwordx4 v[36:39], v[80:81], off offset:2048 nt
	global_load_dwordx4 v[32:35], v[80:81], off offset:3072 nt
	global_load_dwordx4 v[28:31], v[82:83], off nt
	global_load_dwordx4 v[24:27], v[82:83], off offset:1024 nt
	global_load_dwordx4 v[20:23], v[82:83], off offset:2048 nt
	global_load_dwordx4 v[16:19], v[82:83], off offset:3072 nt
	global_load_dwordx4 v[12:15], v[84:85], off nt
	global_load_dwordx4 v[8:11], v[84:85], off offset:1024 nt
	s_waitcnt lgkmcnt(0)
	global_load_dwordx4 v[4:7], v[84:85], off offset:2048 nt
	global_load_dwordx4 v[0:3], v[84:85], off offset:3072 nt
	s_lshl_b64 s[10:11], s[8:9], 11
	s_waitcnt vmcnt(15)
	v_mul_f32_e32 v49, v65, v65
	v_mul_f32_e32 v51, v67, v67
	s_waitcnt vmcnt(14)
	v_mul_f32_e32 v80, v69, v69
	v_mul_f32_e32 v81, v71, v71
	s_waitcnt vmcnt(13)
	v_mul_f32_e32 v82, v73, v73
	v_mul_f32_e32 v83, v75, v75
	v_fmac_f32_e32 v49, v64, v64
	v_fmac_f32_e32 v51, v66, v66
	v_fmac_f32_e32 v80, v68, v68
	v_fmac_f32_e32 v81, v70, v70
	s_waitcnt vmcnt(12)
	v_mul_f32_e32 v84, v77, v77
	v_mul_f32_e32 v85, v79, v79
	v_fmac_f32_e32 v82, v72, v72
	v_fmac_f32_e32 v83, v74, v74
	v_add_f32_e32 v49, v49, v51
	v_add_f32_e32 v51, v80, v81
	v_fmac_f32_e32 v84, v76, v76
	v_fmac_f32_e32 v85, v78, v78
	v_add_f32_e32 v80, v82, v83
	v_add_f32_e32 v49, v49, v51
	v_add_f32_e32 v49, v49, v80
	v_add_f32_e32 v51, v84, v85
	v_add_f32_e32 v49, v49, v51
	ds_bpermute_b32 v51, v58, v49
	v_lshl_add_u64 v[80:81], v[56:57], 0, s[10:11]
	v_cvt_pk_f16_f32 v64, v64, v65
	v_cvt_pk_f16_f32 v65, v66, v67
	global_store_dwordx2 v[80:81], v[64:65], off
	s_waitcnt lgkmcnt(0)
	v_add_f32_e32 v49, v49, v51
	ds_bpermute_b32 v51, v59, v49
	v_cvt_pk_f16_f32 v64, v68, v69
	v_cvt_pk_f16_f32 v65, v70, v71
	global_store_dwordx2 v[80:81], v[64:65], off offset:512
	v_cvt_pk_f16_f32 v64, v72, v73
	s_waitcnt lgkmcnt(0)
	v_add_f32_e32 v49, v49, v51
	ds_bpermute_b32 v51, v60, v49
	v_cvt_pk_f16_f32 v65, v74, v75
	global_store_dwordx2 v[80:81], v[64:65], off offset:1024
	v_cvt_pk_f16_f32 v64, v76, v77
	v_cvt_pk_f16_f32 v65, v78, v79
	s_waitcnt lgkmcnt(0)
	v_add_f32_e32 v49, v49, v51
	ds_bpermute_b32 v51, v61, v49
	global_store_dwordx2 v[80:81], v[64:65], off offset:1536
	s_waitcnt lgkmcnt(0)
	v_add_f32_e32 v49, v49, v51
	ds_bpermute_b32 v51, v62, v49
	s_waitcnt lgkmcnt(0)
	v_add_f32_e32 v49, v49, v51
	ds_bpermute_b32 v51, v63, v49
	s_and_saveexec_b64 s[10:11], vcc
	s_cbranch_execz .LBB0_63
	s_lshl_b64 s[8:9], s[8:9], 6
	s_waitcnt lgkmcnt(0)
	v_add_f32_e32 v49, v49, v51
	v_lshl_add_u64 v[64:65], v[52:53], 0, s[8:9]
	v_cndmask_b32_e64 v49, 0, v49, s[2:3]
	global_store_dword v[64:65], v49, off

; #define GAS __attribute__((address_space(1)))
; __device__ __forceinline__ unsigned pk2(float lo, float hi) { return f2bf(lo) | (f2bf(hi) << 16); }
; __device__ __forceinline__ void p0_prologue(Frame& F, const Args& a) {
;     ...
;     { const GAS f32x4* src = (const GAS f32x4*)a.in[1]; GAS v2u* dst = (GAS v2u*)(ws + WS_PB); const size_t n4 = (size_t)DEPTH * M * PLE / 4;
;       const size_t st = (size_t)NGW * 64;
;       for (size_t i = (size_t)gw * 64 + F.lane; i < n4; i += 16 * st) { f32x4 v[16];
; #pragma unroll
;           for (int k = 0; k < 16; ++k) v[k] = src[i + k * st];
; #pragma unroll
;           for (int k = 0; k < 16; ++k) { v2u w; w.x = pk2(v[k].x, v[k].y); w.y = pk2(v[k].z, v[k].w); dst[i + k * st] = w; } } }
.LBB0_71:
	global_load_dwordx4 v[0:3], v[8:9], off nt
	v_lshl_add_u64 v[12:13], v[8:9], 0, s[4:5]
	global_load_dwordx4 v[14:17], v[12:13], off nt
	v_lshl_add_u64 v[12:13], v[12:13], 0, s[4:5]
	global_load_dwordx4 v[18:21], v[12:13], off nt
	v_lshl_add_u64 v[12:13], v[12:13], 0, s[4:5]
	global_load_dwordx4 v[22:25], v[12:13], off nt
	v_lshl_add_u64 v[12:13], v[12:13], 0, s[4:5]
	global_load_dwordx4 v[26:29], v[12:13], off nt
	v_lshl_add_u64 v[12:13], v[12:13], 0, s[4:5]
	v_lshl_add_u64 v[38:39], v[12:13], 0, s[4:5]
	global_load_dwordx4 v[30:33], v[12:13], off nt
	global_load_dwordx4 v[34:37], v[38:39], off nt
	v_lshl_add_u64 v[12:13], v[38:39], 0, s[4:5]
	v_lshl_add_u64 v[46:47], v[12:13], 0, s[4:5]
	global_load_dwordx4 v[38:41], v[12:13], off nt
	global_load_dwordx4 v[42:45], v[46:47], off nt
	v_lshl_add_u64 v[12:13], v[46:47], 0, s[4:5]
	v_lshl_add_u64 v[54:55], v[12:13], 0, s[4:5]
	global_load_dwordx4 v[46:49], v[12:13], off nt
	global_load_dwordx4 v[50:53], v[54:55], off nt
	v_lshl_add_u64 v[12:13], v[54:55], 0, s[4:5]
	global_load_dwordx4 v[54:57], v[12:13], off nt
	v_lshl_add_u64 v[12:13], v[12:13], 0, s[4:5]
	global_load_dwordx4 v[58:61], v[12:13], off nt
	v_lshl_add_u64 v[12:13], v[12:13], 0, s[4:5]
	global_load_dwordx4 v[62:65], v[12:13], off nt
	v_lshl_add_u64 v[12:13], v[12:13], 0, s[4:5]
	global_load_dwordx4 v[66:69], v[12:13], off nt
	v_lshl_add_u64 v[12:13], v[12:13], 0, s[4:5]
	global_load_dwordx4 v[70:73], v[12:13], off nt
	v_lshl_add_u64 v[10:11], v[6:7], 0, s[6:7]
	v_lshl_add_u64 v[74:75], v[10:11], 0, s[6:7]
	v_lshl_add_u64 v[76:77], v[74:75], 0, s[6:7]
	v_lshl_add_u64 v[78:79], v[76:77], 0, s[6:7]
	v_lshl_add_u64 v[80:81], v[78:79], 0, s[6:7]
	v_lshl_add_u64 v[82:83], v[80:81], 0, s[6:7]
	v_lshl_add_u64 v[84:85], v[82:83], 0, s[6:7]
	v_lshl_add_u64 v[86:87], v[84:85], 0, s[6:7]
	v_lshl_add_u64 v[88:89], v[86:87], 0, s[6:7]
	v_lshl_add_u64 v[90:91], v[88:89], 0, s[6:7]
	v_lshl_add_u64 v[92:93], v[90:91], 0, s[6:7]
	v_lshl_add_u64 v[94:95], v[92:93], 0, s[6:7]
	v_lshl_add_u64 v[4:5], v[4:5], 0, s[4:5]
	v_lshl_add_u64 v[96:97], v[94:95], 0, s[6:7]
	v_cmp_lt_u64_e32 vcc, s[2:3], v[4:5]
	v_lshl_add_u64 v[98:99], v[96:97], 0, s[6:7]
	v_lshl_add_u64 v[8:9], v[8:9], 0, s[12:13]
	s_or_b64 s[10:11], vcc, s[10:11]
	v_lshl_add_u64 v[100:101], v[98:99], 0, s[6:7]
	s_waitcnt vmcnt(15)
	v_bfe_u32 v12, v0, 16, 1
	v_bfe_u32 v102, v2, 16, 1
	v_bfe_u32 v13, v1, 16, 1
	v_bfe_u32 v103, v3, 16, 1
	v_add3_u32 v0, v0, v12, s0
	v_add3_u32 v2, v2, v102, s0
	s_waitcnt vmcnt(14)
	v_bfe_u32 v12, v14, 16, 1
	v_bfe_u32 v102, v16, 16, 1
	v_add3_u32 v1, v1, v13, s0
	v_add3_u32 v3, v3, v103, s0
	v_bfe_u32 v13, v15, 16, 1
	v_bfe_u32 v103, v17, 16, 1
	v_lshrrev_b32_e32 v0, 16, v0
	v_lshrrev_b32_e32 v2, 16, v2
	v_add3_u32 v12, v14, v12, s0
	v_add3_u32 v14, v16, v102, s0
	s_waitcnt vmcnt(13)
	v_bfe_u32 v16, v18, 16, 1
	v_bfe_u32 v102, v20, 16, 1
	v_add3_u32 v13, v15, v13, s0
	v_add3_u32 v15, v17, v103, s0
	v_bfe_u32 v17, v19, 16, 1
	v_bfe_u32 v103, v21, 16, 1
	v_and_or_b32 v0, v1, s1, v0
	v_and_or_b32 v1, v3, s1, v2
	v_lshrrev_b32_e32 v2, 16, v12
	v_lshrrev_b32_e32 v3, 16, v14
	v_add3_u32 v12, v18, v16, s0
	v_add3_u32 v16, v20, v102, s0
	s_waitcnt vmcnt(12)
	v_bfe_u32 v18, v22, 16, 1
	v_bfe_u32 v20, v24, 16, 1
	v_add3_u32 v14, v19, v17, s0
	v_add3_u32 v17, v21, v103, s0
	v_bfe_u32 v19, v23, 16, 1
	v_bfe_u32 v21, v25, 16, 1
	global_store_dwordx2 v[6:7], v[0:1], off
	v_and_or_b32 v0, v13, s1, v2
	v_and_or_b32 v1, v15, s1, v3
	v_lshrrev_b32_e32 v2, 16, v12
	v_lshrrev_b32_e32 v3, 16, v16
	v_add3_u32 v12, v22, v18, s0
	v_add3_u32 v15, v24, v20, s0
	s_waitcnt vmcnt(12)
	v_bfe_u32 v18, v26, 16, 1
	v_bfe_u32 v20, v28, 16, 1
	v_add3_u32 v13, v23, v19, s0
	v_add3_u32 v16, v25, v21, s0
	v_bfe_u32 v19, v27, 16, 1
	v_bfe_u32 v21, v29, 16, 1
	global_store_dwordx2 v[10:11], v[0:1], off
	v_and_or_b32 v0, v14, s1, v2
	v_and_or_b32 v1, v17, s1, v3
	v_lshrrev_b32_e32 v2, 16, v12
	v_lshrrev_b32_e32 v3, 16, v15
	v_add3_u32 v10, v26, v18, s0
	v_add3_u32 v12, v28, v20, s0
	s_waitcnt vmcnt(12)
	v_bfe_u32 v15, v30, 16, 1
	v_bfe_u32 v18, v32, 16, 1
	v_add3_u32 v11, v27, v19, s0
	v_add3_u32 v14, v29, v21, s0
	v_bfe_u32 v17, v31, 16, 1
	v_bfe_u32 v19, v33, 16, 1
	global_store_dwordx2 v[74:75], v[0:1], off
	v_and_or_b32 v0, v13, s1, v2
	v_and_or_b32 v1, v16, s1, v3
	v_lshrrev_b32_e32 v2, 16, v10
	v_lshrrev_b32_e32 v3, 16, v12
	v_add3_u32 v10, v30, v15, s0
	v_add3_u32 v13, v32, v18, s0
	s_waitcnt vmcnt(12)
; #define GAS __attribute__((address_space(1)))
; __device__ __forceinline__ unsigned pk2(float lo, float hi) { return f2bf(lo) | (f2bf(hi) << 16); }
; __device__ __forceinline__ void p0_prologue(Frame& F, const Args& a) {
;     ...
;     { const GAS f32x4* src = (const GAS f32x4*)a.in[1]; GAS v2u* dst = (GAS v2u*)(ws + WS_PB); const size_t n4 = (size_t)DEPTH * M * PLE / 4;
;       const size_t st = (size_t)NGW * 64;
;       for (size_t i = (size_t)gw * 64 + F.lane; i < n4; i += 16 * st) { f32x4 v[16];
; #pragma unroll
;           for (int k = 0; k < 16; ++k) v[k] = src[i + k * st];
; #pragma unroll
;           for (int k = 0; k < 16; ++k) { v2u w; w.x = pk2(v[k].x, v[k].y); w.y = pk2(v[k].z, v[k].w); dst[i + k * st] = w; } } }
	v_bfe_u32 v16, v34, 16, 1
	v_bfe_u32 v18, v36, 16, 1
	v_add3_u32 v12, v31, v17, s0
	v_add3_u32 v15, v33, v19, s0
	v_bfe_u32 v17, v35, 16, 1
	v_bfe_u32 v19, v37, 16, 1
	global_store_dwordx2 v[76:77], v[0:1], off
	v_and_or_b32 v0, v11, s1, v2
	v_and_or_b32 v1, v14, s1, v3
	v_lshrrev_b32_e32 v2, 16, v10
	v_lshrrev_b32_e32 v3, 16, v13
	v_add3_u32 v10, v34, v16, s0
	v_add3_u32 v13, v36, v18, s0
	s_waitcnt vmcnt(12)
	v_bfe_u32 v16, v38, 16, 1
	v_bfe_u32 v18, v40, 16, 1
	v_add3_u32 v11, v35, v17, s0
	v_add3_u32 v14, v37, v19, s0
	v_bfe_u32 v17, v39, 16, 1
	v_bfe_u32 v19, v41, 16, 1
	global_store_dwordx2 v[78:79], v[0:1], off
	v_and_or_b32 v0, v12, s1, v2
	v_and_or_b32 v1, v15, s1, v3
	v_lshrrev_b32_e32 v2, 16, v10
	v_lshrrev_b32_e32 v3, 16, v13
	v_add3_u32 v10, v38, v16, s0
	v_add3_u32 v13, v40, v18, s0
	s_waitcnt vmcnt(12)
	v_bfe_u32 v16, v42, 16, 1
	v_bfe_u32 v18, v44, 16, 1
	v_add3_u32 v12, v39, v17, s0
	v_add3_u32 v15, v41, v19, s0
	v_bfe_u32 v17, v43, 16, 1
	v_bfe_u32 v19, v45, 16, 1
	global_store_dwordx2 v[80:81], v[0:1], off
	v_and_or_b32 v0, v11, s1, v2
	v_and_or_b32 v1, v14, s1, v3
	v_lshrrev_b32_e32 v2, 16, v10
	v_lshrrev_b32_e32 v3, 16, v13
	v_add3_u32 v10, v42, v16, s0
	v_add3_u32 v13, v44, v18, s0
	s_waitcnt vmcnt(12)
	v_bfe_u32 v16, v46, 16, 1
	v_bfe_u32 v18, v48, 16, 1
	v_add3_u32 v11, v43, v17, s0
	v_add3_u32 v14, v45, v19, s0
	v_bfe_u32 v17, v47, 16, 1
	v_bfe_u32 v19, v49, 16, 1
	global_store_dwordx2 v[82:83], v[0:1], off
	v_and_or_b32 v0, v12, s1, v2
	v_and_or_b32 v1, v15, s1, v3
	v_lshrrev_b32_e32 v2, 16, v10
	v_lshrrev_b32_e32 v3, 16, v13
	v_add3_u32 v10, v46, v16, s0
	v_add3_u32 v13, v48, v18, s0
	s_waitcnt vmcnt(12)
	v_bfe_u32 v16, v50, 16, 1
	v_bfe_u32 v18, v52, 16, 1
	v_add3_u32 v12, v47, v17, s0
	v_add3_u32 v15, v49, v19, s0
	v_bfe_u32 v17, v51, 16, 1
	v_bfe_u32 v19, v53, 16, 1
	global_store_dwordx2 v[84:85], v[0:1], off
	v_and_or_b32 v0, v11, s1, v2
	v_and_or_b32 v1, v14, s1, v3
	v_lshrrev_b32_e32 v2, 16, v10
	v_lshrrev_b32_e32 v3, 16, v13
	v_add3_u32 v10, v50, v16, s0
	v_add3_u32 v13, v52, v18, s0
	s_waitcnt vmcnt(12)
	v_bfe_u32 v16, v54, 16, 1
	v_bfe_u32 v18, v56, 16, 1
	v_add3_u32 v11, v51, v17, s0
	v_add3_u32 v14, v53, v19, s0
	v_bfe_u32 v17, v55, 16, 1
	v_bfe_u32 v19, v57, 16, 1
	global_store_dwordx2 v[86:87], v[0:1], off
	v_and_or_b32 v0, v12, s1, v2
	v_and_or_b32 v1, v15, s1, v3
	v_lshrrev_b32_e32 v2, 16, v10
	v_lshrrev_b32_e32 v3, 16, v13
	v_add3_u32 v10, v54, v16, s0
	v_add3_u32 v13, v56, v18, s0
	s_waitcnt vmcnt(12)
	v_bfe_u32 v16, v58, 16, 1
	v_bfe_u32 v18, v60, 16, 1
	v_add3_u32 v12, v55, v17, s0
	v_add3_u32 v15, v57, v19, s0
	v_bfe_u32 v17, v59, 16, 1
	v_bfe_u32 v19, v61, 16, 1
	global_store_dwordx2 v[88:89], v[0:1], off
	v_and_or_b32 v0, v11, s1, v2
	v_and_or_b32 v1, v14, s1, v3
	v_lshrrev_b32_e32 v2, 16, v10
	v_lshrrev_b32_e32 v3, 16, v13
	v_add3_u32 v10, v58, v16, s0
	v_add3_u32 v13, v60, v18, s0
	s_waitcnt vmcnt(12)
	v_bfe_u32 v16, v62, 16, 1
	v_bfe_u32 v18, v64, 16, 1
	v_add3_u32 v11, v59, v17, s0
	v_add3_u32 v14, v61, v19, s0
	v_bfe_u32 v17, v63, 16, 1
	v_bfe_u32 v19, v65, 16, 1
	global_store_dwordx2 v[90:91], v[0:1], off
	v_and_or_b32 v0, v12, s1, v2
	v_and_or_b32 v1, v15, s1, v3
	v_lshrrev_b32_e32 v2, 16, v10
	v_lshrrev_b32_e32 v3, 16, v13
	v_add3_u32 v10, v62, v16, s0
	v_add3_u32 v13, v64, v18, s0
	s_waitcnt vmcnt(12)
	v_bfe_u32 v16, v66, 16, 1
	v_bfe_u32 v18, v68, 16, 1
	v_add3_u32 v12, v63, v17, s0
	v_add3_u32 v15, v65, v19, s0
	v_bfe_u32 v17, v67, 16, 1
	v_bfe_u32 v19, v69, 16, 1
	global_store_dwordx2 v[92:93], v[0:1], off
	v_and_or_b32 v0, v11, s1, v2
	v_and_or_b32 v1, v14, s1, v3
	v_lshrrev_b32_e32 v2, 16, v10
	v_lshrrev_b32_e32 v3, 16, v13
	v_add3_u32 v10, v66, v16, s0
	v_add3_u32 v13, v68, v18, s0
	s_waitcnt vmcnt(12)
	v_bfe_u32 v16, v70, 16, 1
	v_bfe_u32 v18, v72, 16, 1
	v_add3_u32 v11, v67, v17, s0
	v_add3_u32 v14, v69, v19, s0
	v_bfe_u32 v17, v71, 16, 1
	v_bfe_u32 v19, v73, 16, 1
	global_store_dwordx2 v[94:95], v[0:1], off
	v_and_or_b32 v0, v12, s1, v2
	v_and_or_b32 v1, v15, s1, v3
	v_lshrrev_b32_e32 v2, 16, v10
	v_lshrrev_b32_e32 v3, 16, v13
	v_add3_u32 v10, v70, v16, s0
	v_add3_u32 v13, v72, v18, s0
	v_add3_u32 v12, v71, v17, s0
	v_add3_u32 v15, v73, v19, s0
	global_store_dwordx2 v[96:97], v[0:1], off
	v_and_or_b32 v0, v11, s1, v2
	v_and_or_b32 v1, v14, s1, v3
	v_lshrrev_b32_e32 v2, 16, v10
	v_lshrrev_b32_e32 v3, 16, v13
	v_lshl_add_u64 v[6:7], v[6:7], 0, s[8:9]
	global_store_dwordx2 v[98:99], v[0:1], off
	v_and_or_b32 v0, v12, s1, v2
	v_and_or_b32 v1, v15, s1, v3
	global_store_dwordx2 v[100:101], v[0:1], off
	s_andn2_b64 exec, exec, s[10:11]
	s_cbranch_execnz .LBB0_71
	s_or_b64 exec, exec, s[10:11]

; #define GAS __attribute__((address_space(1)))
; template <int MODE, int KL>
; __device__ __forceinline__ void p0_cvt_item(const float* W, int K, int N, unsigned char* WT, int il, int which, int item, int lane, const float* gk, float scale, int ldk, int koff) {
;     const int nblk = N >> 6, kb = item / nblk, nb = item - kb * nblk, nq = lane & 15, kr = lane >> 4, k0 = 4 * KL * kb + KL * kr, n0 = 64 * nb + 4 * nq;
;     const GAS f32x4* src = (const GAS f32x4*)(W + (size_t)k0 * N + n0);
;     f32x4 v[KL];
; #pragma unroll
;     for (int i = 0; i < KL; ++i) v[i] = src[(size_t)i * (N >> 2)];
;     if (MODE == 1) {
; #pragma unroll
;         for (int q = 0; q < KL / 4; ++q) { const f32x4 g = *(const GAS f32x4*)(gk + k0 + 4 * q); v[4 * q] *= g.x; v[4 * q + 1] *= g.y; v[4 * q + 2] *= g.z; v[4 * q + 3] *= g.w; } }
;     if (MODE == 2) {
; #pragma unroll
;         for (int i = 0; i < KL; ++i) v[i] *= scale; }
; #pragma unroll
;     for (int c = 0; c < 4; ++c) { const int n = n0 + c, row = il ? ((n >> 4) * 32 + which * 16 + (n & 15)) : n;
;         if (MODE == 2) { GAS v4u* dst = (GAS v4u*)(WT + (size_t)row * ldk + koff + k0);
; #pragma unroll
;             for (int q = 0; q < KL / 16; ++q) { v4u o;
;                 o.x = pg8::pk4_fp8(v[16 * q][c], v[16 * q + 1][c], v[16 * q + 2][c], v[16 * q + 3][c]);     o.y = pg8::pk4_fp8(v[16 * q + 4][c], v[16 * q + 5][c], v[16 * q + 6][c], v[16 * q + 7][c]);
;                 o.z = pg8::pk4_fp8(v[16 * q + 8][c], v[16 * q + 9][c], v[16 * q + 10][c], v[16 * q + 11][c]); o.w = pg8::pk4_fp8(v[16 * q + 12][c], v[16 * q + 13][c], v[16 * q + 14][c], v[16 * q + 15][c]);
;                 dst[q] = o; } }
;         else { GAS v4u* dst = (GAS v4u*)(WT + ((size_t)row * ldk + koff + k0) * 2);
; #pragma unroll
;             for (int q = 0; q < KL / 8; ++q) { v4u o;
;                 if (MODE == 1) { o.x = pg8::pk_f16(v[8 * q][c], v[8 * q + 1][c]); o.y = pg8::pk_f16(v[8 * q + 2][c], v[8 * q + 3][c]); o.z = pg8::pk_f16(v[8 * q + 4][c], v[8 * q + 5][c]); o.w = pg8::pk_f16(v[8 * q + 6][c], v[8 * q + 7][c]); }
;                 else { o.x = pk2(v[8 * q][c], v[8 * q + 1][c]); o.y = pk2(v[8 * q + 2][c], v[8 * q + 3][c]); o.z = pk2(v[8 * q + 4][c], v[8 * q + 5][c]); o.w = pk2(v[8 * q + 6][c], v[8 * q + 7][c]); }
;                 dst[q] = o; } } }
; }
; __device__ __forceinline__ void moe_cvt_tile(const Args& a, int set, int id, int lane) {
.LBB0_137:
	s_mul_hi_i32 s0, s3, 0x92492493
	s_add_i32 s0, s0, s3
	s_lshr_b32 s1, s0, 31
	s_ashr_i32 s7, s0, 8
	s_add_i32 s7, s7, s1
	s_mul_i32 s0, s7, 0xfffffe40
	s_add_i32 s6, s3, s0
	s_cmpk_gt_i32 s3, 0x1bff
	s_mov_b64 s[0:1], -1
	s_cbranch_scc0 .LBB0_139
	v_mov_b64_e32 v[0:1], s[66:67]
	global_load_dwordx2 v[2:3], v[0:1], off offset:152
	global_load_dwordx2 v[74:75], v[0:1], off offset:192
	s_ashr_i32 s0, s6, 31
	s_lshr_b32 s0, s0, 28
	s_add_i32 s0, s6, s0
	s_ashr_i32 s0, s0, 4
	s_mul_i32 s1, s7, 0x7000
	v_lshl_add_u32 v76, s0, 7, v148
	s_lshl_b32 s0, s0, 10
	s_add_i32 s0, s0, s1
	s_sub_i32 s0, s2, s0
	s_add_i32 s8, s5, s7
	v_ashrrev_i32_e32 v77, 31, v76
	v_add_u32_e32 v152, s0, v151
	v_lshlrev_b64 v[0:1], 12, v[76:77]
	v_add_u32_e32 v68, 0xfffe8000, v152
	v_ashrrev_i32_e32 v69, 31, v68
	v_mov_b32_e32 v64, v81
	v_mov_b32_e32 v65, v81
	v_mov_b32_e32 v66, v81
	v_mov_b32_e32 v67, v81
	s_waitcnt vmcnt(0) lgkmcnt(0)
	v_mad_i64_i32 v[2:3], s[0:1], s8, v192, v[2:3]
	v_lshl_add_u64 v[0:1], v[2:3], 0, v[0:1]
	v_lshl_add_u64 v[72:73], v[68:69], 2, v[0:1]
	v_add_co_u32_e32 v8, vcc, s50, v72
	s_mov_b32 s0, 0xc000
	s_nop 0
	v_addc_co_u32_e32 v9, vcc, 0, v73, vcc
	v_add_co_u32_e32 v16, vcc, s49, v72
	global_load_dwordx4 v[0:3], v[72:73], off nt
	s_nop 0
	v_addc_co_u32_e32 v17, vcc, 0, v73, vcc
	v_add_co_u32_e32 v24, vcc, s52, v72
	s_waitcnt vmcnt(0)
	v_pk_mul_f32 v[138:139], v[0:1], s[82:83] op_sel_hi:[1,0]
	v_addc_co_u32_e32 v25, vcc, 0, v73, vcc
	v_add_co_u32_e32 v32, vcc, s33, v72
	s_nop 1
	v_addc_co_u32_e32 v33, vcc, 0, v73, vcc
	v_add_co_u32_e32 v40, vcc, s97, v72
	s_nop 1
	v_addc_co_u32_e32 v41, vcc, 0, v73, vcc
	v_add_co_u32_e32 v48, vcc, s0, v72
	s_mov_b32 s0, 0xe000
	s_nop 0
	v_addc_co_u32_e32 v49, vcc, 0, v73, vcc
	v_add_co_u32_e32 v56, vcc, s0, v72
	v_mad_i64_i32 v[74:75], s[0:1], s8, v193, v[74:75]
	s_nop 0
	v_addc_co_u32_e32 v57, vcc, 0, v73, vcc
	v_add_co_u32_e32 v70, vcc, s53, v72
	v_lshl_add_u64 v[74:75], v[74:75], 0, v[76:77]
	s_nop 0
	v_addc_co_u32_e32 v71, vcc, 0, v73, vcc
	v_add_co_u32_e32 v76, vcc, s70, v72
	s_mov_b64 s[0:1], 0x33f00000
	s_nop 0
	v_addc_co_u32_e32 v77, vcc, 0, v73, vcc
	v_add_co_u32_e32 v86, vcc, s71, v72
	v_lshl_add_u64 v[134:135], v[74:75], 0, s[0:1]
	s_nop 0
	v_addc_co_u32_e32 v87, vcc, 0, v73, vcc
	s_mov_b32 s0, 0x16000
	v_add_co_u32_e32 v94, vcc, s0, v72
	s_mov_b32 s0, 0x18000
	s_nop 0
	v_addc_co_u32_e32 v95, vcc, 0, v73, vcc
	v_add_co_u32_e32 v102, vcc, s0, v72
	s_mov_b32 s0, 0x1a000
	s_nop 0
	v_addc_co_u32_e32 v103, vcc, 0, v73, vcc
	global_load_dwordx4 v[4:7], v[8:9], off offset:-4096 nt
	s_nop 0
	global_load_dwordx4 v[8:11], v[8:9], off nt
	s_nop 0
	global_load_dwordx4 v[12:15], v[16:17], off offset:-4096 nt
	s_nop 0
	global_load_dwordx4 v[16:19], v[16:17], off nt
	s_nop 0
	global_load_dwordx4 v[20:23], v[24:25], off offset:-4096 nt
	s_nop 0
	global_load_dwordx4 v[24:27], v[24:25], off nt
	s_nop 0
	global_load_dwordx4 v[28:31], v[32:33], off offset:-4096 nt
	s_nop 0
	global_load_dwordx4 v[32:35], v[32:33], off nt
	s_nop 0
	global_load_dwordx4 v[36:39], v[40:41], off offset:-4096 nt
	s_nop 0
	global_load_dwordx4 v[40:43], v[40:41], off nt
	s_nop 0
	global_load_dwordx4 v[44:47], v[48:49], off offset:-4096 nt
	s_nop 0
	global_load_dwordx4 v[48:51], v[48:49], off nt
	s_nop 0
	global_load_dwordx4 v[52:55], v[56:57], off offset:-4096 nt
	s_nop 0
	global_load_dwordx4 v[56:59], v[56:57], off nt
	s_nop 0
	global_load_dwordx4 v[60:63], v[70:71], off offset:-4096 nt
	v_add_co_u32_e32 v114, vcc, s0, v72
	s_mov_b32 s0, 0x1c000
	s_nop 0
	v_addc_co_u32_e32 v115, vcc, 0, v73, vcc
	v_add_co_u32_e32 v122, vcc, s0, v72
	s_mov_b32 s0, 0x1e000
	s_nop 0
	v_addc_co_u32_e32 v123, vcc, 0, v73, vcc
	v_add_co_u32_e32 v130, vcc, s0, v72
	s_mov_b32 s0, 0x1f000
	s_nop 0
	v_addc_co_u32_e32 v131, vcc, 0, v73, vcc
	v_add_co_u32_e32 v104, vcc, s0, v72
	s_movk_i32 s8, 0xe00
	s_nop 0
	v_addc_co_u32_e32 v105, vcc, 0, v73, vcc
	v_mad_i64_i32 v[136:137], s[0:1], v68, s8, v[134:135]
	global_load_dwordx4 v[68:71], v[70:71], off nt
	s_nop 0
	global_load_dwordx4 v[72:75], v[76:77], off offset:-4096 nt
	s_nop 0
	global_load_dwordx4 v[76:79], v[76:77], off nt
	s_nop 0
	global_load_dwordx4 v[82:85], v[86:87], off offset:-4096 nt
	s_nop 0
	global_load_dwordx4 v[86:89], v[86:87], off nt
	s_nop 0
	global_load_dwordx4 v[90:93], v[94:95], off offset:-4096 nt
	s_nop 0
	global_load_dwordx4 v[94:97], v[94:95], off nt
	s_nop 0
	global_load_dwordx4 v[98:101], v[102:103], off offset:-4096 nt
	global_load_dwordx4 v[106:109], v[102:103], off nt
	s_nop 0
	global_load_dwordx4 v[102:105], v[104:105], off nt
	s_nop 0
	global_load_dwordx4 v[110:113], v[114:115], off offset:-4096 nt
	s_nop 0
	global_load_dwordx4 v[114:117], v[114:115], off nt
	s_nop 0
	global_load_dwordx4 v[118:121], v[122:123], off offset:-4096 nt
	s_nop 0
	global_load_dwordx4 v[122:125], v[122:123], off nt
	s_nop 0
	global_load_dwordx4 v[126:129], v[130:131], off offset:-4096 nt
	s_nop 0
	global_load_dwordx4 v[130:133], v[130:131], off nt
	s_waitcnt vmcnt(30)
	v_pk_mul_f32 v[142:143], v[4:5], s[82:83] op_sel_hi:[1,0]
	s_nop 0
	v_cvt_pk_fp8_f32 v64, v138, v142
	s_waitcnt vmcnt(29)
	v_pk_mul_f32 v[0:1], v[8:9], s[82:83] op_sel_hi:[1,0]
	s_waitcnt vmcnt(27)
	v_pk_mul_f32 v[140:141], v[16:17], s[82:83] op_sel_hi:[1,0]
	s_waitcnt vmcnt(26)
	v_pk_mul_f32 v[144:145], v[20:21], s[82:83] op_sel_hi:[1,0]
	v_pk_mul_f32 v[4:5], v[12:13], s[82:83] op_sel_hi:[1,0]
	v_cvt_pk_fp8_f32 v65, v140, v144
	s_waitcnt vmcnt(23)
	v_pk_mul_f32 v[32:33], v[32:33], s[82:83] op_sel_hi:[1,0]
	s_waitcnt vmcnt(22)
	v_pk_mul_f32 v[146:147], v[36:37], s[82:83] op_sel_hi:[1,0]
	s_waitcnt vmcnt(21)
; __device__ __forceinline__ unsigned pk4_fp8(float a, float b, float c, float d) { int w = 0; w = __builtin_amdgcn_cvt_pk_fp8_f32(a, b, w, false); w = __builtin_amdgcn_cvt_pk_fp8_f32(c, d, w, true); return (unsigned)w; }
; #define GAS __attribute__((address_space(1)))
; template <int MODE, int KL>
; __device__ __forceinline__ void p0_cvt_item(const float* W, int K, int N, unsigned char* WT, int il, int which, int item, int lane, const float* gk, float scale, int ldk, int koff) {
;     ...
;     for (int c = 0; c < 4; ++c) { const int n = n0 + c, row = il ? ((n >> 4) * 32 + which * 16 + (n & 15)) : n;
;         if (MODE == 2) { GAS v4u* dst = (GAS v4u*)(WT + (size_t)row * ldk + koff + k0);
; #pragma unroll
;             for (int q = 0; q < KL / 16; ++q) { v4u o;
;                 o.x = pg8::pk4_fp8(v[16 * q][c], v[16 * q + 1][c], v[16 * q + 2][c], v[16 * q + 3][c]);     o.y = pg8::pk4_fp8(v[16 * q + 4][c], v[16 * q + 5][c], v[16 * q + 6][c], v[16 * q + 7][c]);
;                 o.z = pg8::pk4_fp8(v[16 * q + 8][c], v[16 * q + 9][c], v[16 * q + 10][c], v[16 * q + 11][c]); o.w = pg8::pk4_fp8(v[16 * q + 12][c], v[16 * q + 13][c], v[16 * q + 14][c], v[16 * q + 15][c]);
;                 dst[q] = o; } }
	v_pk_mul_f32 v[16:17], v[40:41], s[82:83] op_sel_hi:[1,0]
	v_cvt_pk_fp8_f32 v66, v32, v146
	s_waitcnt vmcnt(19)
	v_pk_mul_f32 v[36:37], v[48:49], s[82:83] op_sel_hi:[1,0]
	s_waitcnt vmcnt(18)
	v_pk_mul_f32 v[40:41], v[52:53], s[82:83] op_sel_hi:[1,0]
	v_pk_mul_f32 v[8:9], v[24:25], s[82:83] op_sel_hi:[1,0]
	v_cvt_pk_fp8_f32 v67, v36, v40
	v_pk_mul_f32 v[12:13], v[28:29], s[82:83] op_sel_hi:[1,0]
	v_pk_mul_f32 v[20:21], v[44:45], s[82:83] op_sel_hi:[1,0]
	s_waitcnt vmcnt(17)
	v_pk_mul_f32 v[24:25], v[56:57], s[82:83] op_sel_hi:[1,0]
	s_waitcnt vmcnt(16)
	v_pk_mul_f32 v[28:29], v[60:61], s[82:83] op_sel_hi:[1,0]
	v_cvt_pk_fp8_f32 v64, v0, v4 op_sel:[0,0,1]
	v_cvt_pk_fp8_f32 v65, v8, v12 op_sel:[0,0,1]
	v_cvt_pk_fp8_f32 v66, v16, v20 op_sel:[0,0,1]
	v_cvt_pk_fp8_f32 v67, v24, v28 op_sel:[0,0,1]
	v_mov_b32_e32 v140, v81
	v_mov_b32_e32 v138, v81
	v_cvt_pk_fp8_f32 v138, v33, v147
	global_store_dwordx4 v[136:137], v[64:67], off
	v_mov_b32_e32 v142, v81
	s_waitcnt vmcnt(16)
	v_pk_mul_f32 v[44:45], v[68:69], s[82:83] op_sel_hi:[1,0]
	v_mov_b32_e32 v64, v81
	v_mov_b32_e32 v65, v81
	v_mov_b32_e32 v66, v81
	v_mov_b32_e32 v67, v81
	s_waitcnt vmcnt(15)
	v_pk_mul_f32 v[48:49], v[72:73], s[82:83] op_sel_hi:[1,0]
	s_waitcnt vmcnt(12)
	v_pk_mul_f32 v[52:53], v[86:87], s[82:83] op_sel_hi:[1,0]
	s_waitcnt vmcnt(11)
	v_pk_mul_f32 v[56:57], v[90:91], s[82:83] op_sel_hi:[1,0]
	s_waitcnt vmcnt(8)
	v_pk_mul_f32 v[60:61], v[106:107], s[82:83] op_sel_hi:[1,0]
	s_waitcnt vmcnt(6)
	v_pk_mul_f32 v[68:69], v[110:111], s[82:83] op_sel_hi:[1,0]
	s_waitcnt vmcnt(3)
	v_pk_mul_f32 v[72:73], v[122:123], s[82:83] op_sel_hi:[1,0]
	s_waitcnt vmcnt(2)
	v_pk_mul_f32 v[86:87], v[126:127], s[82:83] op_sel_hi:[1,0]
	v_cvt_pk_fp8_f32 v64, v44, v48
	v_cvt_pk_fp8_f32 v65, v52, v56
	v_cvt_pk_fp8_f32 v66, v60, v68
	v_cvt_pk_fp8_f32 v67, v72, v86
	v_pk_mul_f32 v[106:107], v[76:77], s[82:83] op_sel_hi:[1,0]
	v_pk_mul_f32 v[82:83], v[82:83], s[82:83] op_sel_hi:[1,0]
	v_pk_mul_f32 v[110:111], v[94:95], s[82:83] op_sel_hi:[1,0]
	v_pk_mul_f32 v[122:123], v[98:99], s[82:83] op_sel_hi:[1,0]
	v_pk_mul_f32 v[114:115], v[114:115], s[82:83] op_sel_hi:[1,0]
	v_pk_mul_f32 v[118:119], v[118:119], s[82:83] op_sel_hi:[1,0]
	s_waitcnt vmcnt(1)
	v_pk_mul_f32 v[126:127], v[130:131], s[82:83] op_sel_hi:[1,0]
	v_pk_mul_f32 v[102:103], v[102:103], s[82:83] op_sel_hi:[1,0]
	v_cvt_pk_fp8_f32 v64, v106, v82 op_sel:[0,0,1]
	v_cvt_pk_fp8_f32 v65, v110, v122 op_sel:[0,0,1]
	v_cvt_pk_fp8_f32 v66, v114, v118 op_sel:[0,0,1]
	v_cvt_pk_fp8_f32 v67, v126, v102 op_sel:[0,0,1]
	v_cvt_pk_fp8_f32 v140, v45, v49
	v_cvt_pk_fp8_f32 v142, v61, v69
	v_pk_mul_f32 v[68:69], v[18:19], s[82:83] op_sel_hi:[1,0]
	global_store_dwordx4 v[136:137], v[64:67], off offset:16
	v_mov_b32_e32 v136, v81
	v_cvt_pk_fp8_f32 v136, v139, v143
	v_mov_b32_e32 v139, v81
	v_cvt_pk_fp8_f32 v139, v37, v41
	v_mov_b32_e32 v137, v81
	v_cvt_pk_fp8_f32 v137, v141, v145
	v_mov_b32_e32 v141, v81
	v_mov_b32_e32 v143, v81
	v_cvt_pk_fp8_f32 v141, v53, v57
	v_cvt_pk_fp8_f32 v143, v73, v87
	v_pk_mul_f32 v[64:65], v[2:3], s[82:83] op_sel_hi:[1,0]
	v_pk_mul_f32 v[86:87], v[6:7], s[82:83] op_sel_hi:[1,0]
	v_pk_mul_f32 v[90:91], v[22:23], s[82:83] op_sel_hi:[1,0]
	v_pk_mul_f32 v[72:73], v[34:35], s[82:83] op_sel_hi:[1,0]
	v_pk_mul_f32 v[94:95], v[38:39], s[82:83] op_sel_hi:[1,0]
	v_pk_mul_f32 v[76:77], v[50:51], s[82:83] op_sel_hi:[1,0]
	v_pk_mul_f32 v[98:99], v[54:55], s[82:83] op_sel_hi:[1,0]
	v_mov_b32_e32 v48, v81
	v_mov_b32_e32 v49, v81
	v_mov_b32_e32 v50, v81
	v_mov_b32_e32 v51, v81
	v_cvt_pk_fp8_f32 v136, v1, v5 op_sel:[0,0,1]
	v_cvt_pk_fp8_f32 v139, v25, v29 op_sel:[0,0,1]
	v_pk_mul_f32 v[40:41], v[30:31], s[82:83] op_sel_hi:[1,0]
	v_pk_mul_f32 v[52:53], v[42:43], s[82:83] op_sel_hi:[1,0]
	v_pk_mul_f32 v[56:57], v[46:47], s[82:83] op_sel_hi:[1,0]
	v_pk_mul_f32 v[28:29], v[70:71], s[82:83] op_sel_hi:[1,0]
	v_pk_mul_f32 v[42:43], v[74:75], s[82:83] op_sel_hi:[1,0]
	v_pk_mul_f32 v[4:5], v[84:85], s[82:83] op_sel_hi:[1,0]
	v_pk_mul_f32 v[30:31], v[88:89], s[82:83] op_sel_hi:[1,0]
	v_pk_mul_f32 v[44:45], v[92:93], s[82:83] op_sel_hi:[1,0]
	v_pk_mul_f32 v[32:33], v[108:109], s[82:83] op_sel_hi:[1,0]
	v_pk_mul_f32 v[46:47], v[112:113], s[82:83] op_sel_hi:[1,0]
	v_pk_mul_f32 v[34:35], v[124:125], s[82:83] op_sel_hi:[1,0]
	v_pk_mul_f32 v[36:37], v[128:129], s[82:83] op_sel_hi:[1,0]
	v_cvt_pk_fp8_f32 v140, v107, v83 op_sel:[0,0,1]
	v_cvt_pk_fp8_f32 v48, v64, v86
	v_cvt_pk_fp8_f32 v49, v68, v90
	v_cvt_pk_fp8_f32 v50, v72, v94
	v_cvt_pk_fp8_f32 v51, v76, v98
	v_mov_b32_e32 v82, v81
	v_mov_b32_e32 v83, v81
	v_mov_b32_e32 v84, v81
	v_mov_b32_e32 v85, v81
	v_cvt_pk_fp8_f32 v82, v28, v42
	v_cvt_pk_fp8_f32 v83, v30, v44
	v_cvt_pk_fp8_f32 v84, v32, v46
	v_cvt_pk_fp8_f32 v85, v34, v36
	v_cvt_pk_fp8_f32 v137, v9, v13 op_sel:[0,0,1]
	v_cvt_pk_fp8_f32 v138, v17, v21 op_sel:[0,0,1]
	v_pk_mul_f32 v[20:21], v[10:11], s[82:83] op_sel_hi:[1,0]
	v_pk_mul_f32 v[24:25], v[14:15], s[82:83] op_sel_hi:[1,0]
	v_pk_mul_f32 v[26:27], v[26:27], s[82:83] op_sel_hi:[1,0]
	v_pk_mul_f32 v[58:59], v[58:59], s[82:83] op_sel_hi:[1,0]
	v_pk_mul_f32 v[60:61], v[62:63], s[82:83] op_sel_hi:[1,0]
	v_cvt_pk_fp8_f32 v141, v111, v123 op_sel:[0,0,1]
	v_cvt_pk_fp8_f32 v142, v115, v119 op_sel:[0,0,1]
	v_cvt_pk_fp8_f32 v143, v127, v103 op_sel:[0,0,1]
	v_pk_mul_f32 v[2:3], v[78:79], s[82:83] op_sel_hi:[1,0]
	v_pk_mul_f32 v[6:7], v[96:97], s[82:83] op_sel_hi:[1,0]
	v_pk_mul_f32 v[8:9], v[100:101], s[82:83] op_sel_hi:[1,0]
	v_pk_mul_f32 v[10:11], v[116:117], s[82:83] op_sel_hi:[1,0]
	v_pk_mul_f32 v[12:13], v[120:121], s[82:83] op_sel_hi:[1,0]
	v_pk_mul_f32 v[14:15], v[132:133], s[82:83] op_sel_hi:[1,0]
	v_pk_mul_f32 v[16:17], v[104:105], s[82:83] op_sel_hi:[1,0]
	v_add_u32_e32 v0, 0xfffe8001, v152
	v_cvt_pk_fp8_f32 v48, v20, v24 op_sel:[0,0,1]
	v_cvt_pk_fp8_f32 v49, v26, v40 op_sel:[0,0,1]
	v_cvt_pk_fp8_f32 v50, v52, v56 op_sel:[0,0,1]
	v_cvt_pk_fp8_f32 v51, v58, v60 op_sel:[0,0,1]
	v_mad_i64_i32 v[0:1], s[0:1], v0, s8, v[134:135]
	v_cvt_pk_fp8_f32 v82, v2, v4 op_sel:[0,0,1]
	v_cvt_pk_fp8_f32 v83, v6, v8 op_sel:[0,0,1]
	v_cvt_pk_fp8_f32 v84, v10, v12 op_sel:[0,0,1]
	v_cvt_pk_fp8_f32 v85, v14, v16 op_sel:[0,0,1]
	global_store_dwordx4 v[0:1], v[136:139], off
	global_store_dwordx4 v[0:1], v[140:143], off offset:16
	v_add_u32_e32 v0, 0xfffe8002, v152
	v_mad_i64_i32 v[0:1], s[0:1], v0, s8, v[134:135]
	global_store_dwordx4 v[0:1], v[48:51], off
	global_store_dwordx4 v[0:1], v[82:85], off offset:16
	v_add_u32_e32 v0, 0xfffe8003, v152
	v_mad_i64_i32 v[0:1], s[0:1], v0, s8, v[134:135]
	s_mov_b64 s[0:1], 0
; #define GAS __attribute__((address_space(1)))
; template <int MODE, int KL>
; __device__ __forceinline__ void p0_cvt_item(const float* W, int K, int N, unsigned char* WT, int il, int which, int item, int lane, const float* gk, float scale, int ldk, int koff) {
;     const int nblk = N >> 6, kb = item / nblk, nb = item - kb * nblk, nq = lane & 15, kr = lane >> 4, k0 = 4 * KL * kb + KL * kr, n0 = 64 * nb + 4 * nq;
;     const GAS f32x4* src = (const GAS f32x4*)(W + (size_t)k0 * N + n0);
;     f32x4 v[KL];
; #pragma unroll
;     for (int i = 0; i < KL; ++i) v[i] = src[(size_t)i * (N >> 2)];
;     if (MODE == 1) {
; #pragma unroll
;         for (int q = 0; q < KL / 4; ++q) { const f32x4 g = *(const GAS f32x4*)(gk + k0 + 4 * q); v[4 * q] *= g.x; v[4 * q + 1] *= g.y; v[4 * q + 2] *= g.z; v[4 * q + 3] *= g.w; } }
;     if (MODE == 2) {
; #pragma unroll
;         for (int i = 0; i < KL; ++i) v[i] *= scale; }
; #pragma unroll
;     for (int c = 0; c < 4; ++c) { const int n = n0 + c, row = il ? ((n >> 4) * 32 + which * 16 + (n & 15)) : n;
;         if (MODE == 2) { GAS v4u* dst = (GAS v4u*)(WT + (size_t)row * ldk + koff + k0);
; #pragma unroll
;             for (int q = 0; q < KL / 16; ++q) { v4u o;
;                 o.x = pg8::pk4_fp8(v[16 * q][c], v[16 * q + 1][c], v[16 * q + 2][c], v[16 * q + 3][c]);     o.y = pg8::pk4_fp8(v[16 * q + 4][c], v[16 * q + 5][c], v[16 * q + 6][c], v[16 * q + 7][c]);
;                 o.z = pg8::pk4_fp8(v[16 * q + 8][c], v[16 * q + 9][c], v[16 * q + 10][c], v[16 * q + 11][c]); o.w = pg8::pk4_fp8(v[16 * q + 12][c], v[16 * q + 13][c], v[16 * q + 14][c], v[16 * q + 15][c]);
;                 dst[q] = o; } }
;         else { GAS v4u* dst = (GAS v4u*)(WT + ((size_t)row * ldk + koff + k0) * 2);
; #pragma unroll
;             for (int q = 0; q < KL / 8; ++q) { v4u o;
;                 if (MODE == 1) { o.x = pg8::pk_f16(v[8 * q][c], v[8 * q + 1][c]); o.y = pg8::pk_f16(v[8 * q + 2][c], v[8 * q + 3][c]); o.z = pg8::pk_f16(v[8 * q + 4][c], v[8 * q + 5][c]); o.w = pg8::pk_f16(v[8 * q + 6][c], v[8 * q + 7][c]); }
;                 else { o.x = pk2(v[8 * q][c], v[8 * q + 1][c]); o.y = pk2(v[8 * q + 2][c], v[8 * q + 3][c]); o.z = pk2(v[8 * q + 4][c], v[8 * q + 5][c]); o.w = pk2(v[8 * q + 6][c], v[8 * q + 7][c]); }
;                 dst[q] = o; } } }
; }
; __device__ __forceinline__ void moe_cvt_tile(const Args& a, int set, int id, int lane) {
.LBB0_139:
	s_andn2_b64 vcc, exec, s[0:1]
	s_cbranch_vccnz .LBB0_136
	s_and_b32 s0, s7, 7
	s_or_b32 s10, s0, s4
	s_ashr_i32 s0, s7, 3
	s_ashr_i32 s1, s0, 31
	s_lshl_b64 s[8:9], s[0:1], 3
	s_add_u32 s8, s66, s8
	s_addc_u32 s9, s67, s9
	v_mov_b64_e32 v[0:1], s[8:9]
	global_load_dwordx2 v[0:1], v[0:1], off offset:136
	v_mov_b64_e32 v[2:3], s[66:67]
	global_load_dwordx2 v[2:3], v[2:3], off offset:192
	s_mul_hi_i32 s1, s6, 0x92492493
	s_add_i32 s1, s1, s6
	s_lshr_b32 s6, s1, 31
	s_ashr_i32 s1, s1, 5
	s_add_i32 s1, s1, s6
	s_mulk_i32 s7, 0x1c0
	s_mul_i32 s6, s1, 0xffffffc8
	v_lshl_add_u32 v98, s1, 7, v148
	s_sub_i32 s1, s6, s7
	s_mul_i32 s62, s10, 0xe00000
	s_add_i32 s1, s3, s1
	v_lshl_or_b32 v100, s1, 6, v149
	s_movk_i32 s1, 0x3800
	v_ashrrev_i32_e32 v101, 31, v100
	v_ashrrev_i32_e32 v99, 31, v98
	s_waitcnt vmcnt(0) lgkmcnt(0)
	v_lshl_add_u64 v[0:1], v[0:1], 0, s[62:63]
	v_mad_i64_i32 v[0:1], s[6:7], v98, s1, v[0:1]
	v_lshl_add_u64 v[112:113], v[100:101], 2, v[0:1]
	s_movk_i32 s1, 0x3000
	v_add_co_u32_e32 v4, vcc, s1, v112
	s_movk_i32 s1, 0x7000
	s_nop 0
	v_addc_co_u32_e32 v5, vcc, 0, v113, vcc
	v_add_co_u32_e32 v8, vcc, s1, v112
	s_mov_b32 s1, 0xe000
	s_nop 0
	v_addc_co_u32_e32 v9, vcc, 0, v113, vcc
	v_add_co_u32_e32 v12, vcc, s97, v112
	s_mul_i32 s62, s10, 0x700000
	s_nop 0
	v_addc_co_u32_e32 v13, vcc, 0, v113, vcc
	v_add_co_u32_e32 v16, vcc, s1, v112
	s_mov_b32 s1, 0x11000
	s_nop 0
	v_addc_co_u32_e32 v17, vcc, 0, v113, vcc
	v_add_co_u32_e32 v20, vcc, s1, v112
	s_mov_b32 s1, 0x15000
	s_nop 0
	v_addc_co_u32_e32 v21, vcc, 0, v113, vcc
	v_add_co_u32_e32 v24, vcc, s1, v112
	s_mov_b32 s1, 0x18000
	s_nop 0
	v_addc_co_u32_e32 v25, vcc, 0, v113, vcc
	v_add_co_u32_e32 v28, vcc, s1, v112
	s_mov_b32 s1, 0x1c000
	s_nop 0
	v_addc_co_u32_e32 v29, vcc, 0, v113, vcc
	v_add_co_u32_e32 v32, vcc, s1, v112
	s_mov_b32 s1, 0x1f000
	s_nop 0
	v_addc_co_u32_e32 v33, vcc, 0, v113, vcc
	v_add_co_u32_e32 v36, vcc, s1, v112
	s_mov_b32 s1, 0x23000
	s_nop 0
	v_addc_co_u32_e32 v37, vcc, 0, v113, vcc
	v_add_co_u32_e32 v40, vcc, s1, v112
	s_mov_b32 s1, 0x26000
	s_nop 0
	v_addc_co_u32_e32 v41, vcc, 0, v113, vcc
	v_add_co_u32_e32 v44, vcc, s1, v112
	v_lshl_add_u64 v[110:111], v[2:3], 0, s[62:63]
	s_nop 0
	v_addc_co_u32_e32 v45, vcc, 0, v113, vcc
	global_load_dwordx4 v[0:3], v[112:113], off nt
	s_nop 0
	global_load_dwordx4 v[4:7], v[4:5], off offset:2048 nt
	s_nop 0
	global_load_dwordx4 v[8:11], v[8:9], off nt
	s_nop 0
	global_load_dwordx4 v[12:15], v[12:13], off offset:2048 nt
	s_nop 0
	global_load_dwordx4 v[16:19], v[16:17], off nt
	s_nop 0
	global_load_dwordx4 v[20:23], v[20:21], off offset:2048 nt
	s_nop 0
	global_load_dwordx4 v[24:27], v[24:25], off nt
	s_nop 0
	global_load_dwordx4 v[28:31], v[28:29], off offset:2048 nt
	s_nop 0
	global_load_dwordx4 v[32:35], v[32:33], off nt
	s_nop 0
	global_load_dwordx4 v[36:39], v[36:37], off offset:2048 nt
	s_nop 0
	global_load_dwordx4 v[40:43], v[40:41], off nt
	s_nop 0
	global_load_dwordx4 v[44:47], v[44:45], off offset:2048 nt
	s_mov_b32 s1, 0x2a000
	v_add_co_u32_e32 v48, vcc, s1, v112
	s_mov_b32 s1, 0x2d000
	s_nop 0
	v_addc_co_u32_e32 v49, vcc, 0, v113, vcc
	v_add_co_u32_e32 v52, vcc, s1, v112
	s_mov_b32 s1, 0x31000
	s_nop 0
	v_addc_co_u32_e32 v53, vcc, 0, v113, vcc
	v_add_co_u32_e32 v56, vcc, s1, v112
	s_mov_b32 s1, 0x34000
	s_nop 0
	v_addc_co_u32_e32 v57, vcc, 0, v113, vcc
	v_add_co_u32_e32 v60, vcc, s1, v112
	s_mov_b32 s1, 0x38000
	s_nop 0
	v_addc_co_u32_e32 v61, vcc, 0, v113, vcc
	v_add_co_u32_e32 v64, vcc, s1, v112
	s_mov_b32 s1, 0x3b000
	s_nop 0
	v_addc_co_u32_e32 v65, vcc, 0, v113, vcc
	v_add_co_u32_e32 v68, vcc, s1, v112
	s_mov_b32 s1, 0x3f000
	s_nop 0
	v_addc_co_u32_e32 v69, vcc, 0, v113, vcc
	v_add_co_u32_e32 v72, vcc, s1, v112
	s_mov_b32 s1, 0x42000
	s_nop 0
	v_addc_co_u32_e32 v73, vcc, 0, v113, vcc
	v_add_co_u32_e32 v76, vcc, s1, v112
	s_mov_b32 s1, 0x46000
	s_nop 0
	v_addc_co_u32_e32 v77, vcc, 0, v113, vcc
	v_add_co_u32_e32 v82, vcc, s1, v112
	s_mov_b32 s1, 0x49000
	s_nop 0
	v_addc_co_u32_e32 v83, vcc, 0, v113, vcc
	v_add_co_u32_e32 v86, vcc, s1, v112
	s_mov_b32 s1, 0x4d000
	s_nop 0
	v_addc_co_u32_e32 v87, vcc, 0, v113, vcc
	v_add_co_u32_e32 v90, vcc, s1, v112
	s_mov_b32 s1, 0x50000
	s_nop 0
	v_addc_co_u32_e32 v91, vcc, 0, v113, vcc
	v_add_co_u32_e32 v94, vcc, s1, v112
	s_mov_b32 s1, 0x54000
	s_nop 0
	v_addc_co_u32_e32 v95, vcc, 0, v113, vcc
	v_add_co_u32_e32 v102, vcc, s1, v112
	s_mov_b32 s1, 0x57000
	s_nop 0
	v_addc_co_u32_e32 v103, vcc, 0, v113, vcc
	v_add_co_u32_e32 v104, vcc, s1, v112
	global_load_dwordx4 v[48:51], v[48:49], off nt
	s_nop 0
	global_load_dwordx4 v[52:55], v[52:53], off offset:2048 nt
	v_addc_co_u32_e32 v105, vcc, 0, v113, vcc
	s_mov_b32 s1, 0x5b000
	v_add_co_u32_e32 v130, vcc, s1, v112
	s_mov_b32 s1, 0x5e000
	s_nop 0
	v_addc_co_u32_e32 v131, vcc, 0, v113, vcc
	v_add_co_u32_e32 v132, vcc, s1, v112
	global_load_dwordx4 v[56:59], v[56:57], off nt
	s_nop 0
	global_load_dwordx4 v[60:63], v[60:61], off offset:2048 nt
	v_addc_co_u32_e32 v133, vcc, 0, v113, vcc
	s_mov_b32 s1, 0x62000
	v_add_co_u32_e32 v106, vcc, s1, v112
	s_mov_b32 s1, 0x65000
	s_nop 0
	v_addc_co_u32_e32 v107, vcc, 0, v113, vcc
	v_add_co_u32_e32 v108, vcc, s1, v112
	s_mov_b32 s1, 0x69000
	s_nop 0
	v_addc_co_u32_e32 v109, vcc, 0, v113, vcc
	global_load_dwordx4 v[64:67], v[64:65], off nt
	s_nop 0
	global_load_dwordx4 v[68:71], v[68:69], off offset:2048 nt
	s_nop 0
	global_load_dwordx4 v[72:75], v[72:73], off nt
	s_nop 0
	global_load_dwordx4 v[76:79], v[76:77], off offset:2048 nt
	s_nop 0
	global_load_dwordx4 v[82:85], v[82:83], off nt
	s_nop 0
	global_load_dwordx4 v[86:89], v[86:87], off offset:2048 nt
	v_add_co_u32_e32 v134, vcc, s1, v112
	s_mov_b32 s1, 0x6c000
	s_nop 0
	v_addc_co_u32_e32 v135, vcc, 0, v113, vcc
	v_add_co_u32_e32 v136, vcc, s1, v112
	s_waitcnt vmcnt(21)
; __device__ __forceinline__ unsigned pk4_fp8(float a, float b, float c, float d) { int w = 0; w = __builtin_amdgcn_cvt_pk_fp8_f32(a, b, w, false); w = __builtin_amdgcn_cvt_pk_fp8_f32(c, d, w, true); return (unsigned)w; }
; #define GAS __attribute__((address_space(1)))
; template <int MODE, int KL>
; __device__ __forceinline__ void p0_cvt_item(const float* W, int K, int N, unsigned char* WT, int il, int which, int item, int lane, const float* gk, float scale, int ldk, int koff) {
;     ...
;     for (int c = 0; c < 4; ++c) { const int n = n0 + c, row = il ? ((n >> 4) * 32 + which * 16 + (n & 15)) : n;
;         if (MODE == 2) { GAS v4u* dst = (GAS v4u*)(WT + (size_t)row * ldk + koff + k0);
; #pragma unroll
;             for (int q = 0; q < KL / 16; ++q) { v4u o;
;                 o.x = pg8::pk4_fp8(v[16 * q][c], v[16 * q + 1][c], v[16 * q + 2][c], v[16 * q + 3][c]);     o.y = pg8::pk4_fp8(v[16 * q + 4][c], v[16 * q + 5][c], v[16 * q + 6][c], v[16 * q + 7][c]);
;                 o.z = pg8::pk4_fp8(v[16 * q + 8][c], v[16 * q + 9][c], v[16 * q + 10][c], v[16 * q + 11][c]); o.w = pg8::pk4_fp8(v[16 * q + 12][c], v[16 * q + 13][c], v[16 * q + 14][c], v[16 * q + 15][c]);
;                 dst[q] = o; } }
	v_pk_mul_f32 v[126:127], v[0:1], s[96:97] op_sel_hi:[1,0]
	v_lshlrev_b32_e32 v0, 1, v100
	v_addc_co_u32_e32 v137, vcc, 0, v113, vcc
	v_and_b32_e32 v0, 0xffffffe0, v0
	global_load_dwordx4 v[90:93], v[90:91], off nt
	s_nop 0
	global_load_dwordx4 v[94:97], v[94:95], off offset:2048 nt
	s_waitcnt vmcnt(19)
	v_pk_mul_f32 v[120:121], v[16:17], s[96:97] op_sel_hi:[1,0]
	s_waitcnt vmcnt(12)
	v_pk_mul_f32 v[16:17], v[44:45], s[96:97] op_sel_hi:[1,0]
	v_lshl_add_u32 v44, s0, 4, v0
	v_lshl_add_u64 v[0:1], v[110:111], 0, v[98:99]
	global_load_dwordx4 v[110:113], v[102:103], off nt
	global_load_dwordx4 v[114:117], v[104:105], off offset:2048 nt
	s_nop 0
	global_load_dwordx4 v[102:105], v[106:107], off nt
	s_nop 0
	global_load_dwordx4 v[106:109], v[108:109], off offset:2048 nt
	s_nop 0
	global_load_dwordx4 v[138:141], v[130:131], off nt
	s_nop 0
	global_load_dwordx4 v[130:133], v[132:133], off offset:2048 nt
	s_nop 0
	global_load_dwordx4 v[142:145], v[134:135], off nt
	s_nop 0
	global_load_dwordx4 v[134:137], v[136:137], off offset:2048 nt
	v_pk_mul_f32 v[128:129], v[4:5], s[96:97] op_sel_hi:[1,0]
	v_pk_mul_f32 v[118:119], v[8:9], s[96:97] op_sel_hi:[1,0]
	v_pk_mul_f32 v[122:123], v[12:13], s[96:97] op_sel_hi:[1,0]
	v_pk_mul_f32 v[124:125], v[20:21], s[96:97] op_sel_hi:[1,0]
	v_pk_mul_f32 v[8:9], v[28:29], s[96:97] op_sel_hi:[1,0]
	v_pk_mul_f32 v[28:29], v[32:33], s[96:97] op_sel_hi:[1,0]
	v_pk_mul_f32 v[36:37], v[36:37], s[96:97] op_sel_hi:[1,0]
	v_pk_mul_f32 v[12:13], v[40:41], s[96:97] op_sel_hi:[1,0]
	v_mov_b32_e32 v98, v81
	v_mov_b32_e32 v99, v81
	v_mov_b32_e32 v100, v81
	v_mov_b32_e32 v101, v81
	v_cvt_pk_fp8_f32 v98, v126, v128
	v_cvt_pk_fp8_f32 v99, v120, v124
	v_cvt_pk_fp8_f32 v100, v28, v36
	v_pk_mul_f32 v[4:5], v[24:25], s[96:97] op_sel_hi:[1,0]
	v_cvt_pk_fp8_f32 v98, v118, v122 op_sel:[0,0,1]
	v_cvt_pk_fp8_f32 v99, v4, v8 op_sel:[0,0,1]
	v_cvt_pk_fp8_f32 v100, v12, v16 op_sel:[0,0,1]
	s_mov_b64 s[0:1], 0x25f00000
	v_lshl_add_u64 v[0:1], v[0:1], 0, s[0:1]
	v_mov_b32_e32 v118, v81
	v_mov_b32_e32 v120, v81
	v_pk_mul_f32 v[26:27], v[26:27], s[96:97] op_sel_hi:[1,0]
	s_waitcnt vmcnt(19)
	v_pk_mul_f32 v[32:33], v[48:49], s[96:97] op_sel_hi:[1,0]
	s_waitcnt vmcnt(18)
	v_pk_mul_f32 v[40:41], v[52:53], s[96:97] op_sel_hi:[1,0]
	v_or_b32_e32 v48, v44, v150
	v_cvt_pk_fp8_f32 v101, v32, v40
	v_ashrrev_i32_e32 v49, 31, v48
	v_lshlrev_b64 v[44:45], 10, v[48:49]
	v_lshl_add_u64 v[44:45], v[0:1], 0, v[44:45]
	s_waitcnt vmcnt(17)
	v_pk_mul_f32 v[20:21], v[56:57], s[96:97] op_sel_hi:[1,0]
	s_waitcnt vmcnt(16)
	v_pk_mul_f32 v[24:25], v[60:61], s[96:97] op_sel_hi:[1,0]
	v_pk_mul_f32 v[58:59], v[58:59], s[96:97] op_sel_hi:[1,0]
	v_cvt_pk_fp8_f32 v101, v20, v24 op_sel:[0,0,1]
	global_store_dwordx4 v[44:45], v[98:101], off
	s_nop 1
	v_mov_b32_e32 v98, v81
	v_mov_b32_e32 v99, v81
	v_mov_b32_e32 v100, v81
	v_mov_b32_e32 v101, v81
	s_waitcnt vmcnt(16)
	v_pk_mul_f32 v[52:53], v[64:65], s[96:97] op_sel_hi:[1,0]
	s_waitcnt vmcnt(15)
	v_pk_mul_f32 v[56:57], v[68:69], s[96:97] op_sel_hi:[1,0]
	s_waitcnt vmcnt(12)
	v_pk_mul_f32 v[60:61], v[82:83], s[96:97] op_sel_hi:[1,0]
	s_waitcnt vmcnt(11)
	v_pk_mul_f32 v[64:65], v[86:87], s[96:97] op_sel_hi:[1,0]
	v_pk_mul_f32 v[68:69], v[72:73], s[96:97] op_sel_hi:[1,0]
	v_pk_mul_f32 v[72:73], v[76:77], s[96:97] op_sel_hi:[1,0]
	v_cvt_pk_fp8_f32 v98, v52, v56
	v_cvt_pk_fp8_f32 v99, v60, v64
	v_cvt_pk_fp8_f32 v118, v53, v57
	v_pk_mul_f32 v[52:53], v[42:43], s[96:97] op_sel_hi:[1,0]
	v_cvt_pk_fp8_f32 v98, v68, v72 op_sel:[0,0,1]
	v_pk_mul_f32 v[56:57], v[46:47], s[96:97] op_sel_hi:[1,0]
	v_cvt_pk_fp8_f32 v118, v69, v73 op_sel:[0,0,1]
	v_pk_mul_f32 v[68:69], v[18:19], s[96:97] op_sel_hi:[1,0]
	s_waitcnt vmcnt(8)
	v_pk_mul_f32 v[76:77], v[110:111], s[96:97] op_sel_hi:[1,0]
	s_waitcnt vmcnt(7)
	v_pk_mul_f32 v[86:87], v[114:115], s[96:97] op_sel_hi:[1,0]
	s_waitcnt vmcnt(6)
	v_pk_mul_f32 v[110:111], v[102:103], s[96:97] op_sel_hi:[1,0]
	s_waitcnt vmcnt(5)
	v_pk_mul_f32 v[106:107], v[106:107], s[96:97] op_sel_hi:[1,0]
	v_cvt_pk_fp8_f32 v100, v76, v86
	v_cvt_pk_fp8_f32 v101, v110, v106
	v_pk_mul_f32 v[82:83], v[90:91], s[96:97] op_sel_hi:[1,0]
	v_pk_mul_f32 v[146:147], v[94:95], s[96:97] op_sel_hi:[1,0]
	s_waitcnt vmcnt(4)
	v_pk_mul_f32 v[114:115], v[138:139], s[96:97] op_sel_hi:[1,0]
	s_waitcnt vmcnt(3)
; __device__ __forceinline__ unsigned pk4_fp8(float a, float b, float c, float d) { int w = 0; w = __builtin_amdgcn_cvt_pk_fp8_f32(a, b, w, false); w = __builtin_amdgcn_cvt_pk_fp8_f32(c, d, w, true); return (unsigned)w; }
; #define GAS __attribute__((address_space(1)))
; template <int MODE, int KL>
; __device__ __forceinline__ void p0_cvt_item(const float* W, int K, int N, unsigned char* WT, int il, int which, int item, int lane, const float* gk, float scale, int ldk, int koff) {
;     ...
;     for (int c = 0; c < 4; ++c) { const int n = n0 + c, row = il ? ((n >> 4) * 32 + which * 16 + (n & 15)) : n;
;         if (MODE == 2) { GAS v4u* dst = (GAS v4u*)(WT + (size_t)row * ldk + koff + k0);
; #pragma unroll
;             for (int q = 0; q < KL / 16; ++q) { v4u o;
;                 o.x = pg8::pk4_fp8(v[16 * q][c], v[16 * q + 1][c], v[16 * q + 2][c], v[16 * q + 3][c]);     o.y = pg8::pk4_fp8(v[16 * q + 4][c], v[16 * q + 5][c], v[16 * q + 6][c], v[16 * q + 7][c]);
;                 o.z = pg8::pk4_fp8(v[16 * q + 8][c], v[16 * q + 9][c], v[16 * q + 10][c], v[16 * q + 11][c]); o.w = pg8::pk4_fp8(v[16 * q + 12][c], v[16 * q + 13][c], v[16 * q + 14][c], v[16 * q + 15][c]);
;                 dst[q] = o; } }
	v_pk_mul_f32 v[130:131], v[130:131], s[96:97] op_sel_hi:[1,0]
	s_waitcnt vmcnt(2)
	v_pk_mul_f32 v[138:139], v[142:143], s[96:97] op_sel_hi:[1,0]
	s_waitcnt vmcnt(1)
	v_pk_mul_f32 v[134:135], v[134:135], s[96:97] op_sel_hi:[1,0]
	v_cvt_pk_fp8_f32 v99, v82, v146 op_sel:[0,0,1]
	v_cvt_pk_fp8_f32 v100, v114, v130 op_sel:[0,0,1]
	v_cvt_pk_fp8_f32 v101, v138, v134 op_sel:[0,0,1]
	v_mov_b32_e32 v102, v81
	v_mov_b32_e32 v103, v81
	v_cvt_pk_fp8_f32 v102, v29, v37
	global_store_dwordx4 v[44:45], v[98:101], off offset:16
	v_cvt_pk_fp8_f32 v103, v33, v41
	v_cvt_pk_fp8_f32 v120, v77, v87
	v_mov_b32_e32 v100, v81
	v_cvt_pk_fp8_f32 v100, v127, v129
	v_mov_b32_e32 v101, v81
	v_cvt_pk_fp8_f32 v101, v121, v125
	v_mov_b32_e32 v121, v81
	v_cvt_pk_fp8_f32 v100, v119, v123 op_sel:[0,0,1]
	v_mov_b32_e32 v119, v81
	v_cvt_pk_fp8_f32 v119, v61, v65
	v_cvt_pk_fp8_f32 v121, v111, v107
	v_cvt_pk_fp8_f32 v101, v5, v9 op_sel:[0,0,1]
	v_cvt_pk_fp8_f32 v102, v13, v17 op_sel:[0,0,1]
	v_cvt_pk_fp8_f32 v103, v21, v25 op_sel:[0,0,1]
	v_or_b32_e32 v18, 1, v48
	v_ashrrev_i32_e32 v19, 31, v18
	v_cvt_pk_fp8_f32 v119, v83, v147 op_sel:[0,0,1]
	v_cvt_pk_fp8_f32 v120, v115, v131 op_sel:[0,0,1]
	v_cvt_pk_fp8_f32 v121, v139, v135 op_sel:[0,0,1]
	v_lshlrev_b64 v[18:19], 10, v[18:19]
	v_pk_mul_f32 v[64:65], v[2:3], s[96:97] op_sel_hi:[1,0]
	v_pk_mul_f32 v[86:87], v[6:7], s[96:97] op_sel_hi:[1,0]
	v_pk_mul_f32 v[90:91], v[22:23], s[96:97] op_sel_hi:[1,0]
	v_pk_mul_f32 v[40:41], v[30:31], s[96:97] op_sel_hi:[1,0]
	v_pk_mul_f32 v[72:73], v[34:35], s[96:97] op_sel_hi:[1,0]
	v_pk_mul_f32 v[94:95], v[38:39], s[96:97] op_sel_hi:[1,0]
	v_pk_mul_f32 v[76:77], v[50:51], s[96:97] op_sel_hi:[1,0]
	v_pk_mul_f32 v[98:99], v[54:55], s[96:97] op_sel_hi:[1,0]
	v_pk_mul_f32 v[30:31], v[84:85], s[96:97] op_sel_hi:[1,0]
	v_lshl_add_u64 v[18:19], v[0:1], 0, v[18:19]
	v_mov_b32_e32 v82, v81
	v_mov_b32_e32 v83, v81
	v_mov_b32_e32 v84, v81
	v_mov_b32_e32 v85, v81
	v_pk_mul_f32 v[28:29], v[66:67], s[96:97] op_sel_hi:[1,0]
	v_pk_mul_f32 v[42:43], v[70:71], s[96:97] op_sel_hi:[1,0]
	v_pk_mul_f32 v[44:45], v[88:89], s[96:97] op_sel_hi:[1,0]
	v_pk_mul_f32 v[32:33], v[112:113], s[96:97] op_sel_hi:[1,0]
	v_pk_mul_f32 v[46:47], v[116:117], s[96:97] op_sel_hi:[1,0]
	v_pk_mul_f32 v[34:35], v[104:105], s[96:97] op_sel_hi:[1,0]
	v_pk_mul_f32 v[36:37], v[108:109], s[96:97] op_sel_hi:[1,0]
	global_store_dwordx4 v[18:19], v[100:103], off
	global_store_dwordx4 v[18:19], v[118:121], off offset:16
	v_cvt_pk_fp8_f32 v82, v64, v86
	v_cvt_pk_fp8_f32 v83, v68, v90
	v_cvt_pk_fp8_f32 v84, v72, v94
	v_cvt_pk_fp8_f32 v85, v76, v98
	v_mov_b32_e32 v100, v81
	v_mov_b32_e32 v101, v81
	v_mov_b32_e32 v102, v81
	v_mov_b32_e32 v103, v81
	v_cvt_pk_fp8_f32 v100, v28, v42
	v_cvt_pk_fp8_f32 v101, v30, v44
	v_cvt_pk_fp8_f32 v102, v32, v46
	v_cvt_pk_fp8_f32 v103, v34, v36
	v_pk_mul_f32 v[20:21], v[10:11], s[96:97] op_sel_hi:[1,0]
	v_pk_mul_f32 v[24:25], v[14:15], s[96:97] op_sel_hi:[1,0]
	v_pk_mul_f32 v[60:61], v[62:63], s[96:97] op_sel_hi:[1,0]
	v_pk_mul_f32 v[2:3], v[74:75], s[96:97] op_sel_hi:[1,0]
	v_pk_mul_f32 v[4:5], v[78:79], s[96:97] op_sel_hi:[1,0]
	v_pk_mul_f32 v[6:7], v[92:93], s[96:97] op_sel_hi:[1,0]
	v_pk_mul_f32 v[8:9], v[96:97], s[96:97] op_sel_hi:[1,0]
	v_pk_mul_f32 v[10:11], v[140:141], s[96:97] op_sel_hi:[1,0]
	v_pk_mul_f32 v[12:13], v[132:133], s[96:97] op_sel_hi:[1,0]
	v_pk_mul_f32 v[14:15], v[144:145], s[96:97] op_sel_hi:[1,0]
	v_pk_mul_f32 v[16:17], v[136:137], s[96:97] op_sel_hi:[1,0]
	v_or_b32_e32 v18, 2, v48
	v_cvt_pk_fp8_f32 v82, v20, v24 op_sel:[0,0,1]
	v_cvt_pk_fp8_f32 v83, v26, v40 op_sel:[0,0,1]
	v_cvt_pk_fp8_f32 v84, v52, v56 op_sel:[0,0,1]
	v_cvt_pk_fp8_f32 v85, v58, v60 op_sel:[0,0,1]
	v_ashrrev_i32_e32 v19, 31, v18
	v_cvt_pk_fp8_f32 v100, v2, v4 op_sel:[0,0,1]
	v_cvt_pk_fp8_f32 v101, v6, v8 op_sel:[0,0,1]
	v_cvt_pk_fp8_f32 v102, v10, v12 op_sel:[0,0,1]
	v_cvt_pk_fp8_f32 v103, v14, v16 op_sel:[0,0,1]
	v_lshlrev_b64 v[18:19], 10, v[18:19]
	v_lshl_add_u64 v[18:19], v[0:1], 0, v[18:19]
	global_store_dwordx4 v[18:19], v[82:85], off
	global_store_dwordx4 v[18:19], v[100:103], off offset:16
	v_or_b32_e32 v18, 3, v48
	v_ashrrev_i32_e32 v19, 31, v18
	v_lshlrev_b64 v[18:19], 10, v[18:19]
	v_lshl_add_u64 v[0:1], v[0:1], 0, v[18:19]
	s_branch .LBB0_136

; __device__ __forceinline__ float row_rstd(const float* ssp, size_t row) {
;     const f32x4* p = (const f32x4*)(ssp + row * 16); const f32x4 a = p[0], b = p[1], c = p[2], d = p[3];
;     const float s = (((a[0] + a[1]) + (a[2] + a[3])) + ((b[0] + b[1]) + (b[2] + b[3]))) + (((c[0] + c[1]) + (c[2] + c[3])) + ((d[0] + d[1]) + (d[2] + d[3])));
;     return rsqrtf(s * (1.f / 1024.f) + 1e-6f);
; }
.LBB0_143:
	v_readlane_b32 s2, v254, 25
	s_nop 1
	v_add_u32_e32 v0, s2, v80
	s_movk_i32 s2, 0x100
	v_cmp_gt_i32_e32 vcc, s2, v0
	s_and_saveexec_b64 s[2:3], vcc
	s_cbranch_execz .LBB0_145
	v_ashrrev_i32_e32 v1, 31, v0
	v_lshl_add_u64 v[2:3], s[4:5], 0, v[0:1]
	v_lshlrev_b64 v[2:3], 6, v[2:3]
	v_lshl_add_u64 v[10:11], s[80:81], 0, v[2:3]
	s_mov_b64 s[4:5], 0x400000
	v_lshl_add_u64 v[14:15], v[10:11], 0, s[4:5]
	v_add_co_u32_e32 v10, vcc, 0x400000, v10
	s_waitcnt lgkmcnt(0)
	global_load_dwordx4 v[2:5], v[14:15], off offset:16 nt
	global_load_dwordx4 v[6:9], v[14:15], off offset:32 nt
	v_addc_co_u32_e32 v11, vcc, 0, v11, vcc
	global_load_dwordx4 v[10:13], v[10:11], off nt
	s_nop 0
	global_load_dwordx4 v[14:17], v[14:15], off offset:48 nt
	s_waitcnt vmcnt(0) lgkmcnt(0)
	v_mov_b32_e32 v22, v2
	v_mov_b32_e32 v19, v6
	v_mov_b32_e32 v21, v8
	v_mov_b32_e32 v2, v4
	v_mov_b32_e32 v18, v10
	v_mov_b32_e32 v6, v11
	v_mov_b32_e32 v20, v12
	v_mov_b32_e32 v8, v13
	v_mov_b32_e32 v23, v14
	v_mov_b32_e32 v14, v3
	v_mov_b32_e32 v3, v16
	v_mov_b32_e32 v16, v5
	v_pk_add_f32 v[4:5], v[18:19], v[6:7]
	v_pk_add_f32 v[6:7], v[20:21], v[8:9]
	v_pk_add_f32 v[8:9], v[22:23], v[14:15]
	v_pk_add_f32 v[2:3], v[2:3], v[16:17]
	v_pk_add_f32 v[4:5], v[4:5], v[6:7]
	v_pk_add_f32 v[2:3], v[8:9], v[2:3]
	s_nop 0
	v_pk_add_f32 v[2:3], v[4:5], v[2:3]
	s_nop 0
	v_add_f32_e32 v1, v2, v3
	v_fmamk_f32 v1, v1, 0x3a800000, v162
	v_mul_f32_e32 v2, 0x4b800000, v1
	v_cmp_gt_f32_e32 vcc, s85, v1
	s_nop 1
	v_cndmask_b32_e32 v1, v1, v2, vcc
	v_rsq_f32_e32 v1, v1
	v_lshl_add_u32 v2, v0, 2, 0
	v_add_u32_e32 v2, 0x20400, v2
	v_mul_f32_e32 v3, 0x45800000, v1
	v_cndmask_b32_e32 v1, v1, v3, vcc
	ds_write_b32 v2, v1

; #define GAS __attribute__((address_space(1)))
; template <int MODE, int KL>
; __device__ __forceinline__ void p0_cvt_item(const float* W, int K, int N, unsigned char* WT, int il, int which, int item, int lane, const float* gk, float scale, int ldk, int koff) {
;     const int nblk = N >> 6, kb = item / nblk, nb = item - kb * nblk, nq = lane & 15, kr = lane >> 4, k0 = 4 * KL * kb + KL * kr, n0 = 64 * nb + 4 * nq;
;     const GAS f32x4* src = (const GAS f32x4*)(W + (size_t)k0 * N + n0);
;     f32x4 v[KL];
; #pragma unroll
;     for (int i = 0; i < KL; ++i) v[i] = src[(size_t)i * (N >> 2)];
;     if (MODE == 1) {
; #pragma unroll
;         for (int q = 0; q < KL / 4; ++q) { const f32x4 g = *(const GAS f32x4*)(gk + k0 + 4 * q); v[4 * q] *= g.x; v[4 * q + 1] *= g.y; v[4 * q + 2] *= g.z; v[4 * q + 3] *= g.w; } }
;     if (MODE == 2) {
; #pragma unroll
;         for (int i = 0; i < KL; ++i) v[i] *= scale; }
; #pragma unroll
;     for (int c = 0; c < 4; ++c) { const int n = n0 + c, row = il ? ((n >> 4) * 32 + which * 16 + (n & 15)) : n;
;         if (MODE == 2) { GAS v4u* dst = (GAS v4u*)(WT + (size_t)row * ldk + koff + k0);
; #pragma unroll
;             for (int q = 0; q < KL / 16; ++q) { v4u o;
;                 o.x = pg8::pk4_fp8(v[16 * q][c], v[16 * q + 1][c], v[16 * q + 2][c], v[16 * q + 3][c]);     o.y = pg8::pk4_fp8(v[16 * q + 4][c], v[16 * q + 5][c], v[16 * q + 6][c], v[16 * q + 7][c]);
;                 o.z = pg8::pk4_fp8(v[16 * q + 8][c], v[16 * q + 9][c], v[16 * q + 10][c], v[16 * q + 11][c]); o.w = pg8::pk4_fp8(v[16 * q + 12][c], v[16 * q + 13][c], v[16 * q + 14][c], v[16 * q + 15][c]);
;                 dst[q] = o; } }
;         else { GAS v4u* dst = (GAS v4u*)(WT + ((size_t)row * ldk + koff + k0) * 2);
; #pragma unroll
;             for (int q = 0; q < KL / 8; ++q) { v4u o;
;                 if (MODE == 1) { o.x = pg8::pk_f16(v[8 * q][c], v[8 * q + 1][c]); o.y = pg8::pk_f16(v[8 * q + 2][c], v[8 * q + 3][c]); o.z = pg8::pk_f16(v[8 * q + 4][c], v[8 * q + 5][c]); o.w = pg8::pk_f16(v[8 * q + 6][c], v[8 * q + 7][c]); }
;                 else { o.x = pk2(v[8 * q][c], v[8 * q + 1][c]); o.y = pk2(v[8 * q + 2][c], v[8 * q + 3][c]); o.z = pk2(v[8 * q + 4][c], v[8 * q + 5][c]); o.w = pk2(v[8 * q + 6][c], v[8 * q + 7][c]); }
;                 dst[q] = o; } } }
; }
; __device__ __forceinline__ void moe_cvt_tile(const Args& a, int set, int id, int lane) {
.LBB0_930:
	s_mul_hi_i32 s0, s7, 0x92492493
	s_add_i32 s0, s0, s7
	s_lshr_b32 s1, s0, 31
	s_ashr_i32 s10, s0, 8
	s_add_i32 s10, s10, s1
	s_mul_i32 s0, s10, 0xfffffe40
	s_add_i32 s11, s7, s0
	s_cmpk_gt_i32 s7, 0x1bff
	s_mov_b64 s[0:1], -1
	s_cbranch_scc0 .LBB0_932
	v_mov_b64_e32 v[0:1], s[66:67]
	global_load_dwordx2 v[2:3], v[0:1], off offset:152
	s_add_i32 s4, s9, s10
	global_load_dwordx2 v[0:1], v[0:1], off offset:192
	s_waitcnt vmcnt(0) lgkmcnt(0)
	v_mad_i64_i32 v[2:3], s[0:1], s4, v192, v[2:3]
	v_mad_i64_i32 v[78:79], s[0:1], s4, v193, v[0:1]
	s_ashr_i32 s0, s11, 31
	s_lshr_b32 s0, s0, 28
	s_add_i32 s0, s11, s0
	s_ashr_i32 s0, s0, 4
	v_lshl_add_u32 v122, s0, 7, v80
	s_lshl_b32 s0, s0, 10
	s_mul_i32 s1, s10, 0x7000
	s_add_i32 s0, s0, s1
	s_sub_i32 s0, s6, s0
	v_add_u32_e32 v157, s0, v156
	v_ashrrev_i32_e32 v123, 31, v122
	v_add_u32_e32 v124, 0xffff0000, v157
	v_lshlrev_b64 v[0:1], 12, v[122:123]
	v_lshl_add_u64 v[0:1], v[2:3], 0, v[0:1]
	v_ashrrev_i32_e32 v125, 31, v124
	v_lshl_add_u64 v[8:9], v[124:125], 2, v[0:1]
	s_movk_i32 s0, 0x2000
	v_add_co_u32_e32 v10, vcc, s0, v8
	s_movk_i32 s0, 0x4000
	s_nop 0
	v_addc_co_u32_e32 v11, vcc, 0, v9, vcc
	v_add_co_u32_e32 v14, vcc, s0, v8
	s_movk_i32 s0, 0x6000
	s_nop 0
	v_addc_co_u32_e32 v15, vcc, 0, v9, vcc
	v_add_co_u32_e32 v18, vcc, s0, v8
	s_mov_b32 s0, 0xc000
	s_nop 0
	v_addc_co_u32_e32 v19, vcc, 0, v9, vcc
	v_add_co_u32_e32 v26, vcc, s33, v8
	global_load_dwordx4 v[0:3], v[8:9], off nt
	s_nop 0
	v_addc_co_u32_e32 v27, vcc, 0, v9, vcc
	v_add_co_u32_e32 v34, vcc, s97, v8
	global_load_dwordx4 v[4:7], v[10:11], off offset:-4096 nt
	s_nop 0
	global_load_dwordx4 v[10:13], v[10:11], off nt
	v_addc_co_u32_e32 v35, vcc, 0, v9, vcc
	v_add_co_u32_e32 v42, vcc, s0, v8
	s_mov_b32 s0, 0xe000
	s_nop 0
	v_addc_co_u32_e32 v43, vcc, 0, v9, vcc
	v_add_co_u32_e32 v50, vcc, s0, v8
	s_mov_b32 s0, 0x10000
	s_nop 0
	v_addc_co_u32_e32 v51, vcc, 0, v9, vcc
	v_add_co_u32_e32 v58, vcc, s0, v8
	s_mov_b32 s0, 0x12000
	s_nop 0
	v_addc_co_u32_e32 v59, vcc, 0, v9, vcc
	v_add_co_u32_e32 v70, vcc, s0, v8
	s_mov_b32 s0, 0x14000
	s_nop 0
	v_addc_co_u32_e32 v71, vcc, 0, v9, vcc
	v_add_co_u32_e32 v82, vcc, s0, v8
	s_mov_b32 s0, 0x16000
	s_nop 0
	v_addc_co_u32_e32 v83, vcc, 0, v9, vcc
	global_load_dwordx4 v[22:25], v[14:15], off offset:-4096 nt
	s_nop 0
	global_load_dwordx4 v[14:17], v[14:15], off nt
	s_nop 0
	global_load_dwordx4 v[30:33], v[18:19], off offset:-4096 nt
	s_nop 0
	global_load_dwordx4 v[18:21], v[18:19], off nt
	s_nop 0
	global_load_dwordx4 v[38:41], v[26:27], off offset:-4096 nt
	s_nop 0
	global_load_dwordx4 v[26:29], v[26:27], off nt
	s_nop 0
	global_load_dwordx4 v[46:49], v[34:35], off offset:-4096 nt
	s_nop 0
	global_load_dwordx4 v[34:37], v[34:35], off nt
	s_nop 0
	global_load_dwordx4 v[54:57], v[42:43], off offset:-4096 nt
	s_nop 0
	global_load_dwordx4 v[42:45], v[42:43], off nt
	s_nop 0
	global_load_dwordx4 v[62:65], v[50:51], off offset:-4096 nt
	s_nop 0
	global_load_dwordx4 v[50:53], v[50:51], off nt
	s_nop 0
	global_load_dwordx4 v[66:69], v[58:59], off offset:-4096 nt
	s_nop 0
	global_load_dwordx4 v[58:61], v[58:59], off nt
	s_nop 0
	global_load_dwordx4 v[74:77], v[70:71], off offset:-4096 nt
	s_nop 0
	global_load_dwordx4 v[70:73], v[70:71], off nt
	v_add_co_u32_e32 v90, vcc, s0, v8
	s_mov_b32 s0, 0x18000
	s_nop 0
	v_addc_co_u32_e32 v91, vcc, 0, v9, vcc
	v_add_co_u32_e32 v98, vcc, s0, v8
	s_mov_b32 s0, 0x1a000
	s_nop 0
	v_addc_co_u32_e32 v99, vcc, 0, v9, vcc
	v_add_co_u32_e32 v106, vcc, s0, v8
	s_mov_b32 s0, 0x1c000
	s_nop 0
	v_addc_co_u32_e32 v107, vcc, 0, v9, vcc
	v_add_co_u32_e32 v114, vcc, s0, v8
	s_mov_b32 s0, 0x1e000
	s_nop 0
	v_addc_co_u32_e32 v115, vcc, 0, v9, vcc
	v_add_co_u32_e32 v126, vcc, s0, v8
	global_load_dwordx4 v[86:89], v[82:83], off offset:-4096 nt
	s_nop 0
	global_load_dwordx4 v[82:85], v[82:83], off nt
	s_nop 0
	global_load_dwordx4 v[94:97], v[90:91], off offset:-4096 nt
	s_nop 0
	global_load_dwordx4 v[90:93], v[90:91], off nt
	s_nop 0
	global_load_dwordx4 v[102:105], v[98:99], off offset:-4096 nt
	s_nop 0
	global_load_dwordx4 v[98:101], v[98:99], off nt
	s_nop 0
	global_load_dwordx4 v[110:113], v[106:107], off offset:-4096 nt
	s_nop 0
	global_load_dwordx4 v[106:109], v[106:107], off nt
	s_nop 0
	global_load_dwordx4 v[118:121], v[114:115], off offset:-4096 nt
	s_nop 0
	global_load_dwordx4 v[114:117], v[114:115], off nt
	v_addc_co_u32_e32 v127, vcc, 0, v9, vcc
	global_load_dwordx4 v[158:161], v[126:127], off offset:-4096 nt
	global_load_dwordx4 v[174:177], v[126:127], off nt
	s_mov_b32 s0, 0x1f000
	v_add_co_u32_e32 v8, vcc, s0, v8
	s_mov_b64 s[0:1], 0x33f00000
	s_nop 0
	v_addc_co_u32_e32 v9, vcc, 0, v9, vcc
	global_load_dwordx4 v[178:181], v[8:9], off nt
	s_movk_i32 s4, 0xe00
	s_waitcnt vmcnt(31)
	v_pk_mul_f32 v[126:127], v[0:1], s[82:83] op_sel_hi:[1,0]
	v_lshl_add_u64 v[0:1], v[78:79], 0, v[122:123]
	v_lshl_add_u64 v[0:1], v[0:1], 0, s[0:1]
	v_mad_i64_i32 v[78:79], s[0:1], v124, s4, v[0:1]
	s_waitcnt vmcnt(30)
	v_pk_mul_f32 v[8:9], v[6:7], s[82:83] op_sel_hi:[1,0]
	v_pk_mul_f32 v[6:7], v[4:5], s[82:83] op_sel_hi:[1,0]
	s_waitcnt vmcnt(29)
	v_pk_mul_f32 v[128:129], v[10:11], s[82:83] op_sel_hi:[1,0]
	v_pk_mul_f32 v[4:5], v[12:13], s[82:83] op_sel_hi:[1,0]
	v_pk_mul_f32 v[2:3], v[2:3], s[82:83] op_sel_hi:[1,0]
	s_waitcnt vmcnt(28)
	v_pk_mul_f32 v[132:133], v[22:23], s[82:83] op_sel_hi:[1,0]
	s_waitcnt vmcnt(27)
	v_pk_mul_f32 v[130:131], v[14:15], s[82:83] op_sel_hi:[1,0]
	s_waitcnt vmcnt(26)
	v_pk_mul_f32 v[134:135], v[30:31], s[82:83] op_sel_hi:[1,0]
	s_waitcnt vmcnt(25)
	v_pk_mul_f32 v[136:137], v[18:19], s[82:83] op_sel_hi:[1,0]
	s_waitcnt vmcnt(24)
; __device__ __forceinline__ unsigned pk4_fp8(float a, float b, float c, float d) { int w = 0; w = __builtin_amdgcn_cvt_pk_fp8_f32(a, b, w, false); w = __builtin_amdgcn_cvt_pk_fp8_f32(c, d, w, true); return (unsigned)w; }
; #define GAS __attribute__((address_space(1)))
; template <int MODE, int KL>
; __device__ __forceinline__ void p0_cvt_item(const float* W, int K, int N, unsigned char* WT, int il, int which, int item, int lane, const float* gk, float scale, int ldk, int koff) {
;     ...
;     for (int c = 0; c < 4; ++c) { const int n = n0 + c, row = il ? ((n >> 4) * 32 + which * 16 + (n & 15)) : n;
;         if (MODE == 2) { GAS v4u* dst = (GAS v4u*)(WT + (size_t)row * ldk + koff + k0);
; #pragma unroll
;             for (int q = 0; q < KL / 16; ++q) { v4u o;
;                 o.x = pg8::pk4_fp8(v[16 * q][c], v[16 * q + 1][c], v[16 * q + 2][c], v[16 * q + 3][c]);     o.y = pg8::pk4_fp8(v[16 * q + 4][c], v[16 * q + 5][c], v[16 * q + 6][c], v[16 * q + 7][c]);
;                 o.z = pg8::pk4_fp8(v[16 * q + 8][c], v[16 * q + 9][c], v[16 * q + 10][c], v[16 * q + 11][c]); o.w = pg8::pk4_fp8(v[16 * q + 12][c], v[16 * q + 13][c], v[16 * q + 14][c], v[16 * q + 15][c]);
;                 dst[q] = o; } }
	v_pk_mul_f32 v[18:19], v[40:41], s[82:83] op_sel_hi:[1,0]
	v_pk_mul_f32 v[138:139], v[38:39], s[82:83] op_sel_hi:[1,0]
	s_waitcnt vmcnt(23)
	v_pk_mul_f32 v[40:41], v[26:27], s[82:83] op_sel_hi:[1,0]
	s_waitcnt vmcnt(22)
	v_pk_mul_f32 v[140:141], v[46:47], s[82:83] op_sel_hi:[1,0]
	s_waitcnt vmcnt(19)
	v_pk_mul_f32 v[148:149], v[42:43], s[82:83] op_sel_hi:[1,0]
	s_waitcnt vmcnt(18)
	v_pk_mul_f32 v[182:183], v[62:63], s[82:83] op_sel_hi:[1,0]
	s_waitcnt vmcnt(14)
	v_pk_mul_f32 v[42:43], v[76:77], s[82:83] op_sel_hi:[1,0]
	s_waitcnt vmcnt(13)
	v_pk_mul_f32 v[38:39], v[72:73], s[82:83] op_sel_hi:[1,0]
	v_pk_mul_f32 v[76:77], v[70:71], s[82:83] op_sel_hi:[1,0]
	v_mov_b32_e32 v70, v81
	v_mov_b32_e32 v71, v81
	v_mov_b32_e32 v72, v81
	v_mov_b32_e32 v73, v81
	v_cvt_pk_fp8_f32 v70, v126, v6
	v_cvt_pk_fp8_f32 v71, v130, v134
	v_cvt_pk_fp8_f32 v72, v40, v140
	v_cvt_pk_fp8_f32 v73, v148, v182
	v_pk_mul_f32 v[142:143], v[34:35], s[82:83] op_sel_hi:[1,0]
	v_pk_mul_f32 v[150:151], v[54:55], s[82:83] op_sel_hi:[1,0]
	v_pk_mul_f32 v[144:145], v[50:51], s[82:83] op_sel_hi:[1,0]
	v_pk_mul_f32 v[152:153], v[66:67], s[82:83] op_sel_hi:[1,0]
	v_cvt_pk_fp8_f32 v70, v128, v132 op_sel:[0,0,1]
	v_cvt_pk_fp8_f32 v71, v136, v138 op_sel:[0,0,1]
	v_cvt_pk_fp8_f32 v72, v142, v150 op_sel:[0,0,1]
	v_cvt_pk_fp8_f32 v73, v144, v152 op_sel:[0,0,1]
	v_pk_mul_f32 v[12:13], v[16:17], s[82:83] op_sel_hi:[1,0]
	v_pk_mul_f32 v[16:17], v[20:21], s[82:83] op_sel_hi:[1,0]
	v_pk_mul_f32 v[20:21], v[28:29], s[82:83] op_sel_hi:[1,0]
	v_pk_mul_f32 v[28:29], v[44:45], s[82:83] op_sel_hi:[1,0]
	v_pk_mul_f32 v[146:147], v[58:59], s[82:83] op_sel_hi:[1,0]
	v_pk_mul_f32 v[74:75], v[74:75], s[82:83] op_sel_hi:[1,0]
	s_waitcnt vmcnt(12)
	v_pk_mul_f32 v[44:45], v[88:89], s[82:83] op_sel_hi:[1,0]
	s_waitcnt vmcnt(11)
	v_pk_mul_f32 v[46:47], v[84:85], s[82:83] op_sel_hi:[1,0]
	v_pk_mul_f32 v[82:83], v[82:83], s[82:83] op_sel_hi:[1,0]
	s_waitcnt vmcnt(10)
	v_pk_mul_f32 v[84:85], v[94:95], s[82:83] op_sel_hi:[1,0]
	s_waitcnt vmcnt(9)
	v_pk_mul_f32 v[50:51], v[92:93], s[82:83] op_sel_hi:[1,0]
	v_pk_mul_f32 v[88:89], v[90:91], s[82:83] op_sel_hi:[1,0]
	s_waitcnt vmcnt(8)
	v_pk_mul_f32 v[90:91], v[102:103], s[82:83] op_sel_hi:[1,0]
	s_waitcnt vmcnt(7)
	v_pk_mul_f32 v[54:55], v[100:101], s[82:83] op_sel_hi:[1,0]
	v_pk_mul_f32 v[92:93], v[98:99], s[82:83] op_sel_hi:[1,0]
	s_waitcnt vmcnt(6)
	v_pk_mul_f32 v[94:95], v[110:111], s[82:83] op_sel_hi:[1,0]
	s_waitcnt vmcnt(3)
	v_pk_mul_f32 v[100:101], v[114:115], s[82:83] op_sel_hi:[1,0]
	s_waitcnt vmcnt(2)
	v_pk_mul_f32 v[102:103], v[158:159], s[82:83] op_sel_hi:[1,0]
	global_store_dwordx4 v[78:79], v[70:73], off
	v_pk_mul_f32 v[14:15], v[32:33], s[82:83] op_sel_hi:[1,0]
	v_pk_mul_f32 v[22:23], v[48:49], s[82:83] op_sel_hi:[1,0]
	v_mov_b32_e32 v70, v81
	v_mov_b32_e32 v71, v81
	v_mov_b32_e32 v72, v81
	v_mov_b32_e32 v73, v81
	v_cvt_pk_fp8_f32 v70, v146, v74
	v_cvt_pk_fp8_f32 v71, v82, v84
	v_cvt_pk_fp8_f32 v72, v92, v94
	v_cvt_pk_fp8_f32 v73, v100, v102
	v_pk_mul_f32 v[32:33], v[52:53], s[82:83] op_sel_hi:[1,0]
	v_pk_mul_f32 v[86:87], v[86:87], s[82:83] op_sel_hi:[1,0]
	v_pk_mul_f32 v[48:49], v[96:97], s[82:83] op_sel_hi:[1,0]
	v_pk_mul_f32 v[52:53], v[104:105], s[82:83] op_sel_hi:[1,0]
	v_pk_mul_f32 v[96:97], v[106:107], s[82:83] op_sel_hi:[1,0]
	v_pk_mul_f32 v[98:99], v[118:119], s[82:83] op_sel_hi:[1,0]
	s_waitcnt vmcnt(2)
	v_pk_mul_f32 v[104:105], v[174:175], s[82:83] op_sel_hi:[1,0]
	s_waitcnt vmcnt(1)
	v_pk_mul_f32 v[106:107], v[178:179], s[82:83] op_sel_hi:[1,0]
	v_cvt_pk_fp8_f32 v70, v76, v86 op_sel:[0,0,1]
	v_cvt_pk_fp8_f32 v71, v88, v90 op_sel:[0,0,1]
	v_cvt_pk_fp8_f32 v72, v96, v98 op_sel:[0,0,1]
	v_cvt_pk_fp8_f32 v73, v104, v106 op_sel:[0,0,1]
	v_add_u32_e32 v6, 0xffff0001, v157
	v_pk_mul_f32 v[30:31], v[64:65], s[82:83] op_sel_hi:[1,0]
	v_pk_mul_f32 v[10:11], v[24:25], s[82:83] op_sel_hi:[1,0]
	global_store_dwordx4 v[78:79], v[70:73], off offset:16
	v_mad_i64_i32 v[78:79], s[0:1], v6, s4, v[0:1]
	s_nop 0
	v_mov_b32_e32 v70, v81
	v_mov_b32_e32 v71, v81
	v_mov_b32_e32 v72, v81
	v_mov_b32_e32 v73, v81
	v_cvt_pk_fp8_f32 v70, v127, v7
	v_cvt_pk_fp8_f32 v71, v131, v135
	v_cvt_pk_fp8_f32 v72, v41, v141
	v_cvt_pk_fp8_f32 v73, v149, v183
	v_cvt_pk_fp8_f32 v70, v129, v133 op_sel:[0,0,1]
	v_cvt_pk_fp8_f32 v71, v137, v139 op_sel:[0,0,1]
	v_cvt_pk_fp8_f32 v72, v143, v151 op_sel:[0,0,1]
	v_cvt_pk_fp8_f32 v73, v145, v153 op_sel:[0,0,1]
	v_pk_mul_f32 v[24:25], v[36:37], s[82:83] op_sel_hi:[1,0]
	v_pk_mul_f32 v[26:27], v[56:57], s[82:83] op_sel_hi:[1,0]
	v_pk_mul_f32 v[34:35], v[68:69], s[82:83] op_sel_hi:[1,0]
	global_store_dwordx4 v[78:79], v[70:73], off
	v_add_u32_e32 v6, 0xffff0002, v157
	v_mad_i64_i32 v[6:7], s[0:1], v6, s4, v[0:1]
	v_mov_b32_e32 v70, v81
	v_mov_b32_e32 v71, v81
	v_mov_b32_e32 v72, v81
	v_mov_b32_e32 v73, v81
	v_cvt_pk_fp8_f32 v70, v147, v75
	v_cvt_pk_fp8_f32 v71, v83, v85
	v_cvt_pk_fp8_f32 v72, v93, v95
	v_cvt_pk_fp8_f32 v73, v101, v103
	v_cvt_pk_fp8_f32 v70, v77, v87 op_sel:[0,0,1]
	v_cvt_pk_fp8_f32 v71, v89, v91 op_sel:[0,0,1]
	v_cvt_pk_fp8_f32 v72, v97, v99 op_sel:[0,0,1]
	v_cvt_pk_fp8_f32 v73, v105, v107 op_sel:[0,0,1]
	v_pk_mul_f32 v[36:37], v[60:61], s[82:83] op_sel_hi:[1,0]
	v_pk_mul_f32 v[56:57], v[112:113], s[82:83] op_sel_hi:[1,0]
	v_pk_mul_f32 v[62:63], v[116:117], s[82:83] op_sel_hi:[1,0]
	global_store_dwordx4 v[78:79], v[70:73], off offset:16
	v_pk_mul_f32 v[64:65], v[160:161], s[82:83] op_sel_hi:[1,0]
	v_pk_mul_f32 v[58:59], v[108:109], s[82:83] op_sel_hi:[1,0]
	v_mov_b32_e32 v70, v81
	v_mov_b32_e32 v71, v81
	v_mov_b32_e32 v72, v81
	v_mov_b32_e32 v73, v81
	v_cvt_pk_fp8_f32 v70, v2, v8
	v_cvt_pk_fp8_f32 v71, v12, v14
	v_cvt_pk_fp8_f32 v72, v20, v22
	v_cvt_pk_fp8_f32 v73, v28, v30
	v_cvt_pk_fp8_f32 v70, v4, v10 op_sel:[0,0,1]
	v_cvt_pk_fp8_f32 v71, v16, v18 op_sel:[0,0,1]
	v_cvt_pk_fp8_f32 v72, v24, v26 op_sel:[0,0,1]
	v_cvt_pk_fp8_f32 v73, v32, v34 op_sel:[0,0,1]
	v_pk_mul_f32 v[60:61], v[120:121], s[82:83] op_sel_hi:[1,0]
	v_pk_mul_f32 v[66:67], v[176:177], s[82:83] op_sel_hi:[1,0]
	v_pk_mul_f32 v[68:69], v[180:181], s[82:83] op_sel_hi:[1,0]
	global_store_dwordx4 v[6:7], v[70:73], off
	v_add_u32_e32 v2, 0xffff0003, v157
	v_mad_i64_i32 v[0:1], s[0:1], v2, s4, v[0:1]
	v_mov_b32_e32 v70, v81
	v_mov_b32_e32 v71, v81
	v_mov_b32_e32 v72, v81
	v_mov_b32_e32 v73, v81
	v_cvt_pk_fp8_f32 v70, v36, v42
	v_cvt_pk_fp8_f32 v71, v46, v48
	v_cvt_pk_fp8_f32 v72, v54, v56
	v_cvt_pk_fp8_f32 v73, v62, v64
	v_cvt_pk_fp8_f32 v70, v38, v44 op_sel:[0,0,1]
	v_cvt_pk_fp8_f32 v71, v50, v52 op_sel:[0,0,1]
	v_cvt_pk_fp8_f32 v72, v58, v60 op_sel:[0,0,1]
	v_cvt_pk_fp8_f32 v73, v66, v68 op_sel:[0,0,1]
	s_mov_b64 s[0:1], 0
	global_store_dwordx4 v[6:7], v[70:73], off offset:16
; #define GAS __attribute__((address_space(1)))
; template <int MODE, int KL>
; __device__ __forceinline__ void p0_cvt_item(const float* W, int K, int N, unsigned char* WT, int il, int which, int item, int lane, const float* gk, float scale, int ldk, int koff) {
;     const int nblk = N >> 6, kb = item / nblk, nb = item - kb * nblk, nq = lane & 15, kr = lane >> 4, k0 = 4 * KL * kb + KL * kr, n0 = 64 * nb + 4 * nq;
;     const GAS f32x4* src = (const GAS f32x4*)(W + (size_t)k0 * N + n0);
;     f32x4 v[KL];
; #pragma unroll
;     for (int i = 0; i < KL; ++i) v[i] = src[(size_t)i * (N >> 2)];
;     if (MODE == 1) {
; #pragma unroll
;         for (int q = 0; q < KL / 4; ++q) { const f32x4 g = *(const GAS f32x4*)(gk + k0 + 4 * q); v[4 * q] *= g.x; v[4 * q + 1] *= g.y; v[4 * q + 2] *= g.z; v[4 * q + 3] *= g.w; } }
;     if (MODE == 2) {
; #pragma unroll
;         for (int i = 0; i < KL; ++i) v[i] *= scale; }
; #pragma unroll
;     for (int c = 0; c < 4; ++c) { const int n = n0 + c, row = il ? ((n >> 4) * 32 + which * 16 + (n & 15)) : n;
;         if (MODE == 2) { GAS v4u* dst = (GAS v4u*)(WT + (size_t)row * ldk + koff + k0);
; #pragma unroll
;             for (int q = 0; q < KL / 16; ++q) { v4u o;
;                 o.x = pg8::pk4_fp8(v[16 * q][c], v[16 * q + 1][c], v[16 * q + 2][c], v[16 * q + 3][c]);     o.y = pg8::pk4_fp8(v[16 * q + 4][c], v[16 * q + 5][c], v[16 * q + 6][c], v[16 * q + 7][c]);
;                 o.z = pg8::pk4_fp8(v[16 * q + 8][c], v[16 * q + 9][c], v[16 * q + 10][c], v[16 * q + 11][c]); o.w = pg8::pk4_fp8(v[16 * q + 12][c], v[16 * q + 13][c], v[16 * q + 14][c], v[16 * q + 15][c]);
;                 dst[q] = o; } }
;         else { GAS v4u* dst = (GAS v4u*)(WT + ((size_t)row * ldk + koff + k0) * 2);
; #pragma unroll
;             for (int q = 0; q < KL / 8; ++q) { v4u o;
;                 if (MODE == 1) { o.x = pg8::pk_f16(v[8 * q][c], v[8 * q + 1][c]); o.y = pg8::pk_f16(v[8 * q + 2][c], v[8 * q + 3][c]); o.z = pg8::pk_f16(v[8 * q + 4][c], v[8 * q + 5][c]); o.w = pg8::pk_f16(v[8 * q + 6][c], v[8 * q + 7][c]); }
;                 else { o.x = pk2(v[8 * q][c], v[8 * q + 1][c]); o.y = pk2(v[8 * q + 2][c], v[8 * q + 3][c]); o.z = pk2(v[8 * q + 4][c], v[8 * q + 5][c]); o.w = pk2(v[8 * q + 6][c], v[8 * q + 7][c]); }
;                 dst[q] = o; } } }
; }
; __device__ __forceinline__ void moe_cvt_tile(const Args& a, int set, int id, int lane) {
.LBB0_932:
	s_andn2_b64 vcc, exec, s[0:1]
	s_cbranch_vccnz .LBB0_929
	s_ashr_i32 s4, s10, 3
	s_and_b32 s0, s10, 7
	s_ashr_i32 s5, s4, 31
	s_or_b32 s12, s0, s8
	s_lshl_b64 s[0:1], s[4:5], 3
	s_add_u32 s0, s66, s0
	s_addc_u32 s1, s67, s1
	v_mov_b64_e32 v[0:1], s[0:1]
	v_mov_b64_e32 v[2:3], s[66:67]
	global_load_dwordx2 v[0:1], v[0:1], off offset:136
	v_mov_b32_e32 v4, 0x700000
	global_load_dwordx2 v[2:3], v[2:3], off offset:192
	s_mulk_i32 s10, 0x1c0
	s_waitcnt vmcnt(0) lgkmcnt(0)
	v_mad_u64_u32 v[0:1], s[0:1], s12, v192, v[0:1]
	v_mad_u64_u32 v[70:71], s[0:1], s12, v4, v[2:3]
	s_mul_hi_i32 s0, s11, 0x92492493
	s_add_i32 s0, s0, s11
	s_lshr_b32 s1, s0, 31
	s_ashr_i32 s0, s0, 5
	s_add_i32 s0, s0, s1
	s_mul_i32 s1, s0, 0xffffffc8
	s_sub_i32 s1, s1, s10
	s_add_i32 s1, s7, s1
	v_lshl_add_u32 v72, s0, 7, v80
	v_lshl_or_b32 v74, s1, 6, v154
	s_movk_i32 s0, 0x3800
	v_mad_i64_i32 v[0:1], s[0:1], v72, s0, v[0:1]
	v_ashrrev_i32_e32 v75, 31, v74
	v_lshl_add_u64 v[8:9], v[74:75], 2, v[0:1]
	s_movk_i32 s0, 0x3000
	v_add_co_u32_e32 v4, vcc, s0, v8
	s_movk_i32 s0, 0x7000
	s_nop 0
	v_addc_co_u32_e32 v5, vcc, 0, v9, vcc
	v_add_co_u32_e32 v10, vcc, s0, v8
	s_mov_b32 s0, 0xe000
	s_nop 0
	v_addc_co_u32_e32 v11, vcc, 0, v9, vcc
	v_add_co_u32_e32 v14, vcc, s97, v8
	global_load_dwordx4 v[0:3], v[8:9], off nt
	s_nop 0
	v_addc_co_u32_e32 v15, vcc, 0, v9, vcc
	v_add_co_u32_e32 v18, vcc, s0, v8
	s_mov_b32 s0, 0x11000
	s_nop 0
	v_addc_co_u32_e32 v19, vcc, 0, v9, vcc
	v_add_co_u32_e32 v22, vcc, s0, v8
	s_mov_b32 s0, 0x15000
	s_nop 0
	v_addc_co_u32_e32 v23, vcc, 0, v9, vcc
	v_add_co_u32_e32 v26, vcc, s0, v8
	s_mov_b32 s0, 0x18000
	s_nop 0
	v_addc_co_u32_e32 v27, vcc, 0, v9, vcc
	v_add_co_u32_e32 v30, vcc, s0, v8
	s_mov_b32 s0, 0x1c000
	s_nop 0
	v_addc_co_u32_e32 v31, vcc, 0, v9, vcc
	v_add_co_u32_e32 v34, vcc, s0, v8
	s_mov_b32 s0, 0x1f000
	s_nop 0
	v_addc_co_u32_e32 v35, vcc, 0, v9, vcc
	v_add_co_u32_e32 v38, vcc, s0, v8
	s_mov_b32 s0, 0x23000
	s_nop 0
	v_addc_co_u32_e32 v39, vcc, 0, v9, vcc
	v_add_co_u32_e32 v42, vcc, s0, v8
	s_mov_b32 s0, 0x26000
	s_nop 0
	v_addc_co_u32_e32 v43, vcc, 0, v9, vcc
	v_add_co_u32_e32 v46, vcc, s0, v8
	s_mov_b32 s0, 0x2a000
	s_nop 0
	v_addc_co_u32_e32 v47, vcc, 0, v9, vcc
	v_add_co_u32_e32 v50, vcc, s0, v8
	s_mov_b32 s0, 0x2d000
	s_nop 0
	v_addc_co_u32_e32 v51, vcc, 0, v9, vcc
	v_add_co_u32_e32 v54, vcc, s0, v8
	s_mov_b32 s0, 0x31000
	s_nop 0
	v_addc_co_u32_e32 v55, vcc, 0, v9, vcc
	v_add_co_u32_e32 v58, vcc, s0, v8
	s_mov_b32 s0, 0x34000
	s_nop 0
	v_addc_co_u32_e32 v59, vcc, 0, v9, vcc
	v_add_co_u32_e32 v62, vcc, s0, v8
	s_mov_b32 s0, 0x38000
	s_nop 0
	v_addc_co_u32_e32 v63, vcc, 0, v9, vcc
	v_add_co_u32_e32 v66, vcc, s0, v8
	s_mov_b32 s0, 0x3b000
	s_nop 0
	v_addc_co_u32_e32 v67, vcc, 0, v9, vcc
	v_add_co_u32_e32 v76, vcc, s0, v8
	s_mov_b32 s0, 0x3f000
	s_nop 0
	v_addc_co_u32_e32 v77, vcc, 0, v9, vcc
	global_load_dwordx4 v[112:115], v[76:77], off offset:2048 nt
	v_add_co_u32_e32 v76, vcc, s0, v8
	s_mov_b32 s0, 0x42000
	s_nop 0
	v_addc_co_u32_e32 v77, vcc, 0, v9, vcc
	global_load_dwordx4 v[116:119], v[76:77], off nt
	v_add_co_u32_e32 v76, vcc, s0, v8
	s_mov_b32 s0, 0x46000
	s_nop 0
	v_addc_co_u32_e32 v77, vcc, 0, v9, vcc
	global_load_dwordx4 v[120:123], v[76:77], off offset:2048 nt
	v_add_co_u32_e32 v76, vcc, s0, v8
	s_mov_b32 s0, 0x49000
	s_nop 0
	v_addc_co_u32_e32 v77, vcc, 0, v9, vcc
	global_load_dwordx4 v[124:127], v[76:77], off nt
	v_add_co_u32_e32 v76, vcc, s0, v8
	s_mov_b32 s0, 0x4d000
	s_nop 0
	v_addc_co_u32_e32 v77, vcc, 0, v9, vcc
	global_load_dwordx4 v[128:131], v[76:77], off offset:2048 nt
	v_add_co_u32_e32 v76, vcc, s0, v8
	s_mov_b32 s0, 0x50000
	s_nop 0
	v_addc_co_u32_e32 v77, vcc, 0, v9, vcc
	global_load_dwordx4 v[132:135], v[76:77], off nt
	v_add_co_u32_e32 v76, vcc, s0, v8
	global_load_dwordx4 v[4:7], v[4:5], off offset:2048 nt
	s_nop 0
	v_addc_co_u32_e32 v77, vcc, 0, v9, vcc
	s_mov_b32 s0, 0x54000
	global_load_dwordx4 v[136:139], v[76:77], off offset:2048 nt
	v_add_co_u32_e32 v76, vcc, s0, v8
	s_mov_b32 s0, 0x57000
	s_nop 0
	v_addc_co_u32_e32 v77, vcc, 0, v9, vcc
	global_load_dwordx4 v[140:143], v[76:77], off nt
	v_add_co_u32_e32 v76, vcc, s0, v8
	global_load_dwordx4 v[14:17], v[14:15], off offset:2048 nt
	s_nop 0
	v_addc_co_u32_e32 v77, vcc, 0, v9, vcc
	global_load_dwordx4 v[18:21], v[18:19], off nt
	s_mov_b32 s0, 0x5b000
	global_load_dwordx4 v[22:25], v[22:23], off offset:2048 nt
	v_ashrrev_i32_e32 v73, 31, v72
	global_load_dwordx4 v[30:33], v[30:31], off offset:2048 nt
	s_waitcnt vmcnt(13)
	v_pk_mul_f32 v[2:3], v[2:3], s[96:97] op_sel_hi:[1,0]
	global_load_dwordx4 v[34:37], v[34:35], off nt
	s_waitcnt vmcnt(13)
	v_pk_mul_f32 v[108:109], v[112:113], s[96:97] op_sel_hi:[1,0]
	global_load_dwordx4 v[38:41], v[38:39], off offset:2048 nt
	s_waitcnt vmcnt(13)
	v_pk_mul_f32 v[112:113], v[116:117], s[96:97] op_sel_hi:[1,0]
	global_load_dwordx4 v[46:49], v[46:47], off offset:2048 nt
	s_waitcnt vmcnt(13)
	v_pk_mul_f32 v[116:117], v[120:121], s[96:97] op_sel_hi:[1,0]
	global_load_dwordx4 v[50:53], v[50:51], off nt
	s_waitcnt vmcnt(11)
	v_pk_mul_f32 v[120:121], v[132:133], s[96:97] op_sel_hi:[1,0]
	global_load_dwordx4 v[54:57], v[54:55], off offset:2048 nt
	s_waitcnt vmcnt(11)
	v_pk_mul_f32 v[78:79], v[4:5], s[96:97] op_sel_hi:[1,0]
	global_load_dwordx4 v[144:147], v[76:77], off offset:2048 nt
	v_add_co_u32_e32 v76, vcc, s0, v8
	s_mov_b32 s0, 0x5e000
	s_nop 0
	v_addc_co_u32_e32 v77, vcc, 0, v9, vcc
	global_load_dwordx4 v[148:151], v[76:77], off nt
	v_add_co_u32_e32 v76, vcc, s0, v8
	global_load_dwordx4 v[10:13], v[10:11], off nt
	s_nop 0
	v_addc_co_u32_e32 v77, vcc, 0, v9, vcc
	global_load_dwordx4 v[26:29], v[26:27], off nt
	s_mov_b32 s0, 0x62000
	global_load_dwordx4 v[42:45], v[42:43], off nt
	s_waitcnt vmcnt(12)
; __device__ __forceinline__ unsigned pk4_fp8(float a, float b, float c, float d) { int w = 0; w = __builtin_amdgcn_cvt_pk_fp8_f32(a, b, w, false); w = __builtin_amdgcn_cvt_pk_fp8_f32(c, d, w, true); return (unsigned)w; }
; #define GAS __attribute__((address_space(1)))
; template <int MODE, int KL>
; __device__ __forceinline__ void p0_cvt_item(const float* W, int K, int N, unsigned char* WT, int il, int which, int item, int lane, const float* gk, float scale, int ldk, int koff) {
;     ...
;     for (int c = 0; c < 4; ++c) { const int n = n0 + c, row = il ? ((n >> 4) * 32 + which * 16 + (n & 15)) : n;
;         if (MODE == 2) { GAS v4u* dst = (GAS v4u*)(WT + (size_t)row * ldk + koff + k0);
; #pragma unroll
;             for (int q = 0; q < KL / 16; ++q) { v4u o;
;                 o.x = pg8::pk4_fp8(v[16 * q][c], v[16 * q + 1][c], v[16 * q + 2][c], v[16 * q + 3][c]);     o.y = pg8::pk4_fp8(v[16 * q + 4][c], v[16 * q + 5][c], v[16 * q + 6][c], v[16 * q + 7][c]);
;                 o.z = pg8::pk4_fp8(v[16 * q + 8][c], v[16 * q + 9][c], v[16 * q + 10][c], v[16 * q + 11][c]); o.w = pg8::pk4_fp8(v[16 * q + 12][c], v[16 * q + 13][c], v[16 * q + 14][c], v[16 * q + 15][c]);
;                 dst[q] = o; } }
	v_pk_mul_f32 v[84:85], v[18:19], s[96:97] op_sel_hi:[1,0]
	global_load_dwordx4 v[58:61], v[58:59], off nt
	s_waitcnt vmcnt(12)
	v_pk_mul_f32 v[88:89], v[22:23], s[96:97] op_sel_hi:[1,0]
	global_load_dwordx4 v[62:65], v[62:63], off offset:2048 nt
	v_pk_mul_f32 v[86:87], v[14:15], s[96:97] op_sel_hi:[1,0]
	global_load_dwordx4 v[158:161], v[76:77], off offset:2048 nt
	v_add_co_u32_e32 v76, vcc, s0, v8
	s_mov_b32 s0, 0x65000
	s_nop 0
	v_addc_co_u32_e32 v77, vcc, 0, v9, vcc
	global_load_dwordx4 v[174:177], v[76:77], off nt
	v_add_co_u32_e32 v76, vcc, s0, v8
	s_mov_b32 s0, 0x69000
	s_nop 0
	v_addc_co_u32_e32 v77, vcc, 0, v9, vcc
	global_load_dwordx4 v[66:69], v[66:67], off nt
	s_waitcnt vmcnt(14)
	v_pk_mul_f32 v[92:93], v[34:35], s[96:97] op_sel_hi:[1,0]
	global_load_dwordx4 v[178:181], v[76:77], off offset:2048 nt
	v_add_co_u32_e32 v76, vcc, s0, v8
	s_mov_b32 s0, 0x6c000
	s_nop 0
	v_addc_co_u32_e32 v77, vcc, 0, v9, vcc
	v_add_co_u32_e32 v8, vcc, s0, v8
	global_load_dwordx4 v[182:185], v[76:77], off nt
	s_nop 0
	v_addc_co_u32_e32 v9, vcc, 0, v9, vcc
	global_load_dwordx4 v[186:189], v[8:9], off offset:2048 nt
	v_pk_mul_f32 v[76:77], v[0:1], s[96:97] op_sel_hi:[1,0]
	v_lshlrev_b32_e32 v0, 1, v74
	v_and_b32_e32 v0, 0xffffffe0, v0
	v_pk_mul_f32 v[8:9], v[6:7], s[96:97] op_sel_hi:[1,0]
	v_lshl_add_u32 v6, s4, 4, v0
	v_or_b32_e32 v6, v6, v155
	v_lshl_add_u64 v[0:1], v[70:71], 0, v[72:73]
	s_mov_b64 s[0:1], 0x25f00000
	v_ashrrev_i32_e32 v7, 31, v6
	v_lshl_add_u64 v[0:1], v[0:1], 0, s[0:1]
	v_lshlrev_b64 v[70:71], 10, v[6:7]
	s_waitcnt vmcnt(16)
	v_pk_mul_f32 v[22:23], v[40:41], s[96:97] op_sel_hi:[1,0]
	v_pk_mul_f32 v[40:41], v[38:39], s[96:97] op_sel_hi:[1,0]
	s_waitcnt vmcnt(14)
	v_pk_mul_f32 v[102:103], v[50:51], s[96:97] op_sel_hi:[1,0]
	v_lshl_add_u64 v[74:75], v[0:1], 0, v[70:71]
	v_mov_b32_e32 v70, v81
	v_mov_b32_e32 v71, v81
	v_mov_b32_e32 v72, v81
	v_mov_b32_e32 v73, v81
	v_cvt_pk_fp8_f32 v70, v76, v78
	v_cvt_pk_fp8_f32 v71, v84, v88
	v_cvt_pk_fp8_f32 v72, v92, v40
	v_pk_mul_f32 v[94:95], v[30:31], s[96:97] op_sel_hi:[1,0]
	v_pk_mul_f32 v[104:105], v[46:47], s[96:97] op_sel_hi:[1,0]
	v_pk_mul_f32 v[38:39], v[118:119], s[96:97] op_sel_hi:[1,0]
	v_pk_mul_f32 v[46:47], v[126:127], s[96:97] op_sel_hi:[1,0]
	v_pk_mul_f32 v[118:119], v[128:129], s[96:97] op_sel_hi:[1,0]
	v_pk_mul_f32 v[50:51], v[134:135], s[96:97] op_sel_hi:[1,0]
	v_pk_mul_f32 v[14:15], v[24:25], s[96:97] op_sel_hi:[1,0]
	v_pk_mul_f32 v[18:19], v[32:33], s[96:97] op_sel_hi:[1,0]
	v_or_b32_e32 v40, 2, v6
	s_waitcnt vmcnt(13)
	v_pk_mul_f32 v[110:111], v[54:55], s[96:97] op_sel_hi:[1,0]
	v_pk_mul_f32 v[30:31], v[56:57], s[96:97] op_sel_hi:[1,0]
	v_cvt_pk_fp8_f32 v73, v102, v110
	s_waitcnt vmcnt(12)
	v_pk_mul_f32 v[126:127], v[144:145], s[96:97] op_sel_hi:[1,0]
	v_pk_mul_f32 v[54:55], v[142:143], s[96:97] op_sel_hi:[1,0]
	v_pk_mul_f32 v[56:57], v[146:147], s[96:97] op_sel_hi:[1,0]
	s_waitcnt vmcnt(11)
	v_pk_mul_f32 v[128:129], v[148:149], s[96:97] op_sel_hi:[1,0]
	s_waitcnt vmcnt(10)
	v_pk_mul_f32 v[82:83], v[10:11], s[96:97] op_sel_hi:[1,0]
	s_nop 0
	v_cvt_pk_fp8_f32 v70, v82, v86 op_sel:[0,0,1]
	v_pk_mul_f32 v[10:11], v[16:17], s[96:97] op_sel_hi:[1,0]
	s_waitcnt vmcnt(9)
	v_pk_mul_f32 v[90:91], v[26:27], s[96:97] op_sel_hi:[1,0]
	v_pk_mul_f32 v[16:17], v[28:29], s[96:97] op_sel_hi:[1,0]
	s_waitcnt vmcnt(8)
	v_pk_mul_f32 v[96:97], v[42:43], s[96:97] op_sel_hi:[1,0]
	v_cvt_pk_fp8_f32 v71, v90, v94 op_sel:[0,0,1]
	s_waitcnt vmcnt(7)
	v_pk_mul_f32 v[98:99], v[58:59], s[96:97] op_sel_hi:[1,0]
	v_cvt_pk_fp8_f32 v72, v96, v104 op_sel:[0,0,1]
	s_waitcnt vmcnt(6)
	v_pk_mul_f32 v[106:107], v[62:63], s[96:97] op_sel_hi:[1,0]
	v_pk_mul_f32 v[42:43], v[114:115], s[96:97] op_sel_hi:[1,0]
	v_cvt_pk_fp8_f32 v73, v98, v106 op_sel:[0,0,1]
	v_pk_mul_f32 v[114:115], v[124:125], s[96:97] op_sel_hi:[1,0]
	v_pk_mul_f32 v[124:125], v[140:141], s[96:97] op_sel_hi:[1,0]
	v_pk_mul_f32 v[24:25], v[44:45], s[96:97] op_sel_hi:[1,0]
	global_store_dwordx4 v[74:75], v[70:73], off
	v_pk_mul_f32 v[26:27], v[48:49], s[96:97] op_sel_hi:[1,0]
	s_waitcnt vmcnt(5)
; __device__ __forceinline__ unsigned pk4_fp8(float a, float b, float c, float d) { int w = 0; w = __builtin_amdgcn_cvt_pk_fp8_f32(a, b, w, false); w = __builtin_amdgcn_cvt_pk_fp8_f32(c, d, w, true); return (unsigned)w; }
; #define GAS __attribute__((address_space(1)))
; template <int MODE, int KL>
; __device__ __forceinline__ void p0_cvt_item(const float* W, int K, int N, unsigned char* WT, int il, int which, int item, int lane, const float* gk, float scale, int ldk, int koff) {
;     ...
;     for (int c = 0; c < 4; ++c) { const int n = n0 + c, row = il ? ((n >> 4) * 32 + which * 16 + (n & 15)) : n;
;         if (MODE == 2) { GAS v4u* dst = (GAS v4u*)(WT + (size_t)row * ldk + koff + k0);
; #pragma unroll
;             for (int q = 0; q < KL / 16; ++q) { v4u o;
;                 o.x = pg8::pk4_fp8(v[16 * q][c], v[16 * q + 1][c], v[16 * q + 2][c], v[16 * q + 3][c]);     o.y = pg8::pk4_fp8(v[16 * q + 4][c], v[16 * q + 5][c], v[16 * q + 6][c], v[16 * q + 7][c]);
;                 o.z = pg8::pk4_fp8(v[16 * q + 8][c], v[16 * q + 9][c], v[16 * q + 10][c], v[16 * q + 11][c]); o.w = pg8::pk4_fp8(v[16 * q + 12][c], v[16 * q + 13][c], v[16 * q + 14][c], v[16 * q + 15][c]);
;                 dst[q] = o; } }
	v_pk_mul_f32 v[132:133], v[174:175], s[96:97] op_sel_hi:[1,0]
	v_mov_b32_e32 v70, v81
	v_mov_b32_e32 v71, v81
	v_mov_b32_e32 v72, v81
	v_mov_b32_e32 v73, v81
	v_cvt_pk_fp8_f32 v71, v114, v118
	s_waitcnt vmcnt(4)
	v_pk_mul_f32 v[100:101], v[66:67], s[96:97] op_sel_hi:[1,0]
	v_cvt_pk_fp8_f32 v72, v124, v126
	s_waitcnt vmcnt(3)
	v_pk_mul_f32 v[134:135], v[178:179], s[96:97] op_sel_hi:[1,0]
	v_cvt_pk_fp8_f32 v70, v100, v108
	v_cvt_pk_fp8_f32 v73, v132, v134
	v_pk_mul_f32 v[28:29], v[52:53], s[96:97] op_sel_hi:[1,0]
	v_pk_mul_f32 v[44:45], v[122:123], s[96:97] op_sel_hi:[1,0]
	v_pk_mul_f32 v[48:49], v[130:131], s[96:97] op_sel_hi:[1,0]
	v_pk_mul_f32 v[52:53], v[138:139], s[96:97] op_sel_hi:[1,0]
	v_pk_mul_f32 v[122:123], v[136:137], s[96:97] op_sel_hi:[1,0]
	v_pk_mul_f32 v[130:131], v[158:159], s[96:97] op_sel_hi:[1,0]
	s_waitcnt vmcnt(2)
	v_pk_mul_f32 v[136:137], v[182:183], s[96:97] op_sel_hi:[1,0]
	v_cvt_pk_fp8_f32 v70, v112, v116 op_sel:[0,0,1]
	s_waitcnt vmcnt(1)
	v_pk_mul_f32 v[138:139], v[186:187], s[96:97] op_sel_hi:[1,0]
	v_cvt_pk_fp8_f32 v71, v120, v122 op_sel:[0,0,1]
	v_cvt_pk_fp8_f32 v72, v128, v130 op_sel:[0,0,1]
	v_cvt_pk_fp8_f32 v73, v136, v138 op_sel:[0,0,1]
	v_pk_mul_f32 v[4:5], v[12:13], s[96:97] op_sel_hi:[1,0]
	v_pk_mul_f32 v[12:13], v[20:21], s[96:97] op_sel_hi:[1,0]
	v_pk_mul_f32 v[20:21], v[36:37], s[96:97] op_sel_hi:[1,0]
	global_store_dwordx4 v[74:75], v[70:73], off offset:16
	v_pk_mul_f32 v[32:33], v[60:61], s[96:97] op_sel_hi:[1,0]
	v_pk_mul_f32 v[34:35], v[64:65], s[96:97] op_sel_hi:[1,0]
	v_or_b32_e32 v70, 1, v6
	v_ashrrev_i32_e32 v71, 31, v70
	v_lshlrev_b64 v[70:71], 10, v[70:71]
	v_lshl_add_u64 v[74:75], v[0:1], 0, v[70:71]
	v_mov_b32_e32 v70, v81
	v_mov_b32_e32 v71, v81
	v_mov_b32_e32 v72, v81
	v_mov_b32_e32 v73, v81
	v_cvt_pk_fp8_f32 v70, v77, v79
	v_cvt_pk_fp8_f32 v71, v85, v89
	v_cvt_pk_fp8_f32 v72, v93, v41
	v_cvt_pk_fp8_f32 v73, v103, v111
	v_cvt_pk_fp8_f32 v70, v83, v87 op_sel:[0,0,1]
	v_cvt_pk_fp8_f32 v71, v91, v95 op_sel:[0,0,1]
	v_cvt_pk_fp8_f32 v72, v97, v105 op_sel:[0,0,1]
	v_cvt_pk_fp8_f32 v73, v99, v107 op_sel:[0,0,1]
	v_ashrrev_i32_e32 v41, 31, v40
	v_lshlrev_b64 v[40:41], 10, v[40:41]
	v_lshl_add_u64 v[40:41], v[0:1], 0, v[40:41]
	global_store_dwordx4 v[74:75], v[70:73], off
	v_pk_mul_f32 v[36:37], v[68:69], s[96:97] op_sel_hi:[1,0]
	v_pk_mul_f32 v[62:63], v[176:177], s[96:97] op_sel_hi:[1,0]
	v_mov_b32_e32 v70, v81
	v_mov_b32_e32 v71, v81
	v_mov_b32_e32 v72, v81
	v_mov_b32_e32 v73, v81
	v_cvt_pk_fp8_f32 v70, v101, v109
	v_cvt_pk_fp8_f32 v71, v115, v119
	v_cvt_pk_fp8_f32 v72, v125, v127
	v_cvt_pk_fp8_f32 v73, v133, v135
	v_cvt_pk_fp8_f32 v70, v113, v117 op_sel:[0,0,1]
	v_cvt_pk_fp8_f32 v71, v121, v123 op_sel:[0,0,1]
	v_cvt_pk_fp8_f32 v72, v129, v131 op_sel:[0,0,1]
	v_cvt_pk_fp8_f32 v73, v137, v139 op_sel:[0,0,1]
	v_pk_mul_f32 v[64:65], v[180:181], s[96:97] op_sel_hi:[1,0]
	v_pk_mul_f32 v[58:59], v[150:151], s[96:97] op_sel_hi:[1,0]
	v_pk_mul_f32 v[60:61], v[160:161], s[96:97] op_sel_hi:[1,0]
	global_store_dwordx4 v[74:75], v[70:73], off offset:16
	v_pk_mul_f32 v[66:67], v[184:185], s[96:97] op_sel_hi:[1,0]
	v_pk_mul_f32 v[68:69], v[188:189], s[96:97] op_sel_hi:[1,0]
	v_mov_b32_e32 v70, v81
	v_mov_b32_e32 v71, v81
	v_mov_b32_e32 v72, v81
	v_mov_b32_e32 v73, v81
	v_cvt_pk_fp8_f32 v70, v2, v8
	v_cvt_pk_fp8_f32 v71, v12, v14
	v_cvt_pk_fp8_f32 v72, v20, v22
	v_cvt_pk_fp8_f32 v73, v28, v30
	v_cvt_pk_fp8_f32 v70, v4, v10 op_sel:[0,0,1]
	v_cvt_pk_fp8_f32 v71, v16, v18 op_sel:[0,0,1]
	v_cvt_pk_fp8_f32 v72, v24, v26 op_sel:[0,0,1]
	v_cvt_pk_fp8_f32 v73, v32, v34 op_sel:[0,0,1]
	v_or_b32_e32 v6, 3, v6
	v_ashrrev_i32_e32 v7, 31, v6
	v_lshlrev_b64 v[6:7], 10, v[6:7]
	global_store_dwordx4 v[40:41], v[70:73], off
	v_lshl_add_u64 v[0:1], v[0:1], 0, v[6:7]
	s_nop 0
	v_mov_b32_e32 v70, v81
	v_mov_b32_e32 v71, v81
	v_mov_b32_e32 v72, v81
	v_mov_b32_e32 v73, v81
	v_cvt_pk_fp8_f32 v70, v36, v42
	v_cvt_pk_fp8_f32 v71, v46, v48
	v_cvt_pk_fp8_f32 v72, v54, v56
	v_cvt_pk_fp8_f32 v73, v62, v64
	v_cvt_pk_fp8_f32 v70, v38, v44 op_sel:[0,0,1]
	v_cvt_pk_fp8_f32 v71, v50, v52 op_sel:[0,0,1]
	v_cvt_pk_fp8_f32 v72, v58, v60 op_sel:[0,0,1]
	v_cvt_pk_fp8_f32 v73, v66, v68 op_sel:[0,0,1]
	global_store_dwordx4 v[40:41], v[70:73], off offset:16
	s_branch .LBB0_929

; #define GAS __attribute__((address_space(1)))
; template <int MODE, int KL>
; __device__ __forceinline__ void p0_cvt_item(const float* W, int K, int N, unsigned char* WT, int il, int which, int item, int lane, const float* gk, float scale, int ldk, int koff) {
;     const int nblk = N >> 6, kb = item / nblk, nb = item - kb * nblk, nq = lane & 15, kr = lane >> 4, k0 = 4 * KL * kb + KL * kr, n0 = 64 * nb + 4 * nq;
;     const GAS f32x4* src = (const GAS f32x4*)(W + (size_t)k0 * N + n0);
;     f32x4 v[KL];
; #pragma unroll
;     for (int i = 0; i < KL; ++i) v[i] = src[(size_t)i * (N >> 2)];
;     if (MODE == 1) {
; #pragma unroll
;         for (int q = 0; q < KL / 4; ++q) { const f32x4 g = *(const GAS f32x4*)(gk + k0 + 4 * q); v[4 * q] *= g.x; v[4 * q + 1] *= g.y; v[4 * q + 2] *= g.z; v[4 * q + 3] *= g.w; } }
;     if (MODE == 2) {
; #pragma unroll
;         for (int i = 0; i < KL; ++i) v[i] *= scale; }
; #pragma unroll
;     for (int c = 0; c < 4; ++c) { const int n = n0 + c, row = il ? ((n >> 4) * 32 + which * 16 + (n & 15)) : n;
;         if (MODE == 2) { GAS v4u* dst = (GAS v4u*)(WT + (size_t)row * ldk + koff + k0);
; #pragma unroll
;             for (int q = 0; q < KL / 16; ++q) { v4u o;
;                 o.x = pg8::pk4_fp8(v[16 * q][c], v[16 * q + 1][c], v[16 * q + 2][c], v[16 * q + 3][c]);     o.y = pg8::pk4_fp8(v[16 * q + 4][c], v[16 * q + 5][c], v[16 * q + 6][c], v[16 * q + 7][c]);
;                 o.z = pg8::pk4_fp8(v[16 * q + 8][c], v[16 * q + 9][c], v[16 * q + 10][c], v[16 * q + 11][c]); o.w = pg8::pk4_fp8(v[16 * q + 12][c], v[16 * q + 13][c], v[16 * q + 14][c], v[16 * q + 15][c]);
;                 dst[q] = o; } }
;         else { GAS v4u* dst = (GAS v4u*)(WT + ((size_t)row * ldk + koff + k0) * 2);
; #pragma unroll
;             for (int q = 0; q < KL / 8; ++q) { v4u o;
;                 if (MODE == 1) { o.x = pg8::pk_f16(v[8 * q][c], v[8 * q + 1][c]); o.y = pg8::pk_f16(v[8 * q + 2][c], v[8 * q + 3][c]); o.z = pg8::pk_f16(v[8 * q + 4][c], v[8 * q + 5][c]); o.w = pg8::pk_f16(v[8 * q + 6][c], v[8 * q + 7][c]); }
;                 else { o.x = pk2(v[8 * q][c], v[8 * q + 1][c]); o.y = pk2(v[8 * q + 2][c], v[8 * q + 3][c]); o.z = pk2(v[8 * q + 4][c], v[8 * q + 5][c]); o.w = pk2(v[8 * q + 6][c], v[8 * q + 7][c]); }
;                 dst[q] = o; } } }
; }
; __device__ __forceinline__ void moe_cvt_tile(const Args& a, int set, int id, int lane) {
.LBB0_1034:
	s_add_i32 s0, s6, s0
	s_mul_hi_i32 s1, s0, 0x92492493
	s_add_i32 s1, s1, s0
	s_lshr_b32 s4, s1, 31
	s_ashr_i32 s1, s1, 8
	s_add_i32 s4, s1, s4
	s_mul_i32 s7, s4, 0xfffffe40
	s_add_i32 s7, s7, s0
	s_cmpk_gt_i32 s0, 0x1bff
	s_mov_b64 s[0:1], -1
	s_cbranch_scc0 .LBB0_1036
	v_mov_b64_e32 v[0:1], s[66:67]
	global_load_dwordx2 v[2:3], v[0:1], off offset:152
	s_add_i32 s5, s4, -8
	global_load_dwordx2 v[0:1], v[0:1], off offset:192
	s_waitcnt vmcnt(0) lgkmcnt(0)
	v_mad_i64_i32 v[2:3], s[0:1], s5, v192, v[2:3]
	v_mad_i64_i32 v[122:123], s[0:1], s5, v193, v[0:1]
	s_ashr_i32 s0, s7, 31
	s_lshr_b32 s0, s0, 28
	s_add_i32 s0, s7, s0
	s_ashr_i32 s0, s0, 4
	v_lshl_add_u32 v124, s0, 7, v80
	s_lshl_b32 s0, s0, 10
	s_lshl_b32 s1, s7, 6
	s_sub_i32 s0, s1, s0
	v_ashrrev_i32_e32 v125, 31, v124
	v_or_b32_e32 v78, s0, v154
	v_lshlrev_b64 v[0:1], 12, v[124:125]
	v_lshl_add_u64 v[0:1], v[2:3], 0, v[0:1]
	v_ashrrev_i32_e32 v79, 31, v78
	v_lshl_add_u64 v[8:9], v[78:79], 2, v[0:1]
	s_movk_i32 s0, 0x2000
	v_add_co_u32_e32 v10, vcc, s0, v8
	s_movk_i32 s0, 0x4000
	s_nop 0
	v_addc_co_u32_e32 v11, vcc, 0, v9, vcc
	v_add_co_u32_e32 v14, vcc, s0, v8
	s_movk_i32 s0, 0x6000
	s_nop 0
	v_addc_co_u32_e32 v15, vcc, 0, v9, vcc
	v_add_co_u32_e32 v18, vcc, s0, v8
	s_mov_b32 s0, 0xc000
	s_nop 0
	v_addc_co_u32_e32 v19, vcc, 0, v9, vcc
	v_add_co_u32_e32 v26, vcc, s33, v8
	global_load_dwordx4 v[0:3], v[8:9], off nt
	s_nop 0
	v_addc_co_u32_e32 v27, vcc, 0, v9, vcc
	v_add_co_u32_e32 v34, vcc, s97, v8
	global_load_dwordx4 v[4:7], v[10:11], off offset:-4096 nt
	s_nop 0
	global_load_dwordx4 v[10:13], v[10:11], off nt
	v_addc_co_u32_e32 v35, vcc, 0, v9, vcc
	v_add_co_u32_e32 v42, vcc, s0, v8
	s_mov_b32 s0, 0xe000
	s_nop 0
	v_addc_co_u32_e32 v43, vcc, 0, v9, vcc
	v_add_co_u32_e32 v50, vcc, s0, v8
	s_mov_b32 s0, 0x10000
	s_nop 0
	v_addc_co_u32_e32 v51, vcc, 0, v9, vcc
	v_add_co_u32_e32 v58, vcc, s0, v8
	s_mov_b32 s0, 0x12000
	s_nop 0
	v_addc_co_u32_e32 v59, vcc, 0, v9, vcc
	v_add_co_u32_e32 v70, vcc, s0, v8
	s_mov_b32 s0, 0x14000
	s_nop 0
	v_addc_co_u32_e32 v71, vcc, 0, v9, vcc
	v_add_co_u32_e32 v82, vcc, s0, v8
	s_mov_b32 s0, 0x16000
	s_nop 0
	v_addc_co_u32_e32 v83, vcc, 0, v9, vcc
	global_load_dwordx4 v[22:25], v[14:15], off offset:-4096 nt
	s_nop 0
	global_load_dwordx4 v[14:17], v[14:15], off nt
	s_nop 0
	global_load_dwordx4 v[30:33], v[18:19], off offset:-4096 nt
	s_nop 0
	global_load_dwordx4 v[18:21], v[18:19], off nt
	s_nop 0
	global_load_dwordx4 v[38:41], v[26:27], off offset:-4096 nt
	s_nop 0
	global_load_dwordx4 v[26:29], v[26:27], off nt
	s_nop 0
	global_load_dwordx4 v[46:49], v[34:35], off offset:-4096 nt
	s_nop 0
	global_load_dwordx4 v[34:37], v[34:35], off nt
	s_nop 0
	global_load_dwordx4 v[54:57], v[42:43], off offset:-4096 nt
	s_nop 0
	global_load_dwordx4 v[42:45], v[42:43], off nt
	s_nop 0
	global_load_dwordx4 v[62:65], v[50:51], off offset:-4096 nt
	s_nop 0
	global_load_dwordx4 v[50:53], v[50:51], off nt
	s_nop 0
	global_load_dwordx4 v[66:69], v[58:59], off offset:-4096 nt
	s_nop 0
	global_load_dwordx4 v[58:61], v[58:59], off nt
	s_nop 0
	global_load_dwordx4 v[74:77], v[70:71], off offset:-4096 nt
	s_nop 0
	global_load_dwordx4 v[70:73], v[70:71], off nt
	v_add_co_u32_e32 v90, vcc, s0, v8
	s_mov_b32 s0, 0x18000
	s_nop 0
	v_addc_co_u32_e32 v91, vcc, 0, v9, vcc
	v_add_co_u32_e32 v98, vcc, s0, v8
	s_mov_b32 s0, 0x1a000
	s_nop 0
	v_addc_co_u32_e32 v99, vcc, 0, v9, vcc
	v_add_co_u32_e32 v106, vcc, s0, v8
	s_mov_b32 s0, 0x1c000
	s_nop 0
	v_addc_co_u32_e32 v107, vcc, 0, v9, vcc
	v_add_co_u32_e32 v114, vcc, s0, v8
	s_mov_b32 s0, 0x1e000
	s_nop 0
	v_addc_co_u32_e32 v115, vcc, 0, v9, vcc
	global_load_dwordx4 v[86:89], v[82:83], off offset:-4096 nt
	s_nop 0
	global_load_dwordx4 v[82:85], v[82:83], off nt
	s_nop 0
	global_load_dwordx4 v[94:97], v[90:91], off offset:-4096 nt
	s_nop 0
	global_load_dwordx4 v[90:93], v[90:91], off nt
	s_nop 0
	global_load_dwordx4 v[102:105], v[98:99], off offset:-4096 nt
	s_nop 0
	global_load_dwordx4 v[98:101], v[98:99], off nt
	s_nop 0
	global_load_dwordx4 v[110:113], v[106:107], off offset:-4096 nt
	s_nop 0
	global_load_dwordx4 v[106:109], v[106:107], off nt
	v_add_co_u32_e32 v126, vcc, s0, v8
	global_load_dwordx4 v[118:121], v[114:115], off offset:-4096 nt
	s_nop 0
	global_load_dwordx4 v[114:117], v[114:115], off nt
	v_addc_co_u32_e32 v127, vcc, 0, v9, vcc
	global_load_dwordx4 v[156:159], v[126:127], off offset:-4096 nt
	global_load_dwordx4 v[174:177], v[126:127], off nt
	s_mov_b32 s0, 0x1f000
	v_add_co_u32_e32 v8, vcc, s0, v8
	s_mov_b64 s[0:1], 0x33f00000
	s_nop 0
	v_addc_co_u32_e32 v9, vcc, 0, v9, vcc
	global_load_dwordx4 v[178:181], v[8:9], off nt
	s_movk_i32 s5, 0xe00
	s_waitcnt vmcnt(31)
	v_pk_mul_f32 v[126:127], v[0:1], s[82:83] op_sel_hi:[1,0]
	v_lshl_add_u64 v[0:1], v[122:123], 0, v[124:125]
	v_lshl_add_u64 v[0:1], v[0:1], 0, s[0:1]
	v_pk_mul_f32 v[2:3], v[2:3], s[82:83] op_sel_hi:[1,0]
	s_waitcnt vmcnt(30)
	v_pk_mul_f32 v[8:9], v[6:7], s[82:83] op_sel_hi:[1,0]
	v_pk_mul_f32 v[6:7], v[4:5], s[82:83] op_sel_hi:[1,0]
	s_waitcnt vmcnt(29)
	v_pk_mul_f32 v[128:129], v[10:11], s[82:83] op_sel_hi:[1,0]
	v_pk_mul_f32 v[4:5], v[12:13], s[82:83] op_sel_hi:[1,0]
	s_waitcnt vmcnt(28)
	v_pk_mul_f32 v[132:133], v[22:23], s[82:83] op_sel_hi:[1,0]
	s_waitcnt vmcnt(27)
	v_pk_mul_f32 v[130:131], v[14:15], s[82:83] op_sel_hi:[1,0]
	s_waitcnt vmcnt(26)
	v_pk_mul_f32 v[134:135], v[30:31], s[82:83] op_sel_hi:[1,0]
	s_waitcnt vmcnt(25)
	v_pk_mul_f32 v[136:137], v[18:19], s[82:83] op_sel_hi:[1,0]
	s_waitcnt vmcnt(24)
	v_pk_mul_f32 v[18:19], v[40:41], s[82:83] op_sel_hi:[1,0]
	v_pk_mul_f32 v[138:139], v[38:39], s[82:83] op_sel_hi:[1,0]
	s_waitcnt vmcnt(23)
; __device__ __forceinline__ unsigned pk4_fp8(float a, float b, float c, float d) { int w = 0; w = __builtin_amdgcn_cvt_pk_fp8_f32(a, b, w, false); w = __builtin_amdgcn_cvt_pk_fp8_f32(c, d, w, true); return (unsigned)w; }
; #define GAS __attribute__((address_space(1)))
; template <int MODE, int KL>
; __device__ __forceinline__ void p0_cvt_item(const float* W, int K, int N, unsigned char* WT, int il, int which, int item, int lane, const float* gk, float scale, int ldk, int koff) {
;     ...
;     for (int c = 0; c < 4; ++c) { const int n = n0 + c, row = il ? ((n >> 4) * 32 + which * 16 + (n & 15)) : n;
;         if (MODE == 2) { GAS v4u* dst = (GAS v4u*)(WT + (size_t)row * ldk + koff + k0);
; #pragma unroll
;             for (int q = 0; q < KL / 16; ++q) { v4u o;
;                 o.x = pg8::pk4_fp8(v[16 * q][c], v[16 * q + 1][c], v[16 * q + 2][c], v[16 * q + 3][c]);     o.y = pg8::pk4_fp8(v[16 * q + 4][c], v[16 * q + 5][c], v[16 * q + 6][c], v[16 * q + 7][c]);
;                 o.z = pg8::pk4_fp8(v[16 * q + 8][c], v[16 * q + 9][c], v[16 * q + 10][c], v[16 * q + 11][c]); o.w = pg8::pk4_fp8(v[16 * q + 12][c], v[16 * q + 13][c], v[16 * q + 14][c], v[16 * q + 15][c]);
;                 dst[q] = o; } }
	v_pk_mul_f32 v[40:41], v[26:27], s[82:83] op_sel_hi:[1,0]
	s_waitcnt vmcnt(22)
	v_pk_mul_f32 v[140:141], v[46:47], s[82:83] op_sel_hi:[1,0]
	s_waitcnt vmcnt(19)
	v_pk_mul_f32 v[148:149], v[42:43], s[82:83] op_sel_hi:[1,0]
	s_waitcnt vmcnt(18)
	v_pk_mul_f32 v[160:161], v[62:63], s[82:83] op_sel_hi:[1,0]
	s_waitcnt vmcnt(14)
	v_pk_mul_f32 v[42:43], v[76:77], s[82:83] op_sel_hi:[1,0]
	s_waitcnt vmcnt(13)
	v_pk_mul_f32 v[38:39], v[72:73], s[82:83] op_sel_hi:[1,0]
	v_pk_mul_f32 v[76:77], v[70:71], s[82:83] op_sel_hi:[1,0]
	v_mov_b32_e32 v70, v81
	v_mov_b32_e32 v71, v81
	v_mov_b32_e32 v72, v81
	v_mov_b32_e32 v73, v81
	v_cvt_pk_fp8_f32 v70, v126, v6
	v_cvt_pk_fp8_f32 v71, v130, v134
	v_cvt_pk_fp8_f32 v72, v40, v140
	v_cvt_pk_fp8_f32 v73, v148, v160
	v_pk_mul_f32 v[142:143], v[34:35], s[82:83] op_sel_hi:[1,0]
	v_pk_mul_f32 v[150:151], v[54:55], s[82:83] op_sel_hi:[1,0]
	v_pk_mul_f32 v[144:145], v[50:51], s[82:83] op_sel_hi:[1,0]
	v_pk_mul_f32 v[152:153], v[66:67], s[82:83] op_sel_hi:[1,0]
	v_cvt_pk_fp8_f32 v70, v128, v132 op_sel:[0,0,1]
	v_cvt_pk_fp8_f32 v71, v136, v138 op_sel:[0,0,1]
	v_cvt_pk_fp8_f32 v72, v142, v150 op_sel:[0,0,1]
	v_cvt_pk_fp8_f32 v73, v144, v152 op_sel:[0,0,1]
	v_pk_mul_f32 v[146:147], v[58:59], s[82:83] op_sel_hi:[1,0]
	v_pk_mul_f32 v[12:13], v[16:17], s[82:83] op_sel_hi:[1,0]
	v_pk_mul_f32 v[16:17], v[20:21], s[82:83] op_sel_hi:[1,0]
	s_waitcnt vmcnt(5)
	v_pk_mul_f32 v[58:59], v[108:109], s[82:83] op_sel_hi:[1,0]
	v_mad_i64_i32 v[108:109], s[0:1], v78, s5, v[0:1]
	v_pk_mul_f32 v[20:21], v[28:29], s[82:83] op_sel_hi:[1,0]
	v_pk_mul_f32 v[28:29], v[44:45], s[82:83] op_sel_hi:[1,0]
	v_pk_mul_f32 v[74:75], v[74:75], s[82:83] op_sel_hi:[1,0]
	v_pk_mul_f32 v[44:45], v[88:89], s[82:83] op_sel_hi:[1,0]
	v_pk_mul_f32 v[46:47], v[84:85], s[82:83] op_sel_hi:[1,0]
	v_pk_mul_f32 v[82:83], v[82:83], s[82:83] op_sel_hi:[1,0]
	v_pk_mul_f32 v[84:85], v[94:95], s[82:83] op_sel_hi:[1,0]
	v_pk_mul_f32 v[50:51], v[92:93], s[82:83] op_sel_hi:[1,0]
	v_pk_mul_f32 v[88:89], v[90:91], s[82:83] op_sel_hi:[1,0]
	v_pk_mul_f32 v[90:91], v[102:103], s[82:83] op_sel_hi:[1,0]
	v_pk_mul_f32 v[54:55], v[100:101], s[82:83] op_sel_hi:[1,0]
	v_pk_mul_f32 v[92:93], v[98:99], s[82:83] op_sel_hi:[1,0]
	v_pk_mul_f32 v[94:95], v[110:111], s[82:83] op_sel_hi:[1,0]
	s_waitcnt vmcnt(3)
	v_pk_mul_f32 v[100:101], v[114:115], s[82:83] op_sel_hi:[1,0]
	s_waitcnt vmcnt(2)
	v_pk_mul_f32 v[102:103], v[156:157], s[82:83] op_sel_hi:[1,0]
	global_store_dwordx4 v[108:109], v[70:73], off
	v_pk_mul_f32 v[14:15], v[32:33], s[82:83] op_sel_hi:[1,0]
	v_pk_mul_f32 v[22:23], v[48:49], s[82:83] op_sel_hi:[1,0]
	v_mov_b32_e32 v70, v81
	v_mov_b32_e32 v71, v81
	v_mov_b32_e32 v72, v81
	v_mov_b32_e32 v73, v81
	v_cvt_pk_fp8_f32 v70, v146, v74
	v_cvt_pk_fp8_f32 v71, v82, v84
	v_cvt_pk_fp8_f32 v72, v92, v94
	v_cvt_pk_fp8_f32 v73, v100, v102
	v_pk_mul_f32 v[32:33], v[52:53], s[82:83] op_sel_hi:[1,0]
	v_pk_mul_f32 v[86:87], v[86:87], s[82:83] op_sel_hi:[1,0]
	v_pk_mul_f32 v[48:49], v[96:97], s[82:83] op_sel_hi:[1,0]
	v_pk_mul_f32 v[52:53], v[104:105], s[82:83] op_sel_hi:[1,0]
	v_pk_mul_f32 v[96:97], v[106:107], s[82:83] op_sel_hi:[1,0]
	v_pk_mul_f32 v[98:99], v[118:119], s[82:83] op_sel_hi:[1,0]
	s_waitcnt vmcnt(2)
	v_pk_mul_f32 v[104:105], v[174:175], s[82:83] op_sel_hi:[1,0]
	s_waitcnt vmcnt(1)
	v_pk_mul_f32 v[106:107], v[178:179], s[82:83] op_sel_hi:[1,0]
	v_cvt_pk_fp8_f32 v70, v76, v86 op_sel:[0,0,1]
	v_cvt_pk_fp8_f32 v71, v88, v90 op_sel:[0,0,1]
	v_cvt_pk_fp8_f32 v72, v96, v98 op_sel:[0,0,1]
	v_cvt_pk_fp8_f32 v73, v104, v106 op_sel:[0,0,1]
	v_or_b32_e32 v6, 1, v78
	v_pk_mul_f32 v[30:31], v[64:65], s[82:83] op_sel_hi:[1,0]
	v_pk_mul_f32 v[10:11], v[24:25], s[82:83] op_sel_hi:[1,0]
	global_store_dwordx4 v[108:109], v[70:73], off offset:16
	v_mad_i64_i32 v[108:109], s[0:1], v6, s5, v[0:1]
	s_nop 0
	v_mov_b32_e32 v70, v81
	v_mov_b32_e32 v71, v81
	v_mov_b32_e32 v72, v81
	v_mov_b32_e32 v73, v81
	v_cvt_pk_fp8_f32 v70, v127, v7
	v_cvt_pk_fp8_f32 v71, v131, v135
	v_cvt_pk_fp8_f32 v72, v41, v141
	v_cvt_pk_fp8_f32 v73, v149, v161
	v_cvt_pk_fp8_f32 v70, v129, v133 op_sel:[0,0,1]
	v_cvt_pk_fp8_f32 v71, v137, v139 op_sel:[0,0,1]
	v_cvt_pk_fp8_f32 v72, v143, v151 op_sel:[0,0,1]
	v_cvt_pk_fp8_f32 v73, v145, v153 op_sel:[0,0,1]
	v_pk_mul_f32 v[24:25], v[36:37], s[82:83] op_sel_hi:[1,0]
	v_pk_mul_f32 v[26:27], v[56:57], s[82:83] op_sel_hi:[1,0]
	v_pk_mul_f32 v[34:35], v[68:69], s[82:83] op_sel_hi:[1,0]
	global_store_dwordx4 v[108:109], v[70:73], off
	v_or_b32_e32 v6, 2, v78
	v_mad_i64_i32 v[6:7], s[0:1], v6, s5, v[0:1]
	v_mov_b32_e32 v70, v81
	v_mov_b32_e32 v71, v81
	v_mov_b32_e32 v72, v81
	v_mov_b32_e32 v73, v81
	v_cvt_pk_fp8_f32 v70, v147, v75
	v_cvt_pk_fp8_f32 v71, v83, v85
	v_cvt_pk_fp8_f32 v72, v93, v95
	v_cvt_pk_fp8_f32 v73, v101, v103
	v_cvt_pk_fp8_f32 v70, v77, v87 op_sel:[0,0,1]
	v_cvt_pk_fp8_f32 v71, v89, v91 op_sel:[0,0,1]
	v_cvt_pk_fp8_f32 v72, v97, v99 op_sel:[0,0,1]
	v_cvt_pk_fp8_f32 v73, v105, v107 op_sel:[0,0,1]
	v_pk_mul_f32 v[36:37], v[60:61], s[82:83] op_sel_hi:[1,0]
	v_pk_mul_f32 v[56:57], v[112:113], s[82:83] op_sel_hi:[1,0]
	v_pk_mul_f32 v[62:63], v[116:117], s[82:83] op_sel_hi:[1,0]
	global_store_dwordx4 v[108:109], v[70:73], off offset:16
	v_pk_mul_f32 v[64:65], v[158:159], s[82:83] op_sel_hi:[1,0]
	v_pk_mul_f32 v[60:61], v[120:121], s[82:83] op_sel_hi:[1,0]
	v_mov_b32_e32 v70, v81
	v_mov_b32_e32 v71, v81
	v_mov_b32_e32 v72, v81
	v_mov_b32_e32 v73, v81
	v_cvt_pk_fp8_f32 v70, v2, v8
	v_cvt_pk_fp8_f32 v71, v12, v14
	v_cvt_pk_fp8_f32 v72, v20, v22
	v_cvt_pk_fp8_f32 v73, v28, v30
	v_cvt_pk_fp8_f32 v70, v4, v10 op_sel:[0,0,1]
	v_cvt_pk_fp8_f32 v71, v16, v18 op_sel:[0,0,1]
	v_cvt_pk_fp8_f32 v72, v24, v26 op_sel:[0,0,1]
	v_cvt_pk_fp8_f32 v73, v32, v34 op_sel:[0,0,1]
	v_pk_mul_f32 v[66:67], v[176:177], s[82:83] op_sel_hi:[1,0]
	v_pk_mul_f32 v[68:69], v[180:181], s[82:83] op_sel_hi:[1,0]
	v_or_b32_e32 v2, 3, v78
	global_store_dwordx4 v[6:7], v[70:73], off
	v_mad_i64_i32 v[0:1], s[0:1], v2, s5, v[0:1]
	s_nop 0
	v_mov_b32_e32 v70, v81
	v_mov_b32_e32 v71, v81
	v_mov_b32_e32 v72, v81
	v_mov_b32_e32 v73, v81
	v_cvt_pk_fp8_f32 v70, v36, v42
	v_cvt_pk_fp8_f32 v71, v46, v48
	v_cvt_pk_fp8_f32 v72, v54, v56
	v_cvt_pk_fp8_f32 v73, v62, v64
	v_cvt_pk_fp8_f32 v70, v38, v44 op_sel:[0,0,1]
	v_cvt_pk_fp8_f32 v71, v50, v52 op_sel:[0,0,1]
	v_cvt_pk_fp8_f32 v72, v58, v60 op_sel:[0,0,1]
	v_cvt_pk_fp8_f32 v73, v66, v68 op_sel:[0,0,1]
	s_mov_b64 s[0:1], 0
	global_store_dwordx4 v[6:7], v[70:73], off offset:16
; #define GAS __attribute__((address_space(1)))
; template <int MODE, int KL>
; __device__ __forceinline__ void p0_cvt_item(const float* W, int K, int N, unsigned char* WT, int il, int which, int item, int lane, const float* gk, float scale, int ldk, int koff) {
;     const int nblk = N >> 6, kb = item / nblk, nb = item - kb * nblk, nq = lane & 15, kr = lane >> 4, k0 = 4 * KL * kb + KL * kr, n0 = 64 * nb + 4 * nq;
;     const GAS f32x4* src = (const GAS f32x4*)(W + (size_t)k0 * N + n0);
;     f32x4 v[KL];
; #pragma unroll
;     for (int i = 0; i < KL; ++i) v[i] = src[(size_t)i * (N >> 2)];
;     if (MODE == 1) {
; #pragma unroll
;         for (int q = 0; q < KL / 4; ++q) { const f32x4 g = *(const GAS f32x4*)(gk + k0 + 4 * q); v[4 * q] *= g.x; v[4 * q + 1] *= g.y; v[4 * q + 2] *= g.z; v[4 * q + 3] *= g.w; } }
;     if (MODE == 2) {
; #pragma unroll
;         for (int i = 0; i < KL; ++i) v[i] *= scale; }
; #pragma unroll
;     for (int c = 0; c < 4; ++c) { const int n = n0 + c, row = il ? ((n >> 4) * 32 + which * 16 + (n & 15)) : n;
;         if (MODE == 2) { GAS v4u* dst = (GAS v4u*)(WT + (size_t)row * ldk + koff + k0);
; #pragma unroll
;             for (int q = 0; q < KL / 16; ++q) { v4u o;
;                 o.x = pg8::pk4_fp8(v[16 * q][c], v[16 * q + 1][c], v[16 * q + 2][c], v[16 * q + 3][c]);     o.y = pg8::pk4_fp8(v[16 * q + 4][c], v[16 * q + 5][c], v[16 * q + 6][c], v[16 * q + 7][c]);
;                 o.z = pg8::pk4_fp8(v[16 * q + 8][c], v[16 * q + 9][c], v[16 * q + 10][c], v[16 * q + 11][c]); o.w = pg8::pk4_fp8(v[16 * q + 12][c], v[16 * q + 13][c], v[16 * q + 14][c], v[16 * q + 15][c]);
;                 dst[q] = o; } }
;         else { GAS v4u* dst = (GAS v4u*)(WT + ((size_t)row * ldk + koff + k0) * 2);
; #pragma unroll
;             for (int q = 0; q < KL / 8; ++q) { v4u o;
;                 if (MODE == 1) { o.x = pg8::pk_f16(v[8 * q][c], v[8 * q + 1][c]); o.y = pg8::pk_f16(v[8 * q + 2][c], v[8 * q + 3][c]); o.z = pg8::pk_f16(v[8 * q + 4][c], v[8 * q + 5][c]); o.w = pg8::pk_f16(v[8 * q + 6][c], v[8 * q + 7][c]); }
;                 else { o.x = pk2(v[8 * q][c], v[8 * q + 1][c]); o.y = pk2(v[8 * q + 2][c], v[8 * q + 3][c]); o.z = pk2(v[8 * q + 4][c], v[8 * q + 5][c]); o.w = pk2(v[8 * q + 6][c], v[8 * q + 7][c]); }
;                 dst[q] = o; } } }
; }
; __device__ __forceinline__ void moe_cvt_tile(const Args& a, int set, int id, int lane) {
.LBB0_1036:
	s_andn2_b64 vcc, exec, s[0:1]
	s_cbranch_vccnz .LBB0_1033
	s_and_b32 s0, s4, 7
	s_ashr_i32 s4, s4, 3
	s_ashr_i32 s5, s4, 31
	s_or_b32 s8, s0, 8
	s_lshl_b64 s[0:1], s[4:5], 3
	s_add_u32 s0, s66, s0
	s_addc_u32 s1, s67, s1
	v_mov_b64_e32 v[0:1], s[0:1]
	global_load_dwordx2 v[0:1], v[0:1], off offset:136
	v_mov_b64_e32 v[2:3], s[66:67]
	global_load_dwordx2 v[2:3], v[2:3], off offset:192
	s_mul_hi_i32 s0, s7, 0x92492493
	s_add_i32 s0, s0, s7
	s_lshr_b32 s1, s0, 31
	s_ashr_i32 s0, s0, 5
	s_add_i32 s0, s0, s1
	s_mul_i32 s1, s0, 0xffffffc8
	s_mul_i32 s62, s8, 0xe00000
	s_add_i32 s1, s1, s7
	v_lshl_add_u32 v72, s0, 7, v80
	v_lshl_or_b32 v74, s1, 6, v154
	s_movk_i32 s0, 0x3800
	v_ashrrev_i32_e32 v75, 31, v74
	v_ashrrev_i32_e32 v73, 31, v72
	s_waitcnt vmcnt(0) lgkmcnt(0)
	v_lshl_add_u64 v[0:1], v[0:1], 0, s[62:63]
	v_mad_i64_i32 v[0:1], s[0:1], v72, s0, v[0:1]
	v_lshl_add_u64 v[8:9], v[74:75], 2, v[0:1]
	s_movk_i32 s0, 0x3000
	v_add_co_u32_e32 v4, vcc, s0, v8
	s_movk_i32 s0, 0x7000
	s_nop 0
	v_addc_co_u32_e32 v5, vcc, 0, v9, vcc
	v_add_co_u32_e32 v10, vcc, s0, v8
	s_mov_b32 s0, 0xe000
	s_nop 0
	v_addc_co_u32_e32 v11, vcc, 0, v9, vcc
	v_add_co_u32_e32 v14, vcc, s97, v8
	s_mul_i32 s62, s8, 0x700000
	s_nop 0
	v_addc_co_u32_e32 v15, vcc, 0, v9, vcc
	v_add_co_u32_e32 v18, vcc, s0, v8
	s_mov_b32 s0, 0x11000
	s_nop 0
	v_addc_co_u32_e32 v19, vcc, 0, v9, vcc
	v_add_co_u32_e32 v22, vcc, s0, v8
	s_mov_b32 s0, 0x15000
	s_nop 0
	v_addc_co_u32_e32 v23, vcc, 0, v9, vcc
	v_add_co_u32_e32 v26, vcc, s0, v8
	s_mov_b32 s0, 0x18000
	s_nop 0
	v_addc_co_u32_e32 v27, vcc, 0, v9, vcc
	v_add_co_u32_e32 v30, vcc, s0, v8
	s_mov_b32 s0, 0x1c000
	s_nop 0
	v_addc_co_u32_e32 v31, vcc, 0, v9, vcc
	v_add_co_u32_e32 v34, vcc, s0, v8
	s_mov_b32 s0, 0x1f000
	s_nop 0
	v_addc_co_u32_e32 v35, vcc, 0, v9, vcc
	v_add_co_u32_e32 v38, vcc, s0, v8
	s_mov_b32 s0, 0x23000
	s_nop 0
	v_addc_co_u32_e32 v39, vcc, 0, v9, vcc
	v_add_co_u32_e32 v42, vcc, s0, v8
	s_mov_b32 s0, 0x26000
	s_nop 0
	v_addc_co_u32_e32 v43, vcc, 0, v9, vcc
	v_add_co_u32_e32 v46, vcc, s0, v8
	s_mov_b32 s0, 0x2a000
	s_nop 0
	v_addc_co_u32_e32 v47, vcc, 0, v9, vcc
	v_add_co_u32_e32 v50, vcc, s0, v8
	s_mov_b32 s0, 0x2d000
	s_nop 0
	v_addc_co_u32_e32 v51, vcc, 0, v9, vcc
	v_add_co_u32_e32 v54, vcc, s0, v8
	s_mov_b32 s0, 0x31000
	s_nop 0
	v_addc_co_u32_e32 v55, vcc, 0, v9, vcc
	global_load_dwordx4 v[58:61], v[54:55], off offset:2048 nt
	v_add_co_u32_e32 v54, vcc, s0, v8
	s_mov_b32 s0, 0x34000
	s_nop 0
	v_addc_co_u32_e32 v55, vcc, 0, v9, vcc
	v_add_co_u32_e32 v62, vcc, s0, v8
	s_mov_b32 s0, 0x38000
	s_nop 0
	v_addc_co_u32_e32 v63, vcc, 0, v9, vcc
	v_add_co_u32_e32 v66, vcc, s0, v8
	s_mov_b32 s0, 0x3b000
	s_nop 0
	v_addc_co_u32_e32 v67, vcc, 0, v9, vcc
	v_add_co_u32_e32 v76, vcc, s0, v8
	s_mov_b32 s0, 0x3f000
	s_nop 0
	v_addc_co_u32_e32 v77, vcc, 0, v9, vcc
	global_load_dwordx4 v[112:115], v[76:77], off offset:2048 nt
	v_add_co_u32_e32 v76, vcc, s0, v8
	s_mov_b32 s0, 0x42000
	s_nop 0
	v_addc_co_u32_e32 v77, vcc, 0, v9, vcc
	global_load_dwordx4 v[66:69], v[66:67], off nt
	v_lshl_add_u64 v[70:71], v[2:3], 0, s[62:63]
	global_load_dwordx4 v[116:119], v[76:77], off nt
	v_add_co_u32_e32 v76, vcc, s0, v8
	s_mov_b32 s0, 0x46000
	s_nop 0
	v_addc_co_u32_e32 v77, vcc, 0, v9, vcc
	global_load_dwordx4 v[120:123], v[76:77], off offset:2048 nt
	v_add_co_u32_e32 v76, vcc, s0, v8
	s_mov_b32 s0, 0x49000
	s_nop 0
	v_addc_co_u32_e32 v77, vcc, 0, v9, vcc
	global_load_dwordx4 v[124:127], v[76:77], off nt
	v_add_co_u32_e32 v76, vcc, s0, v8
	s_mov_b32 s0, 0x4d000
	s_nop 0
	v_addc_co_u32_e32 v77, vcc, 0, v9, vcc
	global_load_dwordx4 v[128:131], v[76:77], off offset:2048 nt
	v_add_co_u32_e32 v76, vcc, s0, v8
	global_load_dwordx4 v[0:3], v[8:9], off nt
	s_nop 0
	v_addc_co_u32_e32 v77, vcc, 0, v9, vcc
	s_mov_b32 s0, 0x50000
	global_load_dwordx4 v[132:135], v[76:77], off nt
	v_add_co_u32_e32 v76, vcc, s0, v8
	global_load_dwordx4 v[4:7], v[4:5], off offset:2048 nt
	s_nop 0
	v_addc_co_u32_e32 v77, vcc, 0, v9, vcc
	s_mov_b32 s0, 0x54000
	global_load_dwordx4 v[136:139], v[76:77], off offset:2048 nt
	v_add_co_u32_e32 v76, vcc, s0, v8
	s_mov_b32 s0, 0x57000
	s_nop 0
	v_addc_co_u32_e32 v77, vcc, 0, v9, vcc
	global_load_dwordx4 v[140:143], v[76:77], off nt
	v_add_co_u32_e32 v76, vcc, s0, v8
	global_load_dwordx4 v[14:17], v[14:15], off offset:2048 nt
	s_nop 0
	v_addc_co_u32_e32 v77, vcc, 0, v9, vcc
	global_load_dwordx4 v[18:21], v[18:19], off nt
	s_mov_b32 s0, 0x5b000
	global_load_dwordx4 v[22:25], v[22:23], off offset:2048 nt
	s_waitcnt vmcnt(14)
	v_pk_mul_f32 v[110:111], v[58:59], s[96:97] op_sel_hi:[1,0]
	global_load_dwordx4 v[30:33], v[30:31], off offset:2048 nt
	s_waitcnt vmcnt(14)
	v_pk_mul_f32 v[108:109], v[112:113], s[96:97] op_sel_hi:[1,0]
	global_load_dwordx4 v[34:37], v[34:35], off nt
	s_waitcnt vmcnt(14)
	v_pk_mul_f32 v[100:101], v[66:67], s[96:97] op_sel_hi:[1,0]
	global_load_dwordx4 v[38:41], v[38:39], off offset:2048 nt
	s_waitcnt vmcnt(14)
	v_pk_mul_f32 v[112:113], v[116:117], s[96:97] op_sel_hi:[1,0]
	global_load_dwordx4 v[46:49], v[46:47], off offset:2048 nt
	s_waitcnt vmcnt(14)
	v_pk_mul_f32 v[116:117], v[120:121], s[96:97] op_sel_hi:[1,0]
	global_load_dwordx4 v[50:53], v[50:51], off nt
	s_waitcnt vmcnt(12)
	v_pk_mul_f32 v[2:3], v[2:3], s[96:97] op_sel_hi:[1,0]
	global_load_dwordx4 v[144:147], v[76:77], off offset:2048 nt
	v_add_co_u32_e32 v76, vcc, s0, v8
	s_mov_b32 s0, 0x5e000
	s_nop 0
	v_addc_co_u32_e32 v77, vcc, 0, v9, vcc
	global_load_dwordx4 v[148:151], v[76:77], off nt
	v_add_co_u32_e32 v76, vcc, s0, v8
	global_load_dwordx4 v[10:13], v[10:11], off nt
	s_nop 0
	v_addc_co_u32_e32 v77, vcc, 0, v9, vcc
	global_load_dwordx4 v[26:29], v[26:27], off nt
	s_mov_b32 s0, 0x62000
	global_load_dwordx4 v[42:45], v[42:43], off nt
	s_waitcnt vmcnt(15)
; __device__ __forceinline__ unsigned pk4_fp8(float a, float b, float c, float d) { int w = 0; w = __builtin_amdgcn_cvt_pk_fp8_f32(a, b, w, false); w = __builtin_amdgcn_cvt_pk_fp8_f32(c, d, w, true); return (unsigned)w; }
; #define GAS __attribute__((address_space(1)))
; template <int MODE, int KL>
; __device__ __forceinline__ void p0_cvt_item(const float* W, int K, int N, unsigned char* WT, int il, int which, int item, int lane, const float* gk, float scale, int ldk, int koff) {
;     ...
;     for (int c = 0; c < 4; ++c) { const int n = n0 + c, row = il ? ((n >> 4) * 32 + which * 16 + (n & 15)) : n;
;         if (MODE == 2) { GAS v4u* dst = (GAS v4u*)(WT + (size_t)row * ldk + koff + k0);
; #pragma unroll
;             for (int q = 0; q < KL / 16; ++q) { v4u o;
;                 o.x = pg8::pk4_fp8(v[16 * q][c], v[16 * q + 1][c], v[16 * q + 2][c], v[16 * q + 3][c]);     o.y = pg8::pk4_fp8(v[16 * q + 4][c], v[16 * q + 5][c], v[16 * q + 6][c], v[16 * q + 7][c]);
;                 o.z = pg8::pk4_fp8(v[16 * q + 8][c], v[16 * q + 9][c], v[16 * q + 10][c], v[16 * q + 11][c]); o.w = pg8::pk4_fp8(v[16 * q + 12][c], v[16 * q + 13][c], v[16 * q + 14][c], v[16 * q + 15][c]);
;                 dst[q] = o; } }
	v_pk_mul_f32 v[78:79], v[4:5], s[96:97] op_sel_hi:[1,0]
	global_load_dwordx4 v[54:57], v[54:55], off nt
	v_pk_mul_f32 v[120:121], v[132:133], s[96:97] op_sel_hi:[1,0]
	global_load_dwordx4 v[62:65], v[62:63], off offset:2048 nt
	s_waitcnt vmcnt(14)
	v_pk_mul_f32 v[86:87], v[14:15], s[96:97] op_sel_hi:[1,0]
	global_load_dwordx4 v[156:159], v[76:77], off offset:2048 nt
	v_add_co_u32_e32 v76, vcc, s0, v8
	s_mov_b32 s0, 0x65000
	s_nop 0
	v_addc_co_u32_e32 v77, vcc, 0, v9, vcc
	global_load_dwordx4 v[174:177], v[76:77], off nt
	v_add_co_u32_e32 v76, vcc, s0, v8
	s_mov_b32 s0, 0x69000
	s_nop 0
	v_addc_co_u32_e32 v77, vcc, 0, v9, vcc
	global_load_dwordx4 v[178:181], v[76:77], off offset:2048 nt
	v_add_co_u32_e32 v76, vcc, s0, v8
	s_mov_b32 s0, 0x6c000
	s_nop 0
	v_addc_co_u32_e32 v77, vcc, 0, v9, vcc
	v_add_co_u32_e32 v8, vcc, s0, v8
	global_load_dwordx4 v[182:185], v[76:77], off nt
	s_nop 0
	v_addc_co_u32_e32 v9, vcc, 0, v9, vcc
	global_load_dwordx4 v[186:189], v[8:9], off offset:2048 nt
	v_pk_mul_f32 v[76:77], v[0:1], s[96:97] op_sel_hi:[1,0]
	v_lshlrev_b32_e32 v0, 1, v74
	v_and_b32_e32 v0, 0xffffffe0, v0
	v_pk_mul_f32 v[8:9], v[6:7], s[96:97] op_sel_hi:[1,0]
	v_lshl_add_u32 v6, s4, 4, v0
	v_or_b32_e32 v6, v6, v155
	v_lshl_add_u64 v[0:1], v[70:71], 0, v[72:73]
	s_mov_b64 s[0:1], 0x25f00000
	v_ashrrev_i32_e32 v7, 31, v6
	v_lshl_add_u64 v[0:1], v[0:1], 0, s[0:1]
	v_lshlrev_b64 v[70:71], 10, v[6:7]
	s_waitcnt vmcnt(18)
	v_pk_mul_f32 v[84:85], v[18:19], s[96:97] op_sel_hi:[1,0]
	s_waitcnt vmcnt(17)
	v_pk_mul_f32 v[88:89], v[22:23], s[96:97] op_sel_hi:[1,0]
	s_waitcnt vmcnt(15)
	v_pk_mul_f32 v[92:93], v[34:35], s[96:97] op_sel_hi:[1,0]
	s_waitcnt vmcnt(14)
	v_pk_mul_f32 v[22:23], v[40:41], s[96:97] op_sel_hi:[1,0]
	v_pk_mul_f32 v[40:41], v[38:39], s[96:97] op_sel_hi:[1,0]
	v_lshl_add_u64 v[74:75], v[0:1], 0, v[70:71]
	v_mov_b32_e32 v70, v81
	v_mov_b32_e32 v71, v81
	v_mov_b32_e32 v72, v81
	v_mov_b32_e32 v73, v81
	s_waitcnt vmcnt(12)
	v_pk_mul_f32 v[102:103], v[50:51], s[96:97] op_sel_hi:[1,0]
	v_cvt_pk_fp8_f32 v70, v76, v78
	v_cvt_pk_fp8_f32 v71, v84, v88
	v_cvt_pk_fp8_f32 v72, v92, v40
	v_cvt_pk_fp8_f32 v73, v102, v110
	v_pk_mul_f32 v[94:95], v[30:31], s[96:97] op_sel_hi:[1,0]
	v_pk_mul_f32 v[104:105], v[46:47], s[96:97] op_sel_hi:[1,0]
	v_pk_mul_f32 v[38:39], v[118:119], s[96:97] op_sel_hi:[1,0]
	v_pk_mul_f32 v[46:47], v[126:127], s[96:97] op_sel_hi:[1,0]
	v_pk_mul_f32 v[118:119], v[128:129], s[96:97] op_sel_hi:[1,0]
	v_pk_mul_f32 v[50:51], v[134:135], s[96:97] op_sel_hi:[1,0]
	v_pk_mul_f32 v[14:15], v[24:25], s[96:97] op_sel_hi:[1,0]
	v_pk_mul_f32 v[30:31], v[60:61], s[96:97] op_sel_hi:[1,0]
	v_pk_mul_f32 v[18:19], v[32:33], s[96:97] op_sel_hi:[1,0]
	v_or_b32_e32 v40, 2, v6
	s_waitcnt vmcnt(11)
	v_pk_mul_f32 v[126:127], v[144:145], s[96:97] op_sel_hi:[1,0]
	s_waitcnt vmcnt(10)
	v_pk_mul_f32 v[128:129], v[148:149], s[96:97] op_sel_hi:[1,0]
	v_pk_mul_f32 v[58:59], v[150:151], s[96:97] op_sel_hi:[1,0]
	s_waitcnt vmcnt(9)
	v_pk_mul_f32 v[82:83], v[10:11], s[96:97] op_sel_hi:[1,0]
	s_nop 0
	v_cvt_pk_fp8_f32 v70, v82, v86 op_sel:[0,0,1]
	v_pk_mul_f32 v[10:11], v[16:17], s[96:97] op_sel_hi:[1,0]
	s_waitcnt vmcnt(8)
	v_pk_mul_f32 v[90:91], v[26:27], s[96:97] op_sel_hi:[1,0]
	v_pk_mul_f32 v[16:17], v[28:29], s[96:97] op_sel_hi:[1,0]
	s_waitcnt vmcnt(7)
	v_pk_mul_f32 v[96:97], v[42:43], s[96:97] op_sel_hi:[1,0]
	v_cvt_pk_fp8_f32 v71, v90, v94 op_sel:[0,0,1]
	s_waitcnt vmcnt(6)
	v_pk_mul_f32 v[98:99], v[54:55], s[96:97] op_sel_hi:[1,0]
	v_cvt_pk_fp8_f32 v72, v96, v104 op_sel:[0,0,1]
	s_waitcnt vmcnt(5)
	v_pk_mul_f32 v[106:107], v[62:63], s[96:97] op_sel_hi:[1,0]
	v_pk_mul_f32 v[42:43], v[114:115], s[96:97] op_sel_hi:[1,0]
	v_cvt_pk_fp8_f32 v73, v98, v106 op_sel:[0,0,1]
	v_pk_mul_f32 v[114:115], v[124:125], s[96:97] op_sel_hi:[1,0]
	v_pk_mul_f32 v[124:125], v[140:141], s[96:97] op_sel_hi:[1,0]
	v_pk_mul_f32 v[24:25], v[44:45], s[96:97] op_sel_hi:[1,0]
	global_store_dwordx4 v[74:75], v[70:73], off
	v_pk_mul_f32 v[26:27], v[48:49], s[96:97] op_sel_hi:[1,0]
	s_waitcnt vmcnt(4)
; __device__ __forceinline__ unsigned pk4_fp8(float a, float b, float c, float d) { int w = 0; w = __builtin_amdgcn_cvt_pk_fp8_f32(a, b, w, false); w = __builtin_amdgcn_cvt_pk_fp8_f32(c, d, w, true); return (unsigned)w; }
; #define GAS __attribute__((address_space(1)))
; template <int MODE, int KL>
; __device__ __forceinline__ void p0_cvt_item(const float* W, int K, int N, unsigned char* WT, int il, int which, int item, int lane, const float* gk, float scale, int ldk, int koff) {
;     ...
;     for (int c = 0; c < 4; ++c) { const int n = n0 + c, row = il ? ((n >> 4) * 32 + which * 16 + (n & 15)) : n;
;         if (MODE == 2) { GAS v4u* dst = (GAS v4u*)(WT + (size_t)row * ldk + koff + k0);
; #pragma unroll
;             for (int q = 0; q < KL / 16; ++q) { v4u o;
;                 o.x = pg8::pk4_fp8(v[16 * q][c], v[16 * q + 1][c], v[16 * q + 2][c], v[16 * q + 3][c]);     o.y = pg8::pk4_fp8(v[16 * q + 4][c], v[16 * q + 5][c], v[16 * q + 6][c], v[16 * q + 7][c]);
;                 o.z = pg8::pk4_fp8(v[16 * q + 8][c], v[16 * q + 9][c], v[16 * q + 10][c], v[16 * q + 11][c]); o.w = pg8::pk4_fp8(v[16 * q + 12][c], v[16 * q + 13][c], v[16 * q + 14][c], v[16 * q + 15][c]);
;                 dst[q] = o; } }
	v_pk_mul_f32 v[132:133], v[174:175], s[96:97] op_sel_hi:[1,0]
	v_mov_b32_e32 v70, v81
	v_mov_b32_e32 v71, v81
	v_mov_b32_e32 v72, v81
	v_mov_b32_e32 v73, v81
	v_cvt_pk_fp8_f32 v70, v100, v108
	s_waitcnt vmcnt(3)
	v_pk_mul_f32 v[134:135], v[178:179], s[96:97] op_sel_hi:[1,0]
	v_cvt_pk_fp8_f32 v71, v114, v118
	v_cvt_pk_fp8_f32 v72, v124, v126
	v_cvt_pk_fp8_f32 v73, v132, v134
	v_pk_mul_f32 v[28:29], v[52:53], s[96:97] op_sel_hi:[1,0]
	v_pk_mul_f32 v[44:45], v[122:123], s[96:97] op_sel_hi:[1,0]
	v_pk_mul_f32 v[48:49], v[130:131], s[96:97] op_sel_hi:[1,0]
	v_pk_mul_f32 v[52:53], v[138:139], s[96:97] op_sel_hi:[1,0]
	v_pk_mul_f32 v[122:123], v[136:137], s[96:97] op_sel_hi:[1,0]
	v_pk_mul_f32 v[130:131], v[156:157], s[96:97] op_sel_hi:[1,0]
	s_waitcnt vmcnt(2)
	v_pk_mul_f32 v[136:137], v[182:183], s[96:97] op_sel_hi:[1,0]
	s_waitcnt vmcnt(1)
	v_pk_mul_f32 v[138:139], v[186:187], s[96:97] op_sel_hi:[1,0]
	v_cvt_pk_fp8_f32 v70, v112, v116 op_sel:[0,0,1]
	v_cvt_pk_fp8_f32 v71, v120, v122 op_sel:[0,0,1]
	v_cvt_pk_fp8_f32 v72, v128, v130 op_sel:[0,0,1]
	v_cvt_pk_fp8_f32 v73, v136, v138 op_sel:[0,0,1]
	v_pk_mul_f32 v[4:5], v[12:13], s[96:97] op_sel_hi:[1,0]
	v_pk_mul_f32 v[12:13], v[20:21], s[96:97] op_sel_hi:[1,0]
	v_pk_mul_f32 v[20:21], v[36:37], s[96:97] op_sel_hi:[1,0]
	global_store_dwordx4 v[74:75], v[70:73], off offset:16
	v_pk_mul_f32 v[32:33], v[56:57], s[96:97] op_sel_hi:[1,0]
	v_pk_mul_f32 v[34:35], v[64:65], s[96:97] op_sel_hi:[1,0]
	v_or_b32_e32 v70, 1, v6
	v_ashrrev_i32_e32 v71, 31, v70
	v_lshlrev_b64 v[70:71], 10, v[70:71]
	v_lshl_add_u64 v[74:75], v[0:1], 0, v[70:71]
	v_mov_b32_e32 v70, v81
	v_mov_b32_e32 v71, v81
	v_mov_b32_e32 v72, v81
	v_mov_b32_e32 v73, v81
	v_cvt_pk_fp8_f32 v70, v77, v79
	v_cvt_pk_fp8_f32 v71, v85, v89
	v_cvt_pk_fp8_f32 v72, v93, v41
	v_cvt_pk_fp8_f32 v73, v103, v111
	v_cvt_pk_fp8_f32 v70, v83, v87 op_sel:[0,0,1]
	v_cvt_pk_fp8_f32 v71, v91, v95 op_sel:[0,0,1]
	v_cvt_pk_fp8_f32 v72, v97, v105 op_sel:[0,0,1]
	v_cvt_pk_fp8_f32 v73, v99, v107 op_sel:[0,0,1]
	v_ashrrev_i32_e32 v41, 31, v40
	v_lshlrev_b64 v[40:41], 10, v[40:41]
	v_lshl_add_u64 v[40:41], v[0:1], 0, v[40:41]
	global_store_dwordx4 v[74:75], v[70:73], off
	v_pk_mul_f32 v[36:37], v[68:69], s[96:97] op_sel_hi:[1,0]
	v_pk_mul_f32 v[54:55], v[142:143], s[96:97] op_sel_hi:[1,0]
	v_mov_b32_e32 v70, v81
	v_mov_b32_e32 v71, v81
	v_mov_b32_e32 v72, v81
	v_mov_b32_e32 v73, v81
	v_cvt_pk_fp8_f32 v70, v101, v109
	v_cvt_pk_fp8_f32 v71, v115, v119
	v_cvt_pk_fp8_f32 v72, v125, v127
	v_cvt_pk_fp8_f32 v73, v133, v135
	v_cvt_pk_fp8_f32 v70, v113, v117 op_sel:[0,0,1]
	v_cvt_pk_fp8_f32 v71, v121, v123 op_sel:[0,0,1]
	v_cvt_pk_fp8_f32 v72, v129, v131 op_sel:[0,0,1]
	v_cvt_pk_fp8_f32 v73, v137, v139 op_sel:[0,0,1]
	v_pk_mul_f32 v[56:57], v[146:147], s[96:97] op_sel_hi:[1,0]
	v_pk_mul_f32 v[62:63], v[176:177], s[96:97] op_sel_hi:[1,0]
	v_pk_mul_f32 v[64:65], v[180:181], s[96:97] op_sel_hi:[1,0]
	global_store_dwordx4 v[74:75], v[70:73], off offset:16
	v_pk_mul_f32 v[60:61], v[158:159], s[96:97] op_sel_hi:[1,0]
	v_pk_mul_f32 v[66:67], v[184:185], s[96:97] op_sel_hi:[1,0]
	v_mov_b32_e32 v70, v81
	v_mov_b32_e32 v71, v81
	v_mov_b32_e32 v72, v81
	v_mov_b32_e32 v73, v81
	v_cvt_pk_fp8_f32 v70, v2, v8
	v_cvt_pk_fp8_f32 v71, v12, v14
	v_cvt_pk_fp8_f32 v72, v20, v22
	v_cvt_pk_fp8_f32 v73, v28, v30
	v_cvt_pk_fp8_f32 v70, v4, v10 op_sel:[0,0,1]
	v_cvt_pk_fp8_f32 v71, v16, v18 op_sel:[0,0,1]
	v_cvt_pk_fp8_f32 v72, v24, v26 op_sel:[0,0,1]
	v_cvt_pk_fp8_f32 v73, v32, v34 op_sel:[0,0,1]
	v_pk_mul_f32 v[68:69], v[188:189], s[96:97] op_sel_hi:[1,0]
	v_or_b32_e32 v6, 3, v6
	v_ashrrev_i32_e32 v7, 31, v6
	global_store_dwordx4 v[40:41], v[70:73], off
	v_lshlrev_b64 v[6:7], 10, v[6:7]
	v_lshl_add_u64 v[0:1], v[0:1], 0, v[6:7]
	v_mov_b32_e32 v70, v81
	v_mov_b32_e32 v71, v81
	v_mov_b32_e32 v72, v81
	v_mov_b32_e32 v73, v81
	v_cvt_pk_fp8_f32 v70, v36, v42
	v_cvt_pk_fp8_f32 v71, v46, v48
	v_cvt_pk_fp8_f32 v72, v54, v56
	v_cvt_pk_fp8_f32 v73, v62, v64
	v_cvt_pk_fp8_f32 v70, v38, v44 op_sel:[0,0,1]
	v_cvt_pk_fp8_f32 v71, v50, v52 op_sel:[0,0,1]
	v_cvt_pk_fp8_f32 v72, v58, v60 op_sel:[0,0,1]
	v_cvt_pk_fp8_f32 v73, v66, v68 op_sel:[0,0,1]
	global_store_dwordx4 v[40:41], v[70:73], off offset:16
	s_branch .LBB0_1033
